# v25: v18 + tables/ph4-gate load hoists, wave-sum xor steps via DPP in ph2/ph13, ph4 and ph6 next-unit L2 prefetch (one dummy load per line)
# baseline (speedup 1.0000x reference)
; __device__ __forceinline__ void ph2_norm1(const Frame& F, const Args& A) {
;     ...
;     for (int row = gw; row < S_; row += 2 * NGW) {
;         const int rowb = row + NGW < S_ ? row + NGW : row;
;         const f32x4* xa = (const f32x4*)(x + (size_t)row * DM) + F.lane; const f32x4* xb = (const f32x4*)(x + (size_t)rowb * DM) + F.lane;
;         f32x4 va[8], vb[8]; float sa = 0.f, sb = 0.f;
; #pragma unroll
;         for (int j = 0; j < 8; ++j) { va[j] = xa[64 * j]; vb[j] = xb[64 * j]; }
; #pragma unroll
;         for (int j = 0; j < 8; ++j) { sa += (va[j].x * va[j].x + va[j].y * va[j].y) + (va[j].z * va[j].z + va[j].w * va[j].w); sb += (vb[j].x * vb[j].x + vb[j].y * vb[j].y) + (vb[j].z * vb[j].z + vb[j].w * vb[j].w); }
;         const float ra = 1.f / sqrtf(wave_sum(sa) * (1.f / DM) + EPS_), rb = 1.f / sqrtf(wave_sum(sb) * (1.f / DM) + EPS_);
;         unsigned long long* oa = (unsigned long long*)(XN + (size_t)row * DM) + F.lane; unsigned long long* ob = (unsigned long long*)(XN + (size_t)rowb * DM) + F.lane;
; #pragma unroll
;         for (int j = 0; j < 8; ++j) { const int col = 4 * F.lane + 256 * j;
;             const f32x4 g = *(const f32x4*)(g1 + col), sh = *(const f32x4*)(MOD + col), sc = *(const f32x4*)(MOD + 2048 + col);
.LBB0_167:
	s_add_i32 s0, s16, s6
	s_cmpk_lt_i32 s0, 0x2000
	s_cselect_b32 s0, s0, s6
	global_load_dwordx4 v[30:33], v[114:115], off offset:-4096
	global_load_dwordx4 v[22:25], v[114:115], off offset:-3072
	global_load_dwordx4 v[26:29], v[114:115], off offset:-2048
	global_load_dwordx4 v[10:13], v[114:115], off offset:1024
	global_load_dwordx4 v[14:17], v[114:115], off
	global_load_dwordx4 v[18:21], v[114:115], off offset:-1024
	global_load_dwordx4 v[2:5], v[114:115], off offset:3072
	global_load_dwordx4 v[6:9], v[114:115], off offset:2048
	global_load_dwordx4 v[136:139], v[74:75], off
	v_lshl_add_u64 v[34:35], s[88:89], 0, v[118:119]
	s_ashr_i32 s1, s0, 31
	v_add_co_u32_e32 v120, vcc, s9, v34
	s_lshl_b64 s[2:3], s[0:1], 13
	s_nop 0
	v_addc_co_u32_e32 v121, vcc, 0, v35, vcc
	v_lshl_add_u64 v[34:35], v[66:67], 0, s[2:3]
	global_load_dwordx4 v[46:49], v[70:71], off
	global_load_dwordx4 v[50:53], v[72:73], off
	v_lshl_add_u64 v[36:37], s[88:89], 0, v[116:117]
	global_load_dwordx4 v[62:65], v[34:35], off offset:2048
	global_load_dwordx4 v[140:143], v[34:35], off
	global_load_dwordx4 v[144:147], v[34:35], off offset:1024
	global_load_dwordx4 v[58:61], v[34:35], off offset:3072
	v_add_co_u32_e32 v122, vcc, s18, v36
	v_mov_b32_e32 v175, 0
	s_nop 0
	v_addc_co_u32_e32 v123, vcc, 0, v37, vcc
	v_add_co_u32_e32 v34, vcc, s17, v34
	s_lshl_b64 s[20:21], s[0:1], 12
	s_nop 0
	v_addc_co_u32_e32 v35, vcc, 0, v35, vcc
	global_load_dwordx4 v[42:45], v[34:35], off offset:1024
	global_load_dwordx4 v[54:57], v[34:35], off
	global_load_dwordx4 v[38:41], v[34:35], off offset:2048
	s_nop 0
	global_load_dwordx4 v[34:37], v[34:35], off offset:3072
	global_load_dwordx4 v[188:191], v[70:71], off offset:1024
	global_load_dwordx4 v[192:195], v[80:81], off
	global_load_dwordx4 v[196:199], v[78:79], off
	global_load_dwordx4 v[200:203], v[70:71], off offset:2048
	global_load_dwordx4 v[204:207], v[84:85], off
	global_load_dwordx4 v[208:211], v[82:83], off
	global_load_dwordx4 v[212:215], v[70:71], off offset:3072
	global_load_dwordx4 v[216:219], v[88:89], off
	global_load_dwordx4 v[220:223], v[86:87], off
	global_load_dwordx4 v[224:227], v[90:91], off
	global_load_dwordx4 v[228:231], v[94:95], off
	global_load_dwordx4 v[232:235], v[92:93], off
	global_load_dwordx4 v[236:239], v[96:97], off
	global_load_dwordx4 v[240:243], v[100:101], off
	global_load_dwordx4 v[244:247], v[98:99], off
	s_lshl_b64 s[0:1], s[0:1], 11
	v_lshl_add_u64 v[124:125], v[76:77], 0, s[0:1]
	v_mov_b32_e32 v176, 0
	v_lshl_add_u64 v[126:127], v[68:69], 0, s[20:21]
	v_mov_b32_e32 v177, 0
	v_mov_b32_e32 v178, 0
	v_mov_b32_e32 v179, 0
	v_mov_b32_e32 v180, 0
	s_add_i32 s6, s6, s8
	v_lshl_add_u64 v[114:115], v[114:115], 0, s[10:11]
	v_lshl_add_u64 v[116:117], v[116:117], 0, s[12:13]
	v_lshl_add_u64 v[118:119], v[118:119], 0, s[14:15]
	s_cmpk_lt_i32 s6, 0x2000
	s_waitcnt vmcnt(33)
	v_mov_b32_e32 v150, v31
	s_waitcnt vmcnt(32)
	v_mov_b32_e32 v151, v23
	s_waitcnt vmcnt(31)
	v_pk_mul_f32 v[152:153], v[28:29], v[28:29]
	v_pk_mul_f32 v[154:155], v[26:27], v[26:27]
	s_waitcnt vmcnt(30)
	v_pk_mul_f32 v[156:157], v[12:13], v[12:13]
	v_pk_mul_f32 v[158:159], v[10:11], v[10:11]
	v_mov_b32_e32 v162, v33
	v_mov_b32_e32 v163, v25
	v_mov_b32_e32 v148, v30
	v_mov_b32_e32 v149, v22
	v_mov_b32_e32 v160, v32
	v_mov_b32_e32 v161, v24
	v_pk_mov_b32 v[170:171], v[154:155], v[152:153] op_sel:[1,0]
	v_mov_b32_e32 v155, v153
	v_pk_mov_b32 v[152:153], v[158:159], v[156:157] op_sel:[1,0]
	v_mov_b32_e32 v159, v157
	v_pk_mul_f32 v[150:151], v[150:151], v[150:151]
	v_pk_mul_f32 v[156:157], v[162:163], v[162:163]
	v_pk_fma_f32 v[148:149], v[148:149], v[148:149], v[150:151]
	v_pk_fma_f32 v[150:151], v[160:161], v[160:161], v[156:157]
	s_waitcnt vmcnt(28)
	v_mul_f32_e32 v128, v19, v19
	v_mul_f32_e32 v164, v21, v21
	s_waitcnt vmcnt(26)
	v_mul_f32_e32 v166, v7, v7
	v_mul_f32_e32 v168, v9, v9
	v_pk_add_f32 v[154:155], v[170:171], v[154:155]
	v_pk_add_f32 v[148:149], v[148:149], v[150:151]
	v_mul_f32_e32 v172, v14, v14
	v_mul_f32_e32 v173, v16, v16
	v_mul_f32_e32 v174, v17, v17
	v_mul_f32_e32 v181, v4, v4
	v_mul_f32_e32 v182, v5, v5
	v_mul_f32_e32 v183, v15, v15
	v_pk_fma_f32 v[162:163], v[18:19], v[18:19], v[128:129] op_sel_hi:[1,1,0]
	v_pk_fma_f32 v[164:165], v[20:21], v[20:21], v[164:165] op_sel_hi:[1,1,0]
	v_pk_fma_f32 v[166:167], v[6:7], v[6:7], v[166:167] op_sel_hi:[1,1,0]
	v_pk_fma_f32 v[168:169], v[8:9], v[8:9], v[168:169] op_sel_hi:[1,1,0]
	v_pk_add_f32 v[154:155], v[154:155], v[154:155] op_sel:[0,1] op_sel_hi:[1,0]
	v_pk_add_f32 v[148:149], v[148:149], v[148:149] op_sel:[0,1] op_sel_hi:[1,0]
	v_mov_b32_e32 v163, v173
	v_mov_b32_e32 v165, v174
	v_mov_b32_e32 v167, v181
	v_mov_b32_e32 v169, v182
	v_mov_b32_e32 v155, v183
	v_mov_b32_e32 v149, v172
	v_pk_add_f32 v[152:153], v[152:153], v[158:159]
	v_pk_add_f32 v[150:151], v[162:163], v[164:165]
	v_pk_add_f32 v[156:157], v[166:167], v[168:169]
	s_waitcnt vmcnt(22)
	v_pk_mul_f32 v[158:159], v[64:65], v[64:65]
	v_pk_mul_f32 v[160:161], v[62:63], v[62:63]
	v_pk_add_f32 v[148:149], v[148:149], v[154:155]
	s_waitcnt vmcnt(21)
	v_mov_b32_e32 v162, v141
	s_waitcnt vmcnt(20)
	v_mov_b32_e32 v163, v145
	v_mov_b32_e32 v166, v143
	v_mov_b32_e32 v167, v147
	v_mov_b32_e32 v154, v140
	v_mov_b32_e32 v155, v144
	v_mov_b32_e32 v164, v142
	v_mov_b32_e32 v165, v146
	v_pk_mov_b32 v[170:171], v[160:161], v[158:159] op_sel:[1,0]
	v_mov_b32_e32 v161, v159
	v_pk_add_f32 v[148:149], v[148:149], v[150:151]
	v_pk_mul_f32 v[150:151], v[162:163], v[162:163]
	v_pk_mul_f32 v[158:159], v[166:167], v[166:167]
	v_mul_f32_e32 v184, v3, v3
	v_mul_f32_e32 v185, v2, v2
	v_pk_add_f32 v[152:153], v[152:153], v[152:153] op_sel:[0,1] op_sel_hi:[1,0]
	v_pk_fma_f32 v[150:151], v[154:155], v[154:155], v[150:151]
	v_pk_fma_f32 v[154:155], v[164:165], v[164:165], v[158:159]
	v_pk_add_f32 v[148:149], v[148:149], v[148:149] op_sel:[0,1] op_sel_hi:[1,0]
	v_mov_b32_e32 v153, v184
	s_waitcnt vmcnt(19)
; __device__ __forceinline__ float wave_sum(float v) {
; #pragma unroll
;     for (int o = 1; o < 64; o <<= 1) v += __shfl_xor(v, o);
;     return v;
; }
; __device__ __forceinline__ void ph2_norm1(const Frame& F, const Args& A) {
;     ...
;         for (int j = 0; j < 8; ++j) { sa += (va[j].x * va[j].x + va[j].y * va[j].y) + (va[j].z * va[j].z + va[j].w * va[j].w); sb += (vb[j].x * vb[j].x + vb[j].y * vb[j].y) + (vb[j].z * vb[j].z + vb[j].w * vb[j].w); }
;         const float ra = 1.f / sqrtf(wave_sum(sa) * (1.f / DM) + EPS_), rb = 1.f / sqrtf(wave_sum(sb) * (1.f / DM) + EPS_);
;         unsigned long long* oa = (unsigned long long*)(XN + (size_t)row * DM) + F.lane; unsigned long long* ob = (unsigned long long*)(XN + (size_t)rowb * DM) + F.lane;
; #pragma unroll
;         for (int j = 0; j < 8; ++j) { const int col = 4 * F.lane + 256 * j;
;             const f32x4 g = *(const f32x4*)(g1 + col), sh = *(const f32x4*)(MOD + col), sc = *(const f32x4*)(MOD + 2048 + col);
;             const f32x4 ha = va[j] * ra * g * (sc + 1.f) + sh, hb = vb[j] * rb * g * (sc + 1.f) + sh;
	v_mul_f32_e32 v128, v59, v59
	v_mul_f32_e32 v168, v61, v61
	v_pk_add_f32 v[158:159], v[170:171], v[160:161]
	v_pk_add_f32 v[150:151], v[150:151], v[154:155]
	v_mov_b32_e32 v149, v185
	v_pk_fma_f32 v[172:173], v[58:59], v[58:59], v[128:129] op_sel_hi:[1,1,0]
	v_pk_fma_f32 v[168:169], v[60:61], v[60:61], v[168:169] op_sel_hi:[1,1,0]
	s_waitcnt vmcnt(17)
	v_mul_f32_e32 v183, v55, v55
	v_mul_f32_e32 v184, v54, v54
	v_pk_add_f32 v[158:159], v[158:159], v[158:159] op_sel:[0,1] op_sel_hi:[1,0]
	v_pk_add_f32 v[148:149], v[148:149], v[152:153]
	v_pk_add_f32 v[150:151], v[150:151], v[150:151] op_sel:[0,1] op_sel_hi:[1,0]
	v_pk_mul_f32 v[162:163], v[44:45], v[44:45]
	v_pk_mul_f32 v[166:167], v[42:43], v[42:43]
	v_mul_f32_e32 v173, v56, v56
	v_mul_f32_e32 v169, v57, v57
	s_waitcnt vmcnt(16)
	v_mul_f32_e32 v128, v39, v39
	v_mov_b32_e32 v159, v183
	v_pk_add_f32 v[148:149], v[148:149], v[156:157]
	v_mov_b32_e32 v151, v184
	v_pk_mov_b32 v[160:161], v[166:167], v[162:163] op_sel:[1,0]
	v_mov_b32_e32 v167, v163
	v_pk_fma_f32 v[162:163], v[38:39], v[38:39], v[128:129] op_sel_hi:[1,1,0]
	v_pk_add_f32 v[154:155], v[172:173], v[168:169]
	v_pk_add_f32 v[150:151], v[150:151], v[158:159]
	v_add_f32_e32 v128, v148, v149
	v_pk_add_f32 v[148:149], v[150:151], v[154:155]
	s_nop 1
	v_mov_b32_dpp v150, v128 quad_perm:[1,0,3,2] row_mask:0xf bank_mask:0xf
	v_mul_f32_e32 v174, v41, v41
	v_pk_add_f32 v[160:161], v[160:161], v[166:167]
	s_waitcnt vmcnt(15)
	v_mul_f32_e32 v181, v36, v36
	v_mul_f32_e32 v182, v37, v37
	v_mul_f32_e32 v186, v35, v35
	v_mul_f32_e32 v187, v34, v34
	v_pk_fma_f32 v[164:165], v[40:41], v[40:41], v[174:175] op_sel_hi:[1,1,0]
	v_pk_add_f32 v[160:161], v[160:161], v[160:161] op_sel:[0,1] op_sel_hi:[1,0]
	v_pk_add_f32 v[148:149], v[148:149], v[148:149] op_sel:[0,1] op_sel_hi:[1,0]
	v_mov_b32_e32 v163, v181
	v_mov_b32_e32 v165, v182
	v_mov_b32_e32 v161, v186
	v_mov_b32_e32 v149, v187
	v_pk_add_f32 v[152:153], v[162:163], v[164:165]
	v_pk_add_f32 v[148:149], v[148:149], v[160:161]
	s_waitcnt lgkmcnt(0)
	v_add_f32_e32 v128, v128, v150
	v_pk_add_f32 v[148:149], v[148:149], v[152:153]
	v_pk_add_f32 v[138:139], v[138:139], 1.0 op_sel_hi:[1,0]
	v_add_f32_e32 v148, v148, v149
	v_mov_b32_dpp v149, v128 quad_perm:[2,3,0,1] row_mask:0xf bank_mask:0xf
	s_nop 1
	v_mov_b32_dpp v150, v148 quad_perm:[1,0,3,2] row_mask:0xf bank_mask:0xf
	v_pk_add_f32 v[136:137], v[136:137], 1.0 op_sel_hi:[1,0]
	s_waitcnt lgkmcnt(0)
	v_add_f32_e32 v128, v128, v149
	s_waitcnt lgkmcnt(0)
	v_add_f32_e32 v148, v148, v150
	ds_bpermute_b32 v149, v130, v128
	s_nop 1
	v_mov_b32_dpp v150, v148 quad_perm:[2,3,0,1] row_mask:0xf bank_mask:0xf
	s_waitcnt lgkmcnt(0)
	v_add_f32_e32 v128, v128, v149
	s_waitcnt lgkmcnt(0)
	v_add_f32_e32 v148, v148, v150
	v_mov_b32_dpp v149, v128 row_ror:8 row_mask:0xf bank_mask:0xf
	ds_bpermute_b32 v150, v130, v148
	s_waitcnt lgkmcnt(0)
	v_add_f32_e32 v128, v128, v149
	s_waitcnt lgkmcnt(0)
	v_add_f32_e32 v148, v148, v150
	ds_bpermute_b32 v149, v132, v128
	s_nop 1
	v_mov_b32_dpp v150, v148 row_ror:8 row_mask:0xf bank_mask:0xf
	s_waitcnt lgkmcnt(0)
	v_add_f32_e32 v128, v128, v149
	s_waitcnt lgkmcnt(0)
	v_add_f32_e32 v148, v148, v150
	ds_bpermute_b32 v149, v133, v128
	ds_bpermute_b32 v150, v132, v148
	s_waitcnt lgkmcnt(0)
	v_add_f32_e32 v128, v128, v149
	s_waitcnt lgkmcnt(0)
	v_add_f32_e32 v148, v148, v150
	v_fmamk_f32 v128, v128, 0x3a000000, v134
	ds_bpermute_b32 v149, v133, v148
	v_mul_f32_e32 v150, 0x4f800000, v128
	v_cmp_gt_f32_e32 vcc, s7, v128
	s_waitcnt lgkmcnt(0)
	v_add_f32_e32 v148, v148, v149
	v_cndmask_b32_e32 v128, v128, v150, vcc
	v_sqrt_f32_e32 v150, v128
	v_fmamk_f32 v148, v148, 0x3a000000, v134
	v_mul_f32_e32 v152, 0x4f800000, v148
	v_cmp_gt_f32_e64 s[0:1], s7, v148
	v_add_u32_e32 v149, -1, v150
	v_add_u32_e32 v151, 1, v150
	v_fma_f32 v153, -v149, v150, v128
	v_fma_f32 v154, -v151, v150, v128
	v_cndmask_b32_e64 v148, v148, v152, s[0:1]
	v_cmp_ge_f32_e64 s[2:3], 0, v153
	s_nop 1
	v_cndmask_b32_e64 v149, v150, v149, s[2:3]
	v_sqrt_f32_e32 v150, v148
	v_cmp_lt_f32_e64 s[2:3], 0, v154
	s_nop 1
	v_cndmask_b32_e64 v149, v149, v151, s[2:3]
	v_mul_f32_e32 v151, 0x37800000, v149
	v_cndmask_b32_e32 v149, v149, v151, vcc
	v_cmp_class_f32_e32 vcc, v128, v135
	v_add_u32_e32 v151, 1, v150
	v_fma_f32 v155, -v151, v150, v148
	v_cndmask_b32_e32 v128, v149, v128, vcc
	v_add_u32_e32 v149, -1, v150
	v_div_scale_f32 v152, s[2:3], v128, v128, 1.0
	v_fma_f32 v154, -v149, v150, v148
	v_cmp_ge_f32_e64 s[2:3], 0, v154
	v_rcp_f32_e32 v156, v152
	v_div_scale_f32 v153, vcc, 1.0, v128, 1.0
	v_cndmask_b32_e64 v149, v150, v149, s[2:3]
	v_cmp_lt_f32_e64 s[2:3], 0, v155
	s_nop 1
	v_cndmask_b32_e64 v149, v149, v151, s[2:3]
	v_mul_f32_e32 v150, 0x37800000, v149
	v_cndmask_b32_e64 v149, v149, v150, s[0:1]
	v_cmp_class_f32_e64 s[0:1], v148, v135
	v_fma_f32 v150, -v152, v156, 1.0
	v_fmac_f32_e32 v156, v150, v156
	v_cndmask_b32_e64 v157, v149, v148, s[0:1]
	v_div_scale_f32 v158, s[0:1], v157, v157, 1.0
	v_mul_f32_e32 v148, v153, v156
	v_rcp_f32_e32 v160, v158
	v_fma_f32 v149, -v152, v148, v153
	v_fmac_f32_e32 v148, v149, v156
	v_fma_f32 v149, -v152, v148, v153
	v_div_fmas_f32 v148, v149, v156, v148
	v_fma_f32 v149, -v158, v160, 1.0
	v_div_scale_f32 v159, s[0:1], 1.0, v157, 1.0
	v_fmac_f32_e32 v160, v149, v160
	v_div_fixup_f32 v128, v148, v128, 1.0
	v_mul_f32_e32 v156, v159, v160
	v_pk_mul_f32 v[32:33], v[32:33], v[128:129] op_sel_hi:[1,0]
	v_pk_mul_f32 v[30:31], v[30:31], v[128:129] op_sel_hi:[1,0]
	v_pk_mul_f32 v[154:155], v[26:27], v[128:129] op_sel_hi:[1,0]
	v_fma_f32 v26, -v158, v156, v159
	v_pk_mul_f32 v[148:149], v[24:25], v[128:129] op_sel_hi:[1,0]
	v_pk_mul_f32 v[150:151], v[22:23], v[128:129] op_sel_hi:[1,0]
; __device__ __forceinline__ unsigned pack_fp8x4(float a, float b, float c, float d) { int w = __builtin_amdgcn_cvt_pk_fp8_f32(a, b, 0, false); w = __builtin_amdgcn_cvt_pk_fp8_f32(c, d, w, true); return (unsigned)w; }
; __device__ __forceinline__ unsigned pk2(float lo, float hi) { const f32x2_t v = {lo, hi}; return __builtin_bit_cast(unsigned, __builtin_convertvector(v, bf16x2_hw)); }
; __device__ __forceinline__ void ph2_norm1(const Frame& F, const Args& A) {
;     ...
;         for (int j = 0; j < 8; ++j) { const int col = 4 * F.lane + 256 * j;
;             const f32x4 g = *(const f32x4*)(g1 + col), sh = *(const f32x4*)(MOD + col), sc = *(const f32x4*)(MOD + 2048 + col);
;             const f32x4 ha = va[j] * ra * g * (sc + 1.f) + sh, hb = vb[j] * rb * g * (sc + 1.f) + sh;
;             oa[64 * j] = (unsigned long long)pk2(ha.x, ha.y) | ((unsigned long long)pk2(ha.z, ha.w) << 32);
;             ob[64 * j] = (unsigned long long)pk2(hb.x, hb.y) | ((unsigned long long)pk2(hb.z, hb.w) << 32);
;             ((unsigned*)((unsigned char*)(A.ws + WS_XN8) + (size_t)row * DM) + F.lane)[64 * j] = pg8::pack_fp8x4(ha.x, ha.y, ha.z, ha.w);
;             ((unsigned*)((unsigned char*)(A.ws + WS_XN8) + (size_t)rowb * DM) + F.lane)[64 * j] = pg8::pack_fp8x4(hb.x, hb.y, hb.z, hb.w); }
	v_pk_mul_f32 v[22:23], v[46:47], v[30:31]
	v_pk_mul_f32 v[24:25], v[48:49], v[32:33]
	v_fmac_f32_e32 v156, v26, v160
	v_pk_fma_f32 v[24:25], v[138:139], v[24:25], v[52:53]
	v_pk_fma_f32 v[22:23], v[136:137], v[22:23], v[50:51]
	v_fma_f32 v26, -v158, v156, v159
	s_mov_b64 vcc, s[0:1]
	v_cvt_pk_fp8_f32 v175, v22, v23
	v_cvt_pk_bf16_f32 v22, v22, v23
	v_cvt_pk_bf16_f32 v23, v24, v25
	v_div_fmas_f32 v26, v26, v160, v156
	global_store_dwordx2 v[120:121], v[22:23], off
	v_div_fixup_f32 v22, v26, v157, 1.0
	v_pk_mul_f32 v[152:153], v[28:29], v[128:129] op_sel_hi:[1,0]
	v_pk_mul_f32 v[26:27], v[142:143], v[22:23] op_sel_hi:[1,0]
	v_pk_mul_f32 v[28:29], v[140:141], v[22:23] op_sel_hi:[1,0]
	v_pk_mul_f32 v[26:27], v[48:49], v[26:27]
	v_pk_mul_f32 v[28:29], v[46:47], v[28:29]
	v_cvt_pk_fp8_f32 v175, v24, v25 op_sel:[0,0,1]
	v_pk_fma_f32 v[24:25], v[138:139], v[26:27], v[52:53]
	v_pk_fma_f32 v[26:27], v[136:137], v[28:29], v[50:51]
	v_pk_mul_f32 v[32:33], v[146:147], v[22:23] op_sel_hi:[1,0]
	v_cvt_pk_fp8_f32 v176, v26, v27
	v_cvt_pk_bf16_f32 v26, v26, v27
	v_cvt_pk_bf16_f32 v27, v24, v25
	global_store_dwordx2 v[126:127], v[26:27], off
	global_store_dword v[122:123], v175, off
	v_cvt_pk_fp8_f32 v176, v24, v25 op_sel:[0,0,1]
	v_pk_mul_f32 v[140:141], v[144:145], v[22:23] op_sel_hi:[1,0]
	v_pk_mul_f32 v[18:19], v[18:19], v[128:129] op_sel_hi:[1,0]
	v_pk_mul_f32 v[20:21], v[20:21], v[128:129] op_sel_hi:[1,0]
	global_store_dword v[124:125], v176, off
	s_waitcnt vmcnt(4)
	v_mov_b64_e32 v[24:25], v[188:189]
	v_mov_b64_e32 v[26:27], v[190:191]
	v_mov_b64_e32 v[28:29], v[192:193]
	v_mov_b64_e32 v[30:31], v[194:195]
	v_mov_b64_e32 v[46:47], v[196:197]
	v_mov_b64_e32 v[48:49], v[198:199]
	v_pk_mul_f32 v[14:15], v[14:15], v[128:129] op_sel_hi:[1,0]
	v_pk_mul_f32 v[16:17], v[16:17], v[128:129] op_sel_hi:[1,0]
	v_pk_mul_f32 v[10:11], v[10:11], v[128:129] op_sel_hi:[1,0]
	v_pk_mul_f32 v[12:13], v[12:13], v[128:129] op_sel_hi:[1,0]
	v_pk_mul_f32 v[6:7], v[6:7], v[128:129] op_sel_hi:[1,0]
	v_pk_mul_f32 v[8:9], v[8:9], v[128:129] op_sel_hi:[1,0]
	v_pk_mul_f32 v[2:3], v[2:3], v[128:129] op_sel_hi:[1,0]
	v_pk_mul_f32 v[4:5], v[4:5], v[128:129] op_sel_hi:[1,0]
	v_pk_mul_f32 v[50:51], v[150:151], v[24:25]
	v_pk_mul_f32 v[52:53], v[148:149], v[26:27]
	v_pk_mul_f32 v[26:27], v[32:33], v[26:27]
	v_pk_add_f32 v[30:31], v[30:31], 1.0 op_sel_hi:[1,0]
	v_pk_add_f32 v[28:29], v[28:29], 1.0 op_sel_hi:[1,0]
	v_pk_mul_f32 v[24:25], v[140:141], v[24:25]
	v_pk_fma_f32 v[32:33], v[52:53], v[30:31], v[48:49]
	v_pk_fma_f32 v[26:27], v[26:27], v[30:31], v[48:49]
	v_pk_fma_f32 v[30:31], v[50:51], v[28:29], v[46:47]
	v_pk_fma_f32 v[24:25], v[24:25], v[28:29], v[46:47]
	v_cvt_pk_fp8_f32 v177, v30, v31
	v_cvt_pk_fp8_f32 v178, v24, v25
	v_cvt_pk_bf16_f32 v28, v30, v31
	v_cvt_pk_bf16_f32 v29, v32, v33
	v_cvt_pk_fp8_f32 v177, v32, v33 op_sel:[0,0,1]
	v_cvt_pk_fp8_f32 v178, v26, v27 op_sel:[0,0,1]
	v_cvt_pk_bf16_f32 v24, v24, v25
	v_cvt_pk_bf16_f32 v25, v26, v27
	global_store_dwordx2 v[120:121], v[28:29], off offset:512
	global_store_dwordx2 v[126:127], v[24:25], off offset:512
	global_store_dword v[122:123], v177, off offset:256
	global_store_dword v[124:125], v178, off offset:256
	v_mov_b64_e32 v[24:25], v[200:201]
	v_mov_b64_e32 v[26:27], v[202:203]
	s_nop 0
	v_mov_b64_e32 v[28:29], v[204:205]
	v_mov_b64_e32 v[30:31], v[206:207]
	v_mov_b64_e32 v[46:47], v[208:209]
	v_mov_b64_e32 v[48:49], v[210:211]
	v_pk_mul_f32 v[32:33], v[64:65], v[22:23] op_sel_hi:[1,0]
	v_pk_mul_f32 v[50:51], v[62:63], v[22:23] op_sel_hi:[1,0]
	v_mov_b32_e32 v23, 0
	v_pk_mul_f32 v[52:53], v[154:155], v[24:25]
	v_pk_mul_f32 v[62:63], v[152:153], v[26:27]
	v_pk_mul_f32 v[26:27], v[32:33], v[26:27]
	v_pk_add_f32 v[30:31], v[30:31], 1.0 op_sel_hi:[1,0]
	v_pk_add_f32 v[28:29], v[28:29], 1.0 op_sel_hi:[1,0]
	v_pk_mul_f32 v[24:25], v[50:51], v[24:25]
	v_pk_fma_f32 v[32:33], v[62:63], v[30:31], v[48:49]
	v_pk_fma_f32 v[26:27], v[26:27], v[30:31], v[48:49]
	v_pk_fma_f32 v[30:31], v[52:53], v[28:29], v[46:47]
	v_pk_fma_f32 v[24:25], v[24:25], v[28:29], v[46:47]
	v_cvt_pk_fp8_f32 v179, v30, v31
	v_cvt_pk_fp8_f32 v180, v24, v25
	v_cvt_pk_bf16_f32 v28, v30, v31
	v_cvt_pk_bf16_f32 v29, v32, v33
	v_cvt_pk_fp8_f32 v179, v32, v33 op_sel:[0,0,1]
	v_cvt_pk_fp8_f32 v180, v26, v27 op_sel:[0,0,1]
	v_cvt_pk_bf16_f32 v24, v24, v25
	v_cvt_pk_bf16_f32 v25, v26, v27
	global_store_dwordx2 v[120:121], v[28:29], off offset:1024
	global_store_dwordx2 v[126:127], v[24:25], off offset:1024
	global_store_dword v[122:123], v179, off offset:512
	global_store_dword v[124:125], v180, off offset:512
	v_mov_b64_e32 v[24:25], v[212:213]
	v_mov_b64_e32 v[26:27], v[214:215]
	s_nop 0
	v_mov_b64_e32 v[28:29], v[216:217]
	v_mov_b64_e32 v[30:31], v[218:219]
	v_mov_b64_e32 v[46:47], v[220:221]
	v_mov_b64_e32 v[48:49], v[222:223]
	v_pk_mul_f32 v[50:51], v[58:59], v[22:23] op_sel_hi:[1,0]
	v_mov_b32_e32 v52, 0
	v_pk_mul_f32 v[32:33], v[60:61], v[22:23] op_sel_hi:[1,0]
	v_pk_mul_f32 v[18:19], v[18:19], v[24:25]
	v_pk_add_f32 v[28:29], v[28:29], 1.0 op_sel_hi:[1,0]
	v_pk_mul_f32 v[24:25], v[50:51], v[24:25]
	v_pk_fma_f32 v[18:19], v[18:19], v[28:29], v[46:47]
	v_pk_fma_f32 v[24:25], v[24:25], v[28:29], v[46:47]
	v_cvt_pk_fp8_f32 v23, v18, v19
	v_cvt_pk_fp8_f32 v52, v24, v25
	v_pk_mul_f32 v[20:21], v[20:21], v[26:27]
	v_pk_add_f32 v[30:31], v[30:31], 1.0 op_sel_hi:[1,0]
	v_pk_mul_f32 v[26:27], v[32:33], v[26:27]
	v_pk_fma_f32 v[20:21], v[20:21], v[30:31], v[48:49]
	v_pk_fma_f32 v[26:27], v[26:27], v[30:31], v[48:49]
	v_cvt_pk_fp8_f32 v23, v20, v21 op_sel:[0,0,1]
	v_cvt_pk_fp8_f32 v52, v26, v27 op_sel:[0,0,1]
	v_cvt_pk_bf16_f32 v28, v18, v19
	v_cvt_pk_bf16_f32 v29, v20, v21
; __device__ __forceinline__ unsigned pack_fp8x4(float a, float b, float c, float d) { int w = __builtin_amdgcn_cvt_pk_fp8_f32(a, b, 0, false); w = __builtin_amdgcn_cvt_pk_fp8_f32(c, d, w, true); return (unsigned)w; }
; __device__ __forceinline__ unsigned pk2(float lo, float hi) { const f32x2_t v = {lo, hi}; return __builtin_bit_cast(unsigned, __builtin_convertvector(v, bf16x2_hw)); }
; __device__ __forceinline__ void ph2_norm1(const Frame& F, const Args& A) {
;     ...
;         for (int j = 0; j < 8; ++j) { const int col = 4 * F.lane + 256 * j;
;             const f32x4 g = *(const f32x4*)(g1 + col), sh = *(const f32x4*)(MOD + col), sc = *(const f32x4*)(MOD + 2048 + col);
;             const f32x4 ha = va[j] * ra * g * (sc + 1.f) + sh, hb = vb[j] * rb * g * (sc + 1.f) + sh;
;             oa[64 * j] = (unsigned long long)pk2(ha.x, ha.y) | ((unsigned long long)pk2(ha.z, ha.w) << 32);
;             ob[64 * j] = (unsigned long long)pk2(hb.x, hb.y) | ((unsigned long long)pk2(hb.z, hb.w) << 32);
;             ((unsigned*)((unsigned char*)(A.ws + WS_XN8) + (size_t)row * DM) + F.lane)[64 * j] = pg8::pack_fp8x4(ha.x, ha.y, ha.z, ha.w);
;             ((unsigned*)((unsigned char*)(A.ws + WS_XN8) + (size_t)rowb * DM) + F.lane)[64 * j] = pg8::pack_fp8x4(hb.x, hb.y, hb.z, hb.w); }
	v_cvt_pk_bf16_f32 v30, v24, v25
	v_cvt_pk_bf16_f32 v31, v26, v27
	global_store_dwordx2 v[120:121], v[28:29], off offset:1536
	global_store_dwordx2 v[126:127], v[30:31], off offset:1536
	global_store_dword v[122:123], v23, off offset:768
	global_store_dword v[124:125], v52, off offset:768
	v_mov_b64_e32 v[18:19], v[224:225]
	v_mov_b64_e32 v[20:21], v[226:227]
	v_mov_b64_e32 v[24:25], v[228:229]
	v_mov_b64_e32 v[26:27], v[230:231]
	s_nop 0
	v_mov_b64_e32 v[28:29], v[232:233]
	v_mov_b64_e32 v[30:31], v[234:235]
	v_mov_b32_e32 v23, 0
	v_pk_mul_f32 v[46:47], v[54:55], v[22:23] op_sel_hi:[1,0]
	v_mov_b32_e32 v48, 0
	v_pk_mul_f32 v[32:33], v[56:57], v[22:23] op_sel_hi:[1,0]
	v_pk_mul_f32 v[14:15], v[14:15], v[18:19]
	v_pk_add_f32 v[24:25], v[24:25], 1.0 op_sel_hi:[1,0]
	v_pk_mul_f32 v[18:19], v[46:47], v[18:19]
	v_pk_fma_f32 v[14:15], v[14:15], v[24:25], v[28:29]
	v_pk_fma_f32 v[18:19], v[18:19], v[24:25], v[28:29]
	v_cvt_pk_fp8_f32 v23, v14, v15
	v_cvt_pk_fp8_f32 v48, v18, v19
	v_pk_mul_f32 v[16:17], v[16:17], v[20:21]
	v_pk_add_f32 v[26:27], v[26:27], 1.0 op_sel_hi:[1,0]
	v_pk_mul_f32 v[20:21], v[32:33], v[20:21]
	v_pk_fma_f32 v[16:17], v[16:17], v[26:27], v[30:31]
	v_pk_fma_f32 v[20:21], v[20:21], v[26:27], v[30:31]
	v_cvt_pk_fp8_f32 v23, v16, v17 op_sel:[0,0,1]
	v_cvt_pk_fp8_f32 v48, v20, v21 op_sel:[0,0,1]
	v_cvt_pk_bf16_f32 v24, v14, v15
	v_cvt_pk_bf16_f32 v25, v16, v17
	v_cvt_pk_bf16_f32 v26, v18, v19
	v_cvt_pk_bf16_f32 v27, v20, v21
	global_store_dwordx2 v[120:121], v[24:25], off offset:2048
	global_store_dwordx2 v[126:127], v[26:27], off offset:2048
	global_store_dword v[122:123], v23, off offset:1024
	global_store_dword v[124:125], v48, off offset:1024
	v_mov_b64_e32 v[14:15], v[236:237]
	v_mov_b64_e32 v[16:17], v[238:239]
	v_mov_b64_e32 v[18:19], v[240:241]
	v_mov_b64_e32 v[20:21], v[242:243]
	s_nop 0
	v_mov_b64_e32 v[24:25], v[244:245]
	v_mov_b64_e32 v[26:27], v[246:247]
	v_mov_b32_e32 v23, 0
	v_pk_mul_f32 v[30:31], v[42:43], v[22:23] op_sel_hi:[1,0]
	v_mov_b32_e32 v32, 0
	v_pk_mul_f32 v[28:29], v[44:45], v[22:23] op_sel_hi:[1,0]
	v_pk_mul_f32 v[10:11], v[10:11], v[14:15]
	v_pk_add_f32 v[18:19], v[18:19], 1.0 op_sel_hi:[1,0]
	v_pk_mul_f32 v[14:15], v[30:31], v[14:15]
	v_pk_fma_f32 v[10:11], v[10:11], v[18:19], v[24:25]
	v_pk_fma_f32 v[14:15], v[14:15], v[18:19], v[24:25]
	v_cvt_pk_fp8_f32 v23, v10, v11
	v_cvt_pk_fp8_f32 v32, v14, v15
	v_pk_mul_f32 v[12:13], v[12:13], v[16:17]
	v_pk_add_f32 v[20:21], v[20:21], 1.0 op_sel_hi:[1,0]
	v_pk_mul_f32 v[16:17], v[28:29], v[16:17]
	v_pk_fma_f32 v[12:13], v[12:13], v[20:21], v[26:27]
	v_pk_fma_f32 v[16:17], v[16:17], v[20:21], v[26:27]
	v_cvt_pk_fp8_f32 v23, v12, v13 op_sel:[0,0,1]
	v_cvt_pk_fp8_f32 v32, v16, v17 op_sel:[0,0,1]
	v_cvt_pk_bf16_f32 v18, v10, v11
	v_cvt_pk_bf16_f32 v19, v12, v13
	v_cvt_pk_bf16_f32 v20, v14, v15
	v_cvt_pk_bf16_f32 v21, v16, v17
	global_store_dwordx2 v[120:121], v[18:19], off offset:2560
	global_store_dwordx2 v[126:127], v[20:21], off offset:2560
	global_store_dword v[122:123], v23, off offset:1280
	global_store_dword v[124:125], v32, off offset:1280
	global_load_dwordx4 v[10:13], v[102:103], off
	global_load_dwordx4 v[14:17], v[106:107], off
	s_nop 0
	global_load_dwordx4 v[18:21], v[104:105], off
	v_mov_b32_e32 v23, 0
	v_pk_mul_f32 v[26:27], v[38:39], v[22:23] op_sel_hi:[1,0]
	v_mov_b32_e32 v28, 0
	v_pk_mul_f32 v[24:25], v[40:41], v[22:23] op_sel_hi:[1,0]
	s_waitcnt vmcnt(2)
	v_pk_mul_f32 v[6:7], v[6:7], v[10:11]
	s_waitcnt vmcnt(1)
	v_pk_add_f32 v[14:15], v[14:15], 1.0 op_sel_hi:[1,0]
	v_pk_mul_f32 v[10:11], v[26:27], v[10:11]
	s_waitcnt vmcnt(0)
	v_pk_fma_f32 v[6:7], v[6:7], v[14:15], v[18:19]
	v_pk_fma_f32 v[10:11], v[10:11], v[14:15], v[18:19]
	v_cvt_pk_fp8_f32 v23, v6, v7
	v_cvt_pk_fp8_f32 v28, v10, v11
	v_pk_mul_f32 v[8:9], v[8:9], v[12:13]
	v_pk_add_f32 v[16:17], v[16:17], 1.0 op_sel_hi:[1,0]
	v_pk_mul_f32 v[12:13], v[24:25], v[12:13]
	v_pk_fma_f32 v[8:9], v[8:9], v[16:17], v[20:21]
	v_pk_fma_f32 v[12:13], v[12:13], v[16:17], v[20:21]
	v_cvt_pk_fp8_f32 v23, v8, v9 op_sel:[0,0,1]
	v_cvt_pk_fp8_f32 v28, v12, v13 op_sel:[0,0,1]
	v_cvt_pk_bf16_f32 v14, v6, v7
	v_cvt_pk_bf16_f32 v15, v8, v9
	v_cvt_pk_bf16_f32 v16, v10, v11
	v_cvt_pk_bf16_f32 v17, v12, v13
	global_store_dwordx2 v[120:121], v[14:15], off offset:3072
	global_store_dwordx2 v[126:127], v[16:17], off offset:3072
	global_store_dword v[122:123], v23, off offset:1536
	global_store_dword v[124:125], v28, off offset:1536
	global_load_dwordx4 v[6:9], v[108:109], off
	global_load_dwordx4 v[10:13], v[112:113], off
	s_nop 0
	global_load_dwordx4 v[14:17], v[110:111], off
	v_mov_b32_e32 v23, 0
	v_pk_mul_f32 v[20:21], v[34:35], v[22:23] op_sel_hi:[1,0]
	v_mov_b32_e32 v24, 0
	v_pk_mul_f32 v[18:19], v[36:37], v[22:23] op_sel_hi:[1,0]
	s_waitcnt vmcnt(2)
	v_pk_mul_f32 v[2:3], v[2:3], v[6:7]
	s_waitcnt vmcnt(1)
	v_pk_add_f32 v[10:11], v[10:11], 1.0 op_sel_hi:[1,0]
	v_pk_mul_f32 v[6:7], v[20:21], v[6:7]
	s_waitcnt vmcnt(0)
	v_pk_fma_f32 v[2:3], v[2:3], v[10:11], v[14:15]
	v_pk_fma_f32 v[6:7], v[6:7], v[10:11], v[14:15]
	v_cvt_pk_fp8_f32 v23, v2, v3
	v_cvt_pk_fp8_f32 v24, v6, v7
	v_pk_mul_f32 v[4:5], v[4:5], v[8:9]
	v_pk_add_f32 v[12:13], v[12:13], 1.0 op_sel_hi:[1,0]
	v_pk_mul_f32 v[8:9], v[18:19], v[8:9]
	v_pk_fma_f32 v[4:5], v[4:5], v[12:13], v[16:17]
	v_pk_fma_f32 v[8:9], v[8:9], v[12:13], v[16:17]
	v_cvt_pk_fp8_f32 v23, v4, v5 op_sel:[0,0,1]
	v_cvt_pk_bf16_f32 v10, v2, v3
	v_cvt_pk_bf16_f32 v11, v4, v5
	v_cvt_pk_fp8_f32 v24, v8, v9 op_sel:[0,0,1]
	v_cvt_pk_bf16_f32 v2, v6, v7
	v_cvt_pk_bf16_f32 v3, v8, v9
	global_store_dwordx2 v[120:121], v[10:11], off offset:3584
	global_store_dwordx2 v[126:127], v[2:3], off offset:3584
	global_store_dword v[122:123], v23, off offset:1792
	global_store_dword v[124:125], v24, off offset:1792
	s_cbranch_scc1 .LBB0_167

; __device__ __forceinline__ void ph4_unit(const Frame& F, const Args& A, int c, int h) {
;     ...
;         { float s0[16], s1[8], s2[4], s3[2];
;           const bool b0 = lane & 1, b1 = lane & 2, b2 = lane & 4, b3 = lane & 8;
; #pragma unroll
;           for (int i = 0; i < 16; ++i) { const float x0 = bflo(qw[i]), x1 = bfhi(qw[i]); s0[i] = x0 * x0 + x1 * x1; }
; #pragma unroll
;           for (int k = 0; k < 8; ++k) s1[k] = (b0 ? s0[2 * k + 1] : s0[2 * k]) + __shfl_xor(b0 ? s0[2 * k] : s0[2 * k + 1], 1);
; #pragma unroll
;           for (int k = 0; k < 4; ++k) s2[k] = (b1 ? s1[2 * k + 1] : s1[2 * k]) + __shfl_xor(b1 ? s1[2 * k] : s1[2 * k + 1], 2);
; #pragma unroll
;           for (int k = 0; k < 2; ++k) s3[k] = (b2 ? s2[2 * k + 1] : s2[2 * k]) + __shfl_xor(b2 ? s2[2 * k] : s2[2 * k + 1], 4);
;           float s4 = (b3 ? s3[1] : s3[0]) + __shfl_xor(b3 ? s3[0] : s3[1], 8);
;           s4 += __shfl_xor(s4, 16); s4 += __shfl_xor(s4, 32);
;           rl = __builtin_amdgcn_rsqf(s4 * (1.f / 128.f) + EPS_); }
.LBB0_333:
	s_or_b64 exec, exec, s[50:51]
	v_lshlrev_b32_e32 v82, 16, v63
	v_and_b32_e32 v83, 0xffff0000, v63
	v_and_b32_e32 v63, 64, v97
	v_lshlrev_b32_e32 v72, 16, v66
	v_and_b32_e32 v73, 0xffff0000, v66
	v_lshlrev_b32_e32 v70, 16, v67
	v_and_b32_e32 v71, 0xffff0000, v67
	v_lshlrev_b32_e32 v66, 16, v74
	v_and_b32_e32 v67, 0xffff0000, v74
	v_xor_b32_e32 v18, 1, v97
	v_add_u32_e32 v74, 64, v63
	v_cmp_lt_i32_e32 vcc, v18, v74
	v_lshlrev_b32_e32 v6, 16, v105
	v_and_b32_e32 v7, 0xffff0000, v105
	v_cndmask_b32_e32 v18, v97, v18, vcc
	v_lshlrev_b32_e32 v105, 2, v18
	v_xor_b32_e32 v18, 2, v97
	v_cmp_lt_i32_e32 vcc, v18, v74
	v_lshlrev_b32_e32 v8, 16, v104
	v_and_b32_e32 v9, 0xffff0000, v104
	v_cndmask_b32_e32 v18, v97, v18, vcc
	v_lshlrev_b32_e32 v104, 2, v18
	v_xor_b32_e32 v18, 4, v97
	v_or_b32_e32 v2, s33, v20
	v_lshlrev_b32_e32 v78, 16, v64
	v_and_b32_e32 v79, 0xffff0000, v64
	v_cmp_lt_i32_e32 vcc, v18, v74
	v_lshlrev_b32_e32 v108, 2, v2
	v_lshlrev_b32_e32 v16, 16, v80
	v_and_b32_e32 v17, 0xffff0000, v80
	v_lshlrev_b32_e32 v14, 16, v81
	v_and_b32_e32 v15, 0xffff0000, v81
	v_lshlrev_b32_e32 v4, 16, v106
	v_and_b32_e32 v5, 0xffff0000, v106
	v_lshlrev_b32_e32 v2, 16, v107
	v_and_b32_e32 v3, 0xffff0000, v107
	v_cndmask_b32_e32 v18, v97, v18, vcc
	v_pk_mul_f32 v[80:81], v[82:83], v[82:83]
	v_pk_mul_f32 v[106:107], v[78:79], v[78:79]
	v_lshlrev_b32_e32 v10, 16, v103
	v_and_b32_e32 v11, 0xffff0000, v103
	v_lshlrev_b32_e32 v103, 2, v18
	v_xor_b32_e32 v18, 8, v97
	v_add_f32_e32 v109, v80, v81
	v_add_f32_e32 v106, v106, v107
	v_cmp_lt_i32_e32 vcc, v18, v74
	v_cndmask_b32_e64 v107, v106, v109, s[20:21]
	v_cndmask_b32_e64 v106, v109, v106, s[20:21]
	v_cndmask_b32_e32 v18, v97, v18, vcc
	s_nop 1
	v_mov_b32_dpp v106, v106 quad_perm:[1,0,3,2] row_mask:0xf bank_mask:0xf
	v_lshlrev_b32_e32 v12, 16, v102
	v_and_b32_e32 v13, 0xffff0000, v102
	v_lshlrev_b32_e32 v102, 2, v18
	v_xor_b32_e32 v18, 16, v97
	v_cmp_lt_i32_e32 vcc, v18, v74
	v_readlane_b32 s0, v254, 16
	v_lshlrev_b32_e32 v76, 16, v65
	v_cndmask_b32_e32 v18, v97, v18, vcc
	v_and_b32_e32 v77, 0xffff0000, v65
	v_lshlrev_b32_e32 v63, 2, v18
	v_xor_b32_e32 v18, 32, v97
	v_readlane_b32 s8, v254, 24
	v_readlane_b32 s9, v254, 25
	v_readlane_b32 s10, v254, 26
	v_readlane_b32 s11, v254, 27
	v_lshlrev_b32_e32 v64, 16, v75
	v_and_b32_e32 v65, 0xffff0000, v75
	v_cmp_lt_i32_e32 vcc, v18, v74
	global_load_dwordx2 v[74:75], v108, s[8:9]
	v_lshlrev_b32_e32 v68, 16, v69
	global_load_dwordx2 v[80:81], v108, s[10:11]
	v_readlane_b32 s98, v254, 49
	s_add_i32 s98, s58, s98
	s_and_b32 s99, s98, 7
	s_ashr_i32 s98, s98, 3
	s_lshl_b32 s98, s98, 6
	v_lshrrev_b32_e32 v124, 3, v0
	v_add_u32_e32 v124, s98, v124
	v_mul_u32_u24_e32 v124, 0x5800, v124
	v_and_b32_e32 v126, 1, v0
	v_bfe_u32 v125, v0, 1, 2
	v_min_u32_e32 v127, 1, v125
	v_lshrrev_b32_e32 v128, 1, v125
	v_add_u32_e32 v128, v128, v125
	v_lshlrev_b32_e32 v128, 11, v128
	v_mul_u32_u24_e32 v129, 0x380, v127
	v_sub_u32_e32 v129, 0x400, v129
	v_mad_u32_u24 v128, v126, v129, v128
	v_lshlrev_b32_e32 v129, 7, v127
	v_add_u32_e32 v129, 0x80, v129
	v_mul_u32_u24_e32 v129, s99, v129
	v_add3_u32 v124, v124, v128, v129
	global_load_dword v130, v124, s[28:29]
	s_mul_i32 s99, s98, 0x60
	s_add_i32 s99, s99, 0x600000
	v_and_b32_e32 v125, 63, v0
	v_lshl_add_u32 v125, v125, 7, s99
	global_load_dword v130, v125, s[88:89]
	s_waitcnt lgkmcnt(0)
	v_add_f32_e32 v108, v107, v106
	v_pk_mul_f32 v[106:107], v[76:77], v[76:77]
	v_and_b32_e32 v69, 0xffff0000, v69
	v_add_f32_e32 v109, v106, v107
	v_pk_mul_f32 v[106:107], v[72:73], v[72:73]
	v_readlane_b32 s1, v254, 17
	v_add_f32_e32 v106, v106, v107
	v_cndmask_b32_e64 v107, v106, v109, s[20:21]
	v_cndmask_b32_e64 v106, v109, v106, s[20:21]
	s_nop 1
	v_mov_b32_dpp v106, v106 quad_perm:[1,0,3,2] row_mask:0xf bank_mask:0xf
	s_lshl_b64 s[0:1], s[96:97], 11
	s_add_u32 s50, s37, s0
	s_addc_u32 s51, s52, s1
	s_lshl_b32 s30, s33, 1
	s_waitcnt lgkmcnt(0)
	v_add_f32_e32 v106, v107, v106
	v_cndmask_b32_e64 v107, v106, v108, s[24:25]
	v_cndmask_b32_e64 v106, v108, v106, s[24:25]
	s_nop 1
	v_mov_b32_dpp v106, v106 quad_perm:[2,3,0,1] row_mask:0xf bank_mask:0xf
	s_add_u32 s50, s50, s30
	s_addc_u32 s51, s51, 0
	s_add_u32 s0, s53, s0
	s_addc_u32 s1, s54, s1
	s_waitcnt lgkmcnt(0)
	v_add_f32_e32 v108, v107, v106
	v_pk_mul_f32 v[106:107], v[70:71], v[70:71]
	s_add_u32 s84, s0, s30
	v_add_f32_e32 v109, v106, v107
	v_pk_mul_f32 v[106:107], v[68:69], v[68:69]
	s_addc_u32 s85, s1, 0
	v_add_f32_e32 v106, v106, v107
	v_cndmask_b32_e64 v107, v106, v109, s[20:21]
	v_cndmask_b32_e64 v106, v109, v106, s[20:21]
	s_nop 1
	v_mov_b32_dpp v106, v106 quad_perm:[1,0,3,2] row_mask:0xf bank_mask:0xf
	s_lshl_b64 s[0:1], s[80:81], 11
	s_add_u32 s33, s37, s0
	s_addc_u32 s59, s52, s1
	s_add_u32 s80, s33, s30
	s_waitcnt lgkmcnt(0)
	v_add_f32_e32 v109, v107, v106
	v_pk_mul_f32 v[106:107], v[66:67], v[66:67]
	s_addc_u32 s81, s59, 0
	v_add_f32_e32 v110, v106, v107
	v_pk_mul_f32 v[106:107], v[64:65], v[64:65]
	s_add_u32 s0, s53, s0
	v_add_f32_e32 v106, v106, v107
	v_cndmask_b32_e64 v107, v106, v110, s[20:21]
	v_cndmask_b32_e64 v106, v110, v106, s[20:21]
	s_nop 1
	v_mov_b32_dpp v106, v106 quad_perm:[1,0,3,2] row_mask:0xf bank_mask:0xf
	s_addc_u32 s1, s54, s1
	s_add_u32 s86, s0, s30
	s_addc_u32 s87, s1, 0
	s_lshl_b64 s[0:1], s[76:77], 11
	s_waitcnt lgkmcnt(0)
	v_add_f32_e32 v106, v107, v106
	v_cndmask_b32_e64 v107, v106, v109, s[24:25]
	v_cndmask_b32_e64 v106, v109, v106, s[24:25]
	s_nop 1
	v_mov_b32_dpp v106, v106 quad_perm:[2,3,0,1] row_mask:0xf bank_mask:0xf
	s_add_u32 s33, s37, s0
	s_addc_u32 s59, s52, s1
	s_add_u32 s76, s33, s30
	s_addc_u32 s77, s59, 0
	s_waitcnt lgkmcnt(0)
; __device__ __forceinline__ void ph4_unit(const Frame& F, const Args& A, int c, int h) {
;     ...
;           for (int k = 0; k < 8; ++k) s1[k] = (b0 ? s0[2 * k + 1] : s0[2 * k]) + __shfl_xor(b0 ? s0[2 * k] : s0[2 * k + 1], 1);
; #pragma unroll
;           for (int k = 0; k < 4; ++k) s2[k] = (b1 ? s1[2 * k + 1] : s1[2 * k]) + __shfl_xor(b1 ? s1[2 * k] : s1[2 * k + 1], 2);
; #pragma unroll
;           for (int k = 0; k < 2; ++k) s3[k] = (b2 ? s2[2 * k + 1] : s2[2 * k]) + __shfl_xor(b2 ? s2[2 * k] : s2[2 * k + 1], 4);
;           float s4 = (b3 ? s3[1] : s3[0]) + __shfl_xor(b3 ? s3[0] : s3[1], 8);
;           s4 += __shfl_xor(s4, 16); s4 += __shfl_xor(s4, 32);
;           rl = __builtin_amdgcn_rsqf(s4 * (1.f / 128.f) + EPS_); }
	v_add_f32_e32 v106, v107, v106
	v_cndmask_b32_e64 v107, v106, v108, s[22:23]
	v_cndmask_b32_e64 v106, v108, v106, s[22:23]
	ds_bpermute_b32 v106, v103, v106
	s_add_u32 s0, s53, s0
	s_addc_u32 s1, s54, s1
	s_add_u32 s92, s0, s30
	s_addc_u32 s93, s1, 0
	s_waitcnt lgkmcnt(0)
	v_add_f32_e32 v108, v107, v106
	v_pk_mul_f32 v[106:107], v[16:17], v[16:17]
	s_lshl_b64 s[0:1], s[72:73], 11
	v_add_f32_e32 v109, v106, v107
	v_pk_mul_f32 v[106:107], v[14:15], v[14:15]
	s_add_u32 s33, s37, s0
	v_add_f32_e32 v106, v106, v107
	v_cndmask_b32_e64 v107, v106, v109, s[20:21]
	v_cndmask_b32_e64 v106, v109, v106, s[20:21]
	s_nop 1
	v_mov_b32_dpp v106, v106 quad_perm:[1,0,3,2] row_mask:0xf bank_mask:0xf
	s_addc_u32 s59, s52, s1
	v_cndmask_b32_e32 v18, v97, v18, vcc
	s_add_u32 s72, s33, s30
	v_lshlrev_b32_e32 v18, 2, v18
	s_waitcnt lgkmcnt(0)
	v_add_f32_e32 v109, v107, v106
	v_pk_mul_f32 v[106:107], v[12:13], v[12:13]
	s_addc_u32 s73, s59, 0
	v_add_f32_e32 v110, v106, v107
	v_pk_mul_f32 v[106:107], v[10:11], v[10:11]
	s_add_u32 s0, s53, s0
	v_add_f32_e32 v106, v106, v107
	v_cndmask_b32_e64 v107, v106, v110, s[20:21]
	v_cndmask_b32_e64 v106, v110, v106, s[20:21]
	s_nop 1
	v_mov_b32_dpp v106, v106 quad_perm:[1,0,3,2] row_mask:0xf bank_mask:0xf
	s_addc_u32 s1, s54, s1
	s_add_u32 s94, s0, s30
	s_addc_u32 s95, s1, 0
	s_lshl_b64 s[0:1], s[68:69], 11
	s_waitcnt lgkmcnt(0)
	v_add_f32_e32 v106, v107, v106
	v_cndmask_b32_e64 v107, v106, v109, s[24:25]
	v_cndmask_b32_e64 v106, v109, v106, s[24:25]
	s_nop 1
	v_mov_b32_dpp v106, v106 quad_perm:[2,3,0,1] row_mask:0xf bank_mask:0xf
	s_add_u32 s33, s37, s0
	s_addc_u32 s59, s52, s1
	s_add_u32 s68, s33, s30
	s_addc_u32 s69, s59, 0
	s_waitcnt lgkmcnt(0)
	v_add_f32_e32 v109, v107, v106
	v_pk_mul_f32 v[106:107], v[8:9], v[8:9]
	s_add_u32 s0, s53, s0
	v_add_f32_e32 v110, v106, v107
	v_pk_mul_f32 v[106:107], v[6:7], v[6:7]
	s_addc_u32 s1, s54, s1
	v_add_f32_e32 v106, v106, v107
	v_cndmask_b32_e64 v107, v106, v110, s[20:21]
	v_cndmask_b32_e64 v106, v110, v106, s[20:21]
	s_nop 1
	v_mov_b32_dpp v106, v106 quad_perm:[1,0,3,2] row_mask:0xf bank_mask:0xf
	s_add_u32 s96, s0, s30
	s_addc_u32 s97, s1, 0
	s_lshl_b64 s[0:1], s[66:67], 11
	s_add_u32 s33, s37, s0
	s_waitcnt lgkmcnt(0)
	v_add_f32_e32 v110, v107, v106
	v_pk_mul_f32 v[106:107], v[4:5], v[4:5]
	s_addc_u32 s59, s52, s1
	v_add_f32_e32 v111, v106, v107
	v_pk_mul_f32 v[106:107], v[2:3], v[2:3]
	s_add_u32 s66, s33, s30
	v_add_f32_e32 v106, v106, v107
	v_cndmask_b32_e64 v107, v106, v111, s[20:21]
	v_cndmask_b32_e64 v106, v111, v106, s[20:21]
	s_nop 1
	v_mov_b32_dpp v105, v106 quad_perm:[1,0,3,2] row_mask:0xf bank_mask:0xf
	s_addc_u32 s67, s59, 0
	s_add_u32 s0, s53, s0
	s_addc_u32 s1, s54, s1
	s_add_u32 vcc_lo, s0, s30
	s_waitcnt lgkmcnt(0)
	v_add_f32_e32 v105, v107, v105
	v_cndmask_b32_e64 v106, v105, v110, s[24:25]
	v_cndmask_b32_e64 v105, v110, v105, s[24:25]
	s_nop 1
	v_mov_b32_dpp v104, v105 quad_perm:[2,3,0,1] row_mask:0xf bank_mask:0xf
	s_addc_u32 vcc_hi, s1, 0
	s_lshl_b64 s[0:1], s[64:65], 11
	s_add_u32 s33, s37, s0
	s_addc_u32 s59, s52, s1
	s_waitcnt lgkmcnt(0)
	v_add_f32_e32 v104, v106, v104
	v_cndmask_b32_e64 v105, v104, v109, s[22:23]
	v_cndmask_b32_e64 v104, v109, v104, s[22:23]
	ds_bpermute_b32 v103, v103, v104
	s_add_u32 s64, s33, s30
	s_addc_u32 s65, s59, 0
	s_add_u32 s0, s53, s0
	s_addc_u32 s1, s54, s1
	s_waitcnt lgkmcnt(0)
	v_add_f32_e32 v103, v105, v103
	v_cndmask_b32_e64 v104, v103, v108, s[26:27]
	v_cndmask_b32_e64 v103, v108, v103, s[26:27]
	s_nop 1
	v_mov_b32_dpp v102, v103 row_ror:8 row_mask:0xf bank_mask:0xf
	s_add_u32 s90, s0, s30
	s_addc_u32 s91, s1, 0
	s_lshl_b64 s[48:49], s[48:49], 11
	s_add_u32 s0, s37, s48
	s_waitcnt lgkmcnt(0)
	v_add_f32_e32 v102, v104, v102
	ds_bpermute_b32 v63, v63, v102
	s_addc_u32 s1, s52, s49
	s_add_u32 s0, s0, s30
	s_addc_u32 s1, s1, 0
	v_readlane_b32 s2, v254, 18
	s_waitcnt lgkmcnt(0)
; __device__ __forceinline__ unsigned pk2(float lo, float hi) { const f32x2_t v = {lo, hi}; return __builtin_bit_cast(unsigned, __builtin_convertvector(v, bf16x2_hw)); }
; __device__ __forceinline__ void ph4_unit(const Frame& F, const Args& A, int c, int h) {
;     ...
;           rl = __builtin_amdgcn_rsqf(s4 * (1.f / 128.f) + EPS_); }
; #pragma unroll
;         for (int i = 0; i < 16; ++i) { const int rv = F.wave * 16 + i, t = rv >> 1, isk2 = rv & 1; const float x0 = bflo(qw[i]), x1 = bfhi(qw[i]);
;             const float r = __builtin_bit_cast(float, __builtin_amdgcn_readlane(__builtin_bit_cast(int, rl), i));
;             *(unsigned*)((isk2 ? KF : QF) + (size_t)(t0 + t) * 1024 + h * 128 + 2 * lane) = pk2(x0 * r * (isk2 ? gk0 : gq0), x1 * r * (isk2 ? gk1 : gq1)); }
	v_add_f32_e32 v63, v102, v63
	ds_bpermute_b32 v18, v18, v63
	v_readlane_b32 s3, v254, 19
	v_readlane_b32 s4, v254, 20
	v_readlane_b32 s5, v254, 21
	v_readlane_b32 s6, v254, 22
	s_waitcnt lgkmcnt(0)
	v_add_f32_e32 v18, v63, v18
	v_fmamk_f32 v18, v18, 0x3c000000, v98
	v_rsq_f32_e32 v18, v18
	v_readlane_b32 s7, v254, 23
	v_readlane_b32 s12, v254, 28
	v_readlane_b32 s13, v254, 29
	v_readlane_b32 s60, v18, 0
	v_readlane_b32 s14, v254, 30
	v_readlane_b32 s15, v254, 31
	v_pk_mul_f32 v[82:83], s[60:61], v[82:83] op_sel_hi:[0,1]
	s_waitcnt vmcnt(3)
	v_pk_mul_f32 v[82:83], v[74:75], v[82:83]
	s_nop 0
	v_cvt_pk_bf16_f32 v63, v82, v83
	global_store_dword v92, v63, s[50:51]
	v_readlane_b32 s50, v18, 1
	s_nop 1
	v_pk_mul_f32 v[78:79], s[50:51], v[78:79] op_sel_hi:[0,1]
	v_readlane_b32 s50, v18, 2
	s_waitcnt vmcnt(3)
	v_pk_mul_f32 v[78:79], v[80:81], v[78:79]
	v_pk_mul_f32 v[76:77], s[50:51], v[76:77] op_sel_hi:[0,1]
	v_readlane_b32 s50, v18, 3
	v_cvt_pk_bf16_f32 v63, v78, v79
	v_pk_mul_f32 v[76:77], v[74:75], v[76:77]
	v_pk_mul_f32 v[72:73], s[50:51], v[72:73] op_sel_hi:[0,1]
	v_readlane_b32 s50, v18, 4
	global_store_dword v92, v63, s[84:85]
	v_cvt_pk_bf16_f32 v63, v76, v77
	v_pk_mul_f32 v[70:71], s[50:51], v[70:71] op_sel_hi:[0,1]
	v_readlane_b32 s50, v18, 5
	v_pk_mul_f32 v[72:73], v[80:81], v[72:73]
	global_store_dword v92, v63, s[80:81]
	v_pk_mul_f32 v[68:69], s[50:51], v[68:69] op_sel_hi:[0,1]
	v_readlane_b32 s50, v18, 6
	v_cvt_pk_bf16_f32 v63, v72, v73
	v_pk_mul_f32 v[70:71], v[74:75], v[70:71]
	v_pk_mul_f32 v[66:67], s[50:51], v[66:67] op_sel_hi:[0,1]
	v_readlane_b32 s50, v18, 7
	global_store_dword v92, v63, s[86:87]
	v_cvt_pk_bf16_f32 v63, v70, v71
	v_pk_mul_f32 v[64:65], s[50:51], v[64:65] op_sel_hi:[0,1]
	v_readlane_b32 s50, v18, 8
	v_pk_mul_f32 v[68:69], v[80:81], v[68:69]
	global_store_dword v92, v63, s[76:77]
	v_pk_mul_f32 v[16:17], s[50:51], v[16:17] op_sel_hi:[0,1]
	v_readlane_b32 s50, v18, 9
	v_cvt_pk_bf16_f32 v63, v68, v69
	v_pk_mul_f32 v[66:67], v[74:75], v[66:67]
	v_pk_mul_f32 v[14:15], s[50:51], v[14:15] op_sel_hi:[0,1]
	v_readlane_b32 s50, v18, 10
	global_store_dword v92, v63, s[92:93]
	v_cvt_pk_bf16_f32 v63, v66, v67
	v_pk_mul_f32 v[12:13], s[50:51], v[12:13] op_sel_hi:[0,1]
	v_readlane_b32 s50, v18, 11
	v_pk_mul_f32 v[64:65], v[80:81], v[64:65]
	v_pk_mul_f32 v[16:17], v[74:75], v[16:17]
	v_pk_mul_f32 v[10:11], s[50:51], v[10:11] op_sel_hi:[0,1]
	v_readlane_b32 s50, v18, 12
	v_pk_mul_f32 v[14:15], v[80:81], v[14:15]
	v_pk_mul_f32 v[12:13], v[74:75], v[12:13]
	v_pk_mul_f32 v[8:9], s[50:51], v[8:9] op_sel_hi:[0,1]
	v_readlane_b32 s50, v18, 13
	v_pk_mul_f32 v[10:11], v[80:81], v[10:11]
	global_store_dword v92, v63, s[72:73]
	v_pk_mul_f32 v[6:7], s[50:51], v[6:7] op_sel_hi:[0,1]
	v_readlane_b32 s50, v18, 14
	v_pk_mul_f32 v[6:7], v[80:81], v[6:7]
	v_cvt_pk_bf16_f32 v63, v64, v65
	v_pk_mul_f32 v[4:5], s[50:51], v[4:5] op_sel_hi:[0,1]
	v_pk_mul_f32 v[4:5], v[74:75], v[4:5]
	v_cvt_pk_bf16_f32 v16, v16, v17
	v_cvt_pk_bf16_f32 v14, v14, v15
	v_cvt_pk_bf16_f32 v12, v12, v13
	v_cvt_pk_bf16_f32 v10, v10, v11
	v_cvt_pk_bf16_f32 v6, v6, v7
	v_cvt_pk_bf16_f32 v4, v4, v5
	global_store_dword v92, v63, s[94:95]
	global_store_dword v92, v16, s[68:69]
	global_store_dword v92, v14, s[96:97]
	global_store_dword v92, v12, s[66:67]
	global_store_dword v92, v10, vcc
	global_store_dword v92, v6, s[90:91]
	global_store_dword v92, v4, s[0:1]
	v_readlane_b32 s0, v18, 15
	v_readlane_b32 s92, v254, 49
	v_pk_mul_f32 v[8:9], v[74:75], v[8:9]
	v_pk_mul_f32 v[2:3], s[0:1], v[2:3] op_sel_hi:[0,1]
	s_add_u32 s0, s53, s48
	s_addc_u32 s1, s54, s49
	s_add_u32 s0, s0, s30
	v_pk_mul_f32 v[2:3], v[80:81], v[2:3]
	s_addc_u32 s1, s1, 0
	s_add_i32 s58, s58, s92
	v_cvt_pk_bf16_f32 v8, v8, v9
	v_cvt_pk_bf16_f32 v2, v2, v3
	s_cmpk_lt_i32 s58, 0x400
	global_store_dword v92, v8, s[64:65]
	global_store_dword v92, v2, s[0:1]
	s_barrier
	s_cbranch_scc0 .LBB0_474

; __device__ __forceinline__ float logsig(float x) { const float e = __builtin_amdgcn_exp2f(-1.4426950408889634f * fabsf(x)); const float l = 0.6931471805599453f * __builtin_amdgcn_logf(1.f + e); return (x < 0.f ? x : 0.f) - l; }
; __device__ __forceinline__ float wave_scan_add(float v, int lane) {
; #pragma unroll
;     for (int o = 1; o < 64; o <<= 1) { const float t = __shfl_up(v, o); if (lane >= o) v += t; }
;     return v;
; }
; __device__ __forceinline__ void ph4_unit(const Frame& F, const Args& A, int c, int h) {
;     ...
;     if (F.wave == 0) {
;         const float* gr = G24 + (size_t)(t0 + lane) * 24;
;         const float ip = gr[h] + A.in[I_MIB][h], lf = logsig(gr[8 + h] + A.in[I_MFB][h]), lff = logsig(gr[16 + h] + A.in[I_FFB][h]);
;         const float b = wave_scan_add(lf, lane), fl = wave_scan_add(lff, lane), g = __shfl(b, 63);
;         const float a = g - b + ip, amax = wave_max(a), wk = expf(a - amax);
.LBB0_374:
	s_andn2_b64 vcc, exec, s[0:1]
	s_lshl_b32 s33, s50, 7
	s_cbranch_vccnz .LBB0_378
	v_readlane_b32 s0, v255, 3
	v_readlane_b32 s1, v255, 4
	v_or_b32_e32 v113, s49, v1
	s_lshl_b32 s30, s50, 2
	v_mov_b64_e32 v[114:115], s[0:1]
	s_movk_i32 s0, 0x60
	v_mad_i64_i32 v[114:115], s[0:1], v113, s0, v[114:115]
	v_readlane_b32 s0, v254, 16
	v_lshl_add_u64 v[114:115], v[114:115], 0, s[30:31]
	v_mov_b32_e32 v116, s30
	v_readlane_b32 s1, v254, 17
	global_load_dword v113, v[114:115], off
	v_readlane_b32 s2, v254, 18
	v_readlane_b32 s3, v254, 19
	v_readlane_b32 s6, v254, 22
	v_readlane_b32 s7, v254, 23
	global_load_dword v117, v116, s[0:1]
	s_mov_b32 s0, 0xbfb8aa3b
	s_lshl_b32 s30, s50, 13
	v_readlane_b32 s4, v254, 20
	v_readlane_b32 s5, v254, 21
	v_readlane_b32 s8, v254, 24
	v_readlane_b32 s9, v254, 25
	v_readlane_b32 s10, v254, 26
	v_readlane_b32 s11, v254, 27
	v_readlane_b32 s12, v254, 28
	v_readlane_b32 s13, v254, 29
	v_readlane_b32 s14, v254, 30
	v_readlane_b32 s15, v254, 31
	global_load_dword v131, v[114:115], off offset:32
	global_load_dword v132, v116, s[2:3]
	global_load_dword v133, v[114:115], off offset:64
	global_load_dword v134, v116, s[6:7]
	s_waitcnt vmcnt(0)
	v_add_f32_e32 v113, v113, v117
	v_mov_b32_e32 v117, v131
	v_mov_b32_e32 v118, v132
	s_nop 0
	v_mov_b32_e32 v114, v133
	s_nop 0
	v_mov_b32_e32 v115, v134
	v_readlane_b32 s2, v255, 13
	v_readlane_b32 s3, v255, 14
	s_waitcnt vmcnt(2)
	v_add_f32_e32 v117, v117, v118
	v_mul_f32_e64 v118, |v117|, s0
	v_exp_f32_e32 v118, v118
	s_waitcnt vmcnt(0)
	v_add_f32_e32 v114, v114, v115
	v_mul_f32_e64 v115, |v114|, s0
	v_exp_f32_e32 v115, v115
	v_add_f32_e32 v118, 1.0, v118
	v_log_f32_e32 v118, v118
	v_min_f32_e32 v117, 0, v117
	v_add_f32_e32 v115, 1.0, v115
	v_log_f32_e32 v115, v115
	v_fmac_f32_e32 v117, 0xbf317218, v118
	v_min_f32_e32 v116, 0, v114
	v_and_b32_e32 v118, 64, v97
	v_add_u32_e32 v114, -1, v97
	v_cmp_lt_i32_e32 vcc, v114, v118
	v_fmac_f32_e32 v116, 0xbf317218, v115
	v_readlane_b32 s0, v255, 5
	v_cndmask_b32_e32 v114, v114, v97, vcc
	v_lshlrev_b32_e32 v115, 2, v114
	ds_bpermute_b32 v114, v115, v117
	v_readlane_b32 s1, v255, 6
	ds_bpermute_b32 v115, v115, v116
	s_waitcnt lgkmcnt(1)
	v_add_f32_e32 v114, v117, v114
	v_cndmask_b32_e64 v114, v114, v117, s[38:39]
	v_add_u32_e32 v117, -2, v97
	v_cmp_lt_i32_e32 vcc, v117, v118
	s_waitcnt lgkmcnt(0)
	v_add_f32_e32 v115, v116, v115
	v_cndmask_b32_e64 v115, v115, v116, s[38:39]
	v_cndmask_b32_e32 v117, v117, v97, vcc
	v_lshlrev_b32_e32 v119, 2, v117
	ds_bpermute_b32 v117, v119, v114
	ds_bpermute_b32 v116, v119, v115
	v_lshl_or_b32 v119, v97, 2, v99
	s_waitcnt lgkmcnt(1)
	v_add_f32_e32 v117, v114, v117
	v_cndmask_b32_e64 v114, v117, v114, s[40:41]
	v_add_u32_e32 v117, -4, v97
	v_cmp_lt_i32_e32 vcc, v117, v118
	s_waitcnt lgkmcnt(0)
	v_add_f32_e32 v116, v115, v116
	v_cndmask_b32_e64 v115, v116, v115, s[40:41]
	v_cndmask_b32_e32 v117, v117, v97, vcc
	v_lshlrev_b32_e32 v120, 2, v117
	ds_bpermute_b32 v117, v120, v114
	ds_bpermute_b32 v116, v120, v115
	v_xor_b32_e32 v120, 1, v97
	s_waitcnt lgkmcnt(1)
	v_add_f32_e32 v117, v114, v117
	v_cndmask_b32_e64 v114, v117, v114, s[42:43]
	v_add_u32_e32 v117, -8, v97
	v_cmp_lt_i32_e32 vcc, v117, v118
	s_waitcnt lgkmcnt(0)
	v_add_f32_e32 v116, v115, v116
	v_cndmask_b32_e64 v115, v116, v115, s[42:43]
	v_cndmask_b32_e32 v117, v117, v97, vcc
	v_lshlrev_b32_e32 v121, 2, v117
	ds_bpermute_b32 v117, v121, v114
	ds_bpermute_b32 v116, v121, v115
	v_xor_b32_e32 v121, 2, v97
	s_waitcnt lgkmcnt(1)
	v_add_f32_e32 v117, v114, v117
	v_cndmask_b32_e64 v114, v117, v114, s[34:35]
	v_add_u32_e32 v117, -16, v97
	v_cmp_lt_i32_e32 vcc, v117, v118
	s_waitcnt lgkmcnt(0)
	v_add_f32_e32 v116, v115, v116
	v_cndmask_b32_e64 v115, v116, v115, s[34:35]
	v_cndmask_b32_e32 v117, v117, v97, vcc
	v_lshlrev_b32_e32 v122, 2, v117
	ds_bpermute_b32 v117, v122, v114
	ds_bpermute_b32 v116, v122, v115
	s_waitcnt lgkmcnt(1)
; __device__ __forceinline__ float wave_max(float v) {
; #pragma unroll
;     for (int o = 1; o < 64; o <<= 1) v = fmaxf(v, __shfl_xor(v, o));
;     return v;
; }
; __device__ __forceinline__ void ph4_unit(const Frame& F, const Args& A, int c, int h) {
;     ...
;         const float b = wave_scan_add(lf, lane), fl = wave_scan_add(lff, lane), g = __shfl(b, 63);
;         const float a = g - b + ip, amax = wave_max(a), wk = expf(a - amax);
;         ((float*)(ws + WS_BL))[h * S_ + t0 + lane] = b; ((float*)(ws + WS_IPL))[h * S_ + t0 + lane] = ip; ((float*)(ws + WS_FLOC))[h * S_ + t0 + lane] = fl;
;         wkL[lane] = wk; uL[lane] = 0.f;
;         if (lane == 63) { float* SC = (float*)(ws + WS_SC); SC[h * 128 + c] = b; SC[1024 + h * 128 + c] = amax; SC[2048 + h * 128 + c] = fl; }
	v_add_f32_e32 v117, v114, v117
	v_cndmask_b32_e64 v117, v117, v114, s[0:1]
	v_subrev_u32_e32 v114, 32, v97
	v_cmp_lt_i32_e32 vcc, v114, v118
	v_add_u32_e32 v118, 64, v118
	s_waitcnt lgkmcnt(0)
	v_add_f32_e32 v116, v115, v116
	v_cndmask_b32_e32 v114, v114, v97, vcc
	v_lshlrev_b32_e32 v123, 2, v114
	ds_bpermute_b32 v114, v123, v117
	v_cmp_lt_i32_e32 vcc, v120, v118
	v_cndmask_b32_e64 v116, v116, v115, s[0:1]
	s_mov_b32 s0, 0x3fb8aa3b
	v_cndmask_b32_e32 v120, v97, v120, vcc
	s_waitcnt lgkmcnt(0)
	v_add_f32_e32 v114, v117, v114
	v_cndmask_b32_e64 v117, v114, v117, s[62:63]
	ds_bpermute_b32 v119, v119, v117
	v_lshlrev_b32_e32 v120, 2, v120
	v_cmp_lt_i32_e32 vcc, v121, v118
	ds_bpermute_b32 v115, v123, v116
	s_waitcnt lgkmcnt(1)
	v_sub_f32_e32 v119, v119, v117
	v_add_f32_e32 v119, v113, v119
	ds_bpermute_b32 v120, v120, v119
	v_cndmask_b32_e32 v121, v97, v121, vcc
	v_lshlrev_b32_e32 v121, 2, v121
	s_waitcnt lgkmcnt(1)
	v_add_f32_e32 v115, v116, v115
	v_cndmask_b32_e64 v116, v115, v116, s[62:63]
	s_waitcnt lgkmcnt(0)
	v_max_f32_e32 v120, v120, v120
	v_max_f32_e32 v120, v119, v120
	ds_bpermute_b32 v121, v121, v120
	s_waitcnt lgkmcnt(0)
	v_max_f32_e32 v121, v121, v121
	v_max_f32_e32 v120, v120, v121
	v_xor_b32_e32 v121, 4, v97
	v_cmp_lt_i32_e32 vcc, v121, v118
	s_nop 1
	v_cndmask_b32_e32 v121, v97, v121, vcc
	v_lshlrev_b32_e32 v121, 2, v121
	ds_bpermute_b32 v121, v121, v120
	s_waitcnt lgkmcnt(0)
	v_max_f32_e32 v121, v121, v121
	v_max_f32_e32 v120, v120, v121
	v_xor_b32_e32 v121, 8, v97
	v_cmp_lt_i32_e32 vcc, v121, v118
	s_nop 1
	v_cndmask_b32_e32 v121, v97, v121, vcc
	v_lshlrev_b32_e32 v121, 2, v121
	ds_bpermute_b32 v121, v121, v120
	s_waitcnt lgkmcnt(0)
	v_max_f32_e32 v121, v121, v121
	v_max_f32_e32 v120, v120, v121
	v_xor_b32_e32 v121, 16, v97
	v_cmp_lt_i32_e32 vcc, v121, v118
	s_nop 1
	v_cndmask_b32_e32 v121, v97, v121, vcc
	v_lshlrev_b32_e32 v121, 2, v121
	ds_bpermute_b32 v121, v121, v120
	s_waitcnt lgkmcnt(0)
	v_max_f32_e32 v121, v121, v121
	v_max_f32_e32 v120, v120, v121
	v_xor_b32_e32 v121, 32, v97
	v_cmp_lt_i32_e32 vcc, v121, v118
	s_nop 1
	v_cndmask_b32_e32 v118, v97, v121, vcc
	v_lshlrev_b32_e32 v118, 2, v118
	ds_bpermute_b32 v118, v118, v120
	s_waitcnt lgkmcnt(0)
	v_max_f32_e32 v118, v118, v118
	v_max_f32_e32 v118, v120, v118
	v_sub_f32_e32 v119, v119, v118
	v_mul_f32_e32 v120, 0x3fb8aa3b, v119
	v_fma_f32 v121, v119, s0, -v120
	v_rndne_f32_e32 v122, v120
	v_fmac_f32_e32 v121, 0x32a5705f, v119
	v_sub_f32_e32 v120, v120, v122
	v_add_f32_e32 v120, v120, v121
	v_exp_f32_e32 v120, v120
	v_cvt_i32_f32_e32 v121, v122
	s_mov_b32 s0, 0xc2ce8ed0
	v_cmp_ngt_f32_e32 vcc, s0, v119
	s_mov_b32 s0, 0x42b17218
	v_ldexp_f32 v120, v120, v121
	v_cndmask_b32_e32 v120, 0, v120, vcc
	v_cmp_nlt_f32_e32 vcc, s0, v119
	s_add_i32 s0, s30, s49
	s_nop 0
	v_cndmask_b32_e32 v119, v100, v120, vcc
	v_or_b32_e32 v120, s0, v1
	v_ashrrev_i32_e32 v121, 31, v120
	v_readlane_b32 s0, v255, 7
	v_lshlrev_b64 v[120:121], 2, v[120:121]
	v_readlane_b32 s1, v255, 8
	ds_write2st64_b32 v87, v119, v19 offset0:128 offset1:129
	s_nop 0
	v_lshl_add_u64 v[122:123], s[0:1], 0, v[120:121]
	v_readlane_b32 s0, v255, 9
	v_readlane_b32 s1, v255, 10
	global_store_dword v[122:123], v117, off
	s_nop 0
	v_lshl_add_u64 v[122:123], s[0:1], 0, v[120:121]
	v_readlane_b32 s0, v255, 11
	v_readlane_b32 s1, v255, 12
	global_store_dword v[122:123], v113, off
	s_nop 0
	v_lshl_add_u64 v[120:121], s[0:1], 0, v[120:121]
	global_store_dword v[120:121], v116, off
	s_and_saveexec_b64 s[0:1], s[2:3]
	s_cbranch_execz .LBB0_377
	s_add_i32 s50, s33, s59
	s_ashr_i32 s51, s50, 31
	s_lshl_b64 s[50:51], s[50:51], 2
	v_readlane_b32 s2, v255, 15
	s_add_u32 s50, s2, s50
	v_readlane_b32 s2, v255, 17
	s_addc_u32 s51, s2, s51
	global_store_dword v19, v114, s[50:51]
	global_store_dword v93, v118, s[50:51]
	global_store_dword v94, v115, s[50:51]

; __device__ __forceinline__ void ph5_tables(const Frame& F, const Args& A) {
;     ...
;     {
;         const float v0 = SC[2048 + h * 128 + 2 * l], v1 = SC[2048 + h * 128 + 2 * l + 1]; const float sm = v0 + v1; const float incl = wave_scan_add(sm, l);
;         inclL[h * 128 + 2 * l] = incl - v1; inclL[h * 128 + 2 * l + 1] = incl;
;         const float* gq = A.in[I_FQG] + h * 128 + 2 * l; const float* gk = A.in[I_FKG] + h * 128 + 2 * l;
;         const float gqm = wave_max(fmaxf(fabsf(gq[0]), fabsf(gq[1]))), gkm = wave_max(fmaxf(fabsf(gk[0]), fabsf(gk[1])));
;         if (l == 0) thL[h] = 106.f + 2.f * 11.313708498984761f * gqm * gkm * 1.02f;
;     }
;     {
;         const float g0 = SC[h * 128 + 2 * l], g1 = SC[h * 128 + 2 * l + 1], a0 = SC[1024 + h * 128 + 2 * l], a1 = SC[1024 + h * 128 + 2 * l + 1];
;         const float gi1 = wave_scan_add(g0 + g1, l), gi0 = gi1 - g1, gx0 = gi0 - g0;
;         const float val0 = a0 - gi0, val1 = a1 - gi1;
;         const float pmi = wave_scan_max(fmaxf(val0, val1), l); float pme = __shfl_up(pmi, 1); if (l == 0) pme = -INFINITY;
.LBB0_529:
	v_readlane_b32 s0, v254, 9
	v_readlane_b32 s1, v254, 10
	s_cmp_lt_i32 s0, 6
	s_cselect_b64 s[0:1], -1, 0
	s_and_b64 s[80:81], s[0:1], s[2:3]
	s_andn2_b64 vcc, exec, s[80:81]
	s_cbranch_vccnz .LBB0_882
	v_mov_b32_e32 v2, v0
	s_add_u32 s0, s88, 0xb00000
	v_and_b32_e32 v14, 63, v2
	v_readlane_b32 s2, v254, 32
	v_readlane_b32 s4, v254, 16
	s_addc_u32 s1, s89, 0
	s_lshl_b32 s2, s2, 7
	v_lshlrev_b32_e32 v75, 1, v14
	s_mov_b32 s3, 0
	v_readlane_b32 s8, v254, 20
	v_readlane_b32 s9, v254, 21
	v_readlane_b32 s10, v254, 22
	v_readlane_b32 s11, v254, 23
	v_readlane_b32 s12, v254, 24
	v_readlane_b32 s13, v254, 25
	v_or_b32_e32 v4, s2, v75
	s_lshl_b64 s[2:3], s[2:3], 2
	v_readlane_b32 s14, v254, 26
	v_readlane_b32 s15, v254, 27
	s_mov_b64 s[8:9], s[12:13]
	v_readlane_b32 s5, v254, 17
	s_add_u32 s4, s8, s2
	v_add_u32_e32 v6, 0x800, v4
	s_mov_b64 s[10:11], s[14:15]
	s_addc_u32 s5, s9, s3
	v_lshlrev_b32_e32 v1, 3, v14
	global_load_dwordx2 v[16:17], v1, s[4:5]
	v_ashrrev_i32_e32 v7, 31, v6
	s_add_u32 s2, s10, s2
	s_addc_u32 s3, s11, s3
	v_lshl_add_u64 v[6:7], v[6:7], 2, s[0:1]
	global_load_dwordx2 v[18:19], v1, s[2:3]
	global_load_dwordx2 v[20:21], v[6:7], off
	v_lshlrev_b32_e32 v60, 2, v4
	v_add_u32_e32 v61, 0x1000, v60
	global_load_dwordx2 v[64:65], v60, s[0:1]
	global_load_dwordx2 v[66:67], v61, s[0:1]
	v_mbcnt_lo_u32_b32 v1, -1, 0
	v_mbcnt_hi_u32_b32 v1, -1, v1
	v_and_b32_e32 v3, 64, v1
	v_add_u32_e32 v5, -1, v1
	v_add_u32_e32 v6, -2, v1
	v_cmp_lt_i32_e32 vcc, v5, v3
	v_add_u32_e32 v7, -4, v1
	v_add_u32_e32 v8, -8, v1
	v_cndmask_b32_e32 v5, v5, v1, vcc
	v_cmp_lt_i32_e32 vcc, v6, v3
	v_add_u32_e32 v9, -16, v1
	v_subrev_u32_e32 v10, 32, v1
	v_cndmask_b32_e32 v6, v6, v1, vcc
	v_cmp_lt_i32_e32 vcc, v7, v3
	v_xor_b32_e32 v13, 1, v1
	v_add_u32_e32 v28, 64, v3
	v_cndmask_b32_e32 v7, v7, v1, vcc
	v_cmp_lt_i32_e32 vcc, v8, v3
	v_xor_b32_e32 v15, 2, v1
	v_xor_b32_e32 v22, 4, v1
	v_cndmask_b32_e32 v8, v8, v1, vcc
	v_cmp_lt_i32_e32 vcc, v9, v3
	v_lshlrev_b32_e32 v12, 2, v5
	v_xor_b32_e32 v23, 8, v1
	v_cndmask_b32_e32 v26, v9, v1, vcc
	v_cmp_lt_i32_e32 vcc, v10, v3
	v_lshlrev_b32_e32 v11, 2, v6
	v_xor_b32_e32 v24, 16, v1
	v_cndmask_b32_e32 v27, v10, v1, vcc
	v_cmp_lt_i32_e32 vcc, v13, v28
	v_lshlrev_b32_e32 v10, 2, v7
	v_xor_b32_e32 v25, 32, v1
	v_cndmask_b32_e32 v5, v1, v13, vcc
	v_cmp_lt_i32_e32 vcc, v15, v28
	v_cmp_eq_u32_e64 s[2:3], 0, v14
	v_readlane_b32 s6, v254, 18
	v_cndmask_b32_e32 v6, v1, v15, vcc
	v_cmp_lt_i32_e32 vcc, v22, v28
	v_readlane_b32 s7, v254, 19
	v_cmp_gt_u32_e64 s[6:7], 2, v14
	v_cndmask_b32_e32 v7, v1, v22, vcc
	v_cmp_lt_i32_e32 vcc, v23, v28
	v_cmp_gt_u32_e64 s[8:9], 4, v14
	v_lshlrev_b32_e32 v9, 2, v8
	v_cndmask_b32_e32 v13, v1, v23, vcc
	v_cmp_lt_i32_e32 vcc, v24, v28
	v_cmp_gt_u32_e64 s[10:11], 8, v14
	v_lshlrev_b32_e32 v8, 2, v26
	v_cndmask_b32_e32 v15, v1, v24, vcc
	v_cmp_lt_i32_e32 vcc, v25, v28
	v_cmp_gt_u32_e64 s[12:13], 16, v14
	v_lshlrev_b32_e32 v3, 2, v27
	v_cndmask_b32_e32 v22, v1, v25, vcc
	v_lshlrev_b32_e32 v1, 2, v5
	v_lshlrev_b32_e32 v5, 2, v6
	v_lshlrev_b32_e32 v6, 2, v7
	v_lshlrev_b32_e32 v7, 2, v13
	v_lshlrev_b32_e32 v13, 2, v15
	v_cmp_gt_u32_e64 s[14:15], 32, v14
	v_readlane_b32 s16, v254, 28
	v_readlane_b32 s17, v254, 29
	v_readlane_b32 s18, v254, 30
	v_readlane_b32 s19, v254, 31
	s_waitcnt vmcnt(0)
	v_max_f32_e64 v15, |v17|, |v17|
	v_max_f32_e64 v16, |v16|, |v16|
	v_max_f32_e32 v15, v16, v15
	ds_bpermute_b32 v16, v1, v15
	v_max_f32_e64 v17, |v19|, |v19|
	v_add_f32_e32 v19, v20, v21
	ds_bpermute_b32 v20, v12, v19
	v_max_f32_e64 v18, |v18|, |v18|
	v_max_f32_e32 v17, v18, v17
	s_waitcnt lgkmcnt(1)
	v_max_f32_e32 v16, v16, v16
	ds_bpermute_b32 v18, v1, v17
	v_max_f32_e32 v15, v15, v16
	s_waitcnt lgkmcnt(1)
	v_add_f32_e32 v16, v19, v20
	ds_bpermute_b32 v20, v5, v15
	v_cndmask_b32_e64 v16, v16, v19, s[2:3]
	ds_bpermute_b32 v19, v11, v16
	s_waitcnt lgkmcnt(2)
	v_max_f32_e32 v18, v18, v18
	v_max_f32_e32 v17, v17, v18
	s_waitcnt lgkmcnt(1)
	v_max_f32_e32 v18, v20, v20
	ds_bpermute_b32 v5, v5, v17
	v_max_f32_e32 v15, v15, v18
	s_waitcnt lgkmcnt(1)
	v_add_f32_e32 v18, v16, v19
	ds_bpermute_b32 v19, v6, v15
	v_cndmask_b32_e64 v16, v18, v16, s[6:7]
	ds_bpermute_b32 v18, v10, v16
	s_waitcnt lgkmcnt(2)
	v_max_f32_e32 v5, v5, v5
	v_max_f32_e32 v5, v17, v5
	s_waitcnt lgkmcnt(1)
	v_max_f32_e32 v17, v19, v19
	ds_bpermute_b32 v6, v6, v5
	v_max_f32_e32 v15, v15, v17
	s_waitcnt lgkmcnt(1)
	v_add_f32_e32 v17, v16, v18
	v_cndmask_b32_e64 v16, v17, v16, s[8:9]
	ds_bpermute_b32 v17, v9, v16
	s_waitcnt lgkmcnt(1)
	v_max_f32_e32 v6, v6, v6
	v_max_f32_e32 v5, v5, v6
	ds_bpermute_b32 v18, v7, v15
	ds_bpermute_b32 v6, v7, v5
	s_waitcnt lgkmcnt(2)
	v_add_f32_e32 v7, v16, v17
	v_cndmask_b32_e64 v7, v7, v16, s[10:11]
	ds_bpermute_b32 v16, v8, v7
	s_waitcnt lgkmcnt(2)
	v_max_f32_e32 v17, v18, v18
	v_max_f32_e32 v15, v15, v17
	ds_bpermute_b32 v17, v13, v15
	s_waitcnt lgkmcnt(2)
	v_max_f32_e32 v6, v6, v6
	s_waitcnt lgkmcnt(1)
	v_add_f32_e32 v16, v7, v16
	v_cndmask_b32_e64 v7, v16, v7, s[12:13]
	ds_bpermute_b32 v16, v3, v7
	v_max_f32_e32 v6, v5, v6
	ds_bpermute_b32 v13, v13, v6
	s_waitcnt lgkmcnt(2)
	v_max_f32_e32 v5, v17, v17
	v_max_f32_e32 v5, v15, v5
	s_waitcnt lgkmcnt(1)
	v_add_f32_e32 v15, v7, v16
	v_cndmask_b32_e64 v17, v15, v7, s[14:15]
	s_waitcnt lgkmcnt(0)
	v_max_f32_e32 v7, v13, v13
	v_lshlrev_b32_e32 v16, 2, v22
	v_max_f32_e32 v7, v6, v7
	ds_bpermute_b32 v15, v16, v5
	ds_bpermute_b32 v13, v16, v7
	v_lshl_add_u32 v6, v4, 2, 0
	v_sub_f32_e32 v16, v17, v21
	v_add_u32_e32 v18, 0x19400, v6
	ds_write_b64 v18, v[16:17]
	s_and_saveexec_b64 s[4:5], s[2:3]
	s_cbranch_execz .LBB0_532
	v_readlane_b32 s16, v254, 32
	s_waitcnt lgkmcnt(2)
	v_max_f32_e32 v15, v15, v15
	v_max_f32_e32 v5, v5, v5
	s_lshl_b32 s16, s16, 2
	v_max_f32_e32 v5, v5, v15
	s_waitcnt lgkmcnt(1)
	v_max_f32_e32 v13, v13, v13
	v_max_f32_e32 v7, v7, v7
	s_add_i32 s16, s16, 0
	v_mul_f32_e32 v5, 0x41b504f3, v5
	v_max_f32_e32 v7, v7, v13
	s_add_i32 s16, s16, 0x1b020
	v_mul_f32_e32 v5, v5, v7
	v_mov_b32_e32 v7, 0x42d40000
	v_fmac_f32_e32 v7, 0x3f828f5c, v5
	v_mov_b32_e32 v5, s16
	ds_write_b32 v5, v7
; __device__ __forceinline__ void ph5_tables(const Frame& F, const Args& A) {
;     ...
;     {
;         const float g0 = SC[h * 128 + 2 * l], g1 = SC[h * 128 + 2 * l + 1], a0 = SC[1024 + h * 128 + 2 * l], a1 = SC[1024 + h * 128 + 2 * l + 1];
;         const float gi1 = wave_scan_add(g0 + g1, l), gi0 = gi1 - g1, gx0 = gi0 - g0;
;         const float val0 = a0 - gi0, val1 = a1 - gi1;
;         const float pmi = wave_scan_max(fmaxf(val0, val1), l); float pme = __shfl_up(pmi, 1); if (l == 0) pme = -INFINITY;
;         const float M0 = fmaxf(0.f, pme), M1 = fmaxf(M0, val0), M2 = fmaxf(M1, val1);
;         const float m0 = M0 + gx0, m1 = M1 + gi0, m2 = M2 + gi1;
;         decL[h * 128 + 2 * l] = expf(g0 + m0 - m1); sclL[h * 128 + 2 * l] = expf(a0 - m1);
;         decL[h * 128 + 2 * l + 1] = expf(g1 + m1 - m2); sclL[h * 128 + 2 * l + 1] = expf(a1 - m2);
;         if (F.vcu == 0) { float* MST = (float*)(ws + WS_SC) + 3072; MST[h * 128 + 2 * l] = m0; MST[h * 128 + 2 * l + 1] = m1; }
.LBB0_532:
	s_or_b64 exec, exec, s[4:5]
	v_mov_b32_e32 v5, 0
	v_lshl_add_u64 v[16:17], v[4:5], 2, s[0:1]
	v_mov_b64_e32 v[16:17], v[64:65]
	v_add_u32_e32 v18, 0x400, v4
	v_ashrrev_i32_e32 v19, 31, v18
	v_lshl_add_u64 v[18:19], v[18:19], 2, s[0:1]
	v_mov_b64_e32 v[18:19], v[66:67]
	v_add_u32_e32 v24, 0x1b400, v6
	v_add_u32_e32 v25, 0x1c400, v6
	s_mov_b32 s0, 0x3fb8aa3b
	s_mov_b32 s1, 0xc2ce8ed0
	s_mov_b32 s4, 0x42b17218
	v_mov_b32_e32 v23, 0x7f800000
	v_readlane_b32 s5, v254, 4
	s_cmp_eq_u32 s5, 0
	s_cselect_b64 s[18:19], -1, 0
	s_cmp_lg_u32 s5, 0
	s_waitcnt vmcnt(1)
	v_add_f32_e32 v7, v16, v17
	s_waitcnt lgkmcnt(1)
	ds_bpermute_b32 v13, v12, v7
	s_waitcnt lgkmcnt(0)
	v_add_f32_e32 v13, v7, v13
	v_cndmask_b32_e64 v7, v13, v7, s[2:3]
	ds_bpermute_b32 v13, v11, v7
	s_waitcnt lgkmcnt(0)
	v_add_f32_e32 v13, v7, v13
	v_cndmask_b32_e64 v7, v13, v7, s[6:7]
	ds_bpermute_b32 v13, v10, v7
	s_waitcnt lgkmcnt(0)
	v_add_f32_e32 v13, v7, v13
	v_cndmask_b32_e64 v7, v13, v7, s[8:9]
	ds_bpermute_b32 v13, v9, v7
	s_waitcnt lgkmcnt(0)
	v_add_f32_e32 v13, v7, v13
	v_cndmask_b32_e64 v7, v13, v7, s[10:11]
	ds_bpermute_b32 v13, v8, v7
	s_waitcnt lgkmcnt(0)
	v_add_f32_e32 v13, v7, v13
	v_cndmask_b32_e64 v7, v13, v7, s[12:13]
	ds_bpermute_b32 v13, v3, v7
	s_waitcnt lgkmcnt(0)
	v_add_f32_e32 v13, v7, v13
	v_cndmask_b32_e64 v13, v13, v7, s[14:15]
	v_sub_f32_e32 v7, v13, v17
	s_waitcnt vmcnt(0)
	v_sub_f32_e32 v15, v19, v13
	v_sub_f32_e32 v21, v18, v7
	v_max_f32_e32 v20, v21, v15
	ds_bpermute_b32 v22, v12, v20
	s_waitcnt lgkmcnt(0)
	v_max_f32_e32 v22, v22, v22
	v_max_f32_e32 v22, v20, v22
	v_cndmask_b32_e64 v20, v22, v20, s[2:3]
	ds_bpermute_b32 v22, v11, v20
	s_waitcnt lgkmcnt(0)
	v_max_f32_e32 v22, v22, v22
	v_max_f32_e32 v22, v20, v22
	v_cndmask_b32_e64 v20, v22, v20, s[6:7]
	ds_bpermute_b32 v22, v10, v20
	s_waitcnt lgkmcnt(0)
	v_max_f32_e32 v22, v22, v22
	v_max_f32_e32 v22, v20, v22
	v_cndmask_b32_e64 v20, v22, v20, s[8:9]
	ds_bpermute_b32 v22, v9, v20
	s_waitcnt lgkmcnt(0)
	v_max_f32_e32 v22, v22, v22
	v_max_f32_e32 v22, v20, v22
	v_cndmask_b32_e64 v20, v22, v20, s[10:11]
	ds_bpermute_b32 v22, v8, v20
	s_waitcnt lgkmcnt(0)
	v_max_f32_e32 v22, v22, v22
	v_max_f32_e32 v22, v20, v22
	v_cndmask_b32_e64 v20, v22, v20, s[12:13]
	ds_bpermute_b32 v22, v3, v20
	v_max_f32_e32 v6, v20, v20
	s_waitcnt lgkmcnt(0)
	v_max_f32_e32 v22, v22, v22
	v_max_f32_e32 v6, v6, v22
	v_cndmask_b32_e64 v6, v6, v20, s[14:15]
	ds_bpermute_b32 v20, v12, v6
	v_sub_f32_e32 v6, v7, v16
	s_waitcnt lgkmcnt(0)
	v_max_f32_e32 v20, v20, v20
	v_max_f32_e32 v20, 0, v20
	v_cndmask_b32_e64 v20, v20, 0, s[2:3]
	v_max_f32_e32 v21, v20, v21
	v_max_f32_e32 v15, v21, v15
	v_pk_add_f32 v[6:7], v[20:21], v[6:7]
	v_add_f32_e32 v13, v13, v15
	v_pk_add_f32 v[16:17], v[16:17], v[6:7]
	v_sub_f32_e32 v15, v18, v7
	v_sub_f32_e32 v18, v16, v7
	v_mul_f32_e32 v16, 0x3fb8aa3b, v15
	v_sub_f32_e32 v17, v17, v13
	v_sub_f32_e32 v13, v19, v13
	v_mul_f32_e32 v19, 0x3fb8aa3b, v18
	v_fma_f32 v20, v15, s0, -v16
	v_rndne_f32_e32 v21, v16
	v_fma_f32 v27, v18, s0, -v19
	v_rndne_f32_e32 v28, v19
	v_fmac_f32_e32 v20, 0x32a5705f, v15
	v_sub_f32_e32 v16, v16, v21
	v_mul_f32_e32 v22, 0x3fb8aa3b, v17
	v_fmac_f32_e32 v27, 0x32a5705f, v18
	v_sub_f32_e32 v19, v19, v28
	v_add_f32_e32 v16, v16, v20
	v_mul_f32_e32 v26, 0x3fb8aa3b, v13
	v_cvt_i32_f32_e32 v21, v21
	v_fma_f32 v29, v17, s0, -v22
	v_rndne_f32_e32 v30, v22
	v_add_f32_e32 v19, v19, v27
	v_exp_f32_e32 v16, v16
	v_fma_f32 v31, v13, s0, -v26
	v_rndne_f32_e32 v32, v26
	v_cvt_i32_f32_e32 v28, v28
	v_fmac_f32_e32 v29, 0x32a5705f, v17
	v_sub_f32_e32 v20, v22, v30
	v_exp_f32_e32 v19, v19
	v_fmac_f32_e32 v31, 0x32a5705f, v13
	v_sub_f32_e32 v26, v26, v32
	v_add_f32_e32 v20, v20, v29
	v_cvt_i32_f32_e32 v22, v30
	v_add_f32_e32 v26, v26, v31
	v_exp_f32_e32 v20, v20
	v_cvt_i32_f32_e32 v30, v32
	v_exp_f32_e32 v26, v26
	v_ldexp_f32 v16, v16, v21
	v_cmp_ngt_f32_e32 vcc, s1, v15
	v_ldexp_f32 v19, v19, v28
	v_ldexp_f32 v20, v20, v22
	v_cndmask_b32_e32 v16, 0, v16, vcc
	v_cmp_ngt_f32_e32 vcc, s1, v18
	v_ldexp_f32 v21, v26, v30
	s_nop 0
	v_cndmask_b32_e32 v19, 0, v19, vcc
	v_cmp_nlt_f32_e32 vcc, s4, v15
	s_nop 1
	v_cndmask_b32_e32 v16, v23, v16, vcc
	v_cmp_ngt_f32_e32 vcc, s1, v17
	s_nop 1
	v_cndmask_b32_e32 v15, 0, v20, vcc
	v_cmp_ngt_f32_e32 vcc, s1, v13
	s_nop 1
	v_cndmask_b32_e32 v20, 0, v21, vcc
	v_cmp_nlt_f32_e32 vcc, s4, v18
	s_nop 1
	v_cndmask_b32_e32 v18, v23, v19, vcc
	v_cmp_nlt_f32_e32 vcc, s4, v17
	s_nop 1
	v_cndmask_b32_e32 v19, v23, v15, vcc
	v_cmp_nlt_f32_e32 vcc, s4, v13
	s_nop 1
	v_cndmask_b32_e32 v17, v23, v20, vcc
	ds_write_b64 v24, v[18:19]
	ds_write_b64 v25, v[16:17]
	s_cbranch_scc1 .LBB0_534
	v_lshl_add_u64 v[16:17], v[4:5], 2, s[88:89]
	v_add_co_u32_e32 v16, vcc, 0xb03000, v16
	s_nop 1
	v_addc_co_u32_e32 v17, vcc, 0, v17, vcc
	global_store_dwordx2 v[16:17], v[6:7], off

; __device__ __forceinline__ void ph5_m2(const Frame& F, const Args& A) {
;     ...
;     for (int task0 = F.vcu; task0 < NT_C; task0 += 2 * F.G) {
;         const bool hasB = task0 + F.G < NT_C;
;         const int ttA = task0, ttB = hasB ? task0 + F.G : task0;
;         const int hA = ttA >> 6, rA = (ttA * 128 + 2 * l) & 8191, jA = ttA & 63, hB = ttB >> 6, rB = (ttB * 128 + 2 * l) & 8191, jB = ttB & 63;
;         const bf16* srcA = U + (size_t)hA * 128 * 8192 + rA; const bf16* srcB = U + (size_t)hB * 128 * 8192 + rB;
;         const float* snA = UN + (size_t)hA * 128 * 64 + jA; const float* snB = UN + (size_t)hB * 128 * 64 + jB;
;         f32x2_t uA[16], uB[16]; float nA[16], nB[16];
; #pragma unroll
;         for (int i = 0; i < 16; ++i) { const unsigned wa = *(const unsigned*)(srcA + (size_t)(16 * g + i) * 8192), wb = *(const unsigned*)(srcB + (size_t)(16 * g + i) * 8192);
;             uA[i] = (f32x2_t){bflo(wa), bfhi(wa)}; uB[i] = (f32x2_t){bflo(wb), bfhi(wb)};
;             nA[i] = snA[(16 * g + i) * 64]; nB[i] = snB[(16 * g + i) * 64]; }
.LBB0_583:
	v_readlane_b32 s4, v254, 49
	s_add_i32 s6, s89, s4
	s_cmpk_lt_i32 s6, 0x200
	s_cselect_b64 s[50:51], -1, 0
	s_and_b64 s[4:5], s[50:51], exec
	s_cselect_b32 s5, s6, s89
	s_ashr_i32 s4, s89, 6
	s_lshl_b32 s6, s89, 7
	s_lshl_b32 s8, s5, 7
	s_and_b32 s6, s6, 0x1f80
	s_ashr_i32 s92, s5, 6
	s_and_b32 s8, s8, 0x1f80
	s_and_b32 s11, s5, 63
	s_ashr_i32 s5, s4, 31
	v_or_b32_e32 v2, s6, v75
	s_and_b32 s6, s89, 63
	v_or_b32_e32 v4, s8, v75
	s_lshl_b64 s[8:9], s[4:5], 21
	v_readlane_b32 s10, v255, 7
	s_add_u32 s8, s10, s8
	v_readlane_b32 s12, v255, 9
	s_addc_u32 s9, s12, s9
	v_lshlrev_b32_e32 v2, 1, v2
	s_ashr_i32 s93, s92, 31
	v_lshl_add_u64 v[66:67], s[8:9], 0, v[2:3]
	s_lshl_b64 s[8:9], s[92:93], 21
	s_add_u32 s8, s10, s8
	s_addc_u32 s9, s12, s9
	v_lshlrev_b32_e32 v62, 1, v4
	v_mov_b32_e32 v63, v3
	v_lshl_add_u64 v[68:69], s[8:9], 0, v[62:63]
	s_lshl_b64 s[8:9], s[4:5], 15
	v_readlane_b32 s14, v255, 11
	s_add_u32 s8, s14, s8
	v_readlane_b32 s15, v255, 13
	s_addc_u32 s10, s15, s9
	s_lshl_b32 s44, s6, 2
	s_add_u32 s9, s8, s44
	s_addc_u32 s10, s10, 0
	s_lshl_b64 s[12:13], s[92:93], 15
	s_add_u32 s6, s14, s12
	s_addc_u32 s8, s15, s13
	s_lshl_b32 s56, s11, 2
	v_readlane_b32 s12, v254, 52
	s_add_u32 s6, s6, s56
	v_readlane_b32 s13, v254, 53
	s_addc_u32 s8, s8, 0
	s_lshl_b64 s[12:13], s[12:13], 1
	s_mov_b32 s98, 0x4000
	s_mov_b32 s99, 0
	v_lshl_add_u64 v[166:167], v[66:67], 0, s[12:13]
	v_lshl_add_u64 v[168:169], v[68:69], 0, s[12:13]
	global_load_dword v134, v[166:167], off
	global_load_dword v135, v[168:169], off
	v_lshl_add_u64 v[166:167], v[166:167], 0, s[98:99]
	v_lshl_add_u64 v[168:169], v[168:169], 0, s[98:99]
	global_load_dword v136, v[166:167], off
	global_load_dword v137, v[168:169], off
	v_lshl_add_u64 v[166:167], v[166:167], 0, s[98:99]
	v_lshl_add_u64 v[168:169], v[168:169], 0, s[98:99]
	global_load_dword v138, v[166:167], off
	global_load_dword v139, v[168:169], off
	v_lshl_add_u64 v[166:167], v[166:167], 0, s[98:99]
	v_lshl_add_u64 v[168:169], v[168:169], 0, s[98:99]
	global_load_dword v140, v[166:167], off
	global_load_dword v141, v[168:169], off
	v_lshl_add_u64 v[166:167], v[166:167], 0, s[98:99]
	v_lshl_add_u64 v[168:169], v[168:169], 0, s[98:99]
	global_load_dword v142, v[166:167], off
	global_load_dword v143, v[168:169], off
	v_lshl_add_u64 v[166:167], v[166:167], 0, s[98:99]
	v_lshl_add_u64 v[168:169], v[168:169], 0, s[98:99]
	global_load_dword v144, v[166:167], off
	global_load_dword v145, v[168:169], off
	v_lshl_add_u64 v[166:167], v[166:167], 0, s[98:99]
	v_lshl_add_u64 v[168:169], v[168:169], 0, s[98:99]
	global_load_dword v146, v[166:167], off
	global_load_dword v147, v[168:169], off
	v_lshl_add_u64 v[166:167], v[166:167], 0, s[98:99]
	v_lshl_add_u64 v[168:169], v[168:169], 0, s[98:99]
	global_load_dword v148, v[166:167], off
	global_load_dword v149, v[168:169], off
	v_lshl_add_u64 v[166:167], v[166:167], 0, s[98:99]
	v_lshl_add_u64 v[168:169], v[168:169], 0, s[98:99]
	global_load_dword v150, v[166:167], off
	global_load_dword v151, v[168:169], off
	v_lshl_add_u64 v[166:167], v[166:167], 0, s[98:99]
	v_lshl_add_u64 v[168:169], v[168:169], 0, s[98:99]
	global_load_dword v152, v[166:167], off
	global_load_dword v153, v[168:169], off
	v_lshl_add_u64 v[166:167], v[166:167], 0, s[98:99]
	v_lshl_add_u64 v[168:169], v[168:169], 0, s[98:99]
	global_load_dword v154, v[166:167], off
	global_load_dword v155, v[168:169], off
	v_lshl_add_u64 v[166:167], v[166:167], 0, s[98:99]
	v_lshl_add_u64 v[168:169], v[168:169], 0, s[98:99]
	global_load_dword v156, v[166:167], off
	global_load_dword v157, v[168:169], off
	v_lshl_add_u64 v[166:167], v[166:167], 0, s[98:99]
	v_lshl_add_u64 v[168:169], v[168:169], 0, s[98:99]
	global_load_dword v158, v[166:167], off
	global_load_dword v159, v[168:169], off
	v_lshl_add_u64 v[166:167], v[166:167], 0, s[98:99]
	v_lshl_add_u64 v[168:169], v[168:169], 0, s[98:99]
	global_load_dword v160, v[166:167], off
	global_load_dword v161, v[168:169], off
	v_lshl_add_u64 v[166:167], v[166:167], 0, s[98:99]
	v_lshl_add_u64 v[168:169], v[168:169], 0, s[98:99]
	global_load_dword v162, v[166:167], off
	global_load_dword v163, v[168:169], off
	v_lshl_add_u64 v[166:167], v[166:167], 0, s[98:99]
	v_lshl_add_u64 v[168:169], v[168:169], 0, s[98:99]
	global_load_dword v164, v[166:167], off
	global_load_dword v165, v[168:169], off
	s_waitcnt vmcnt(0)
; __device__ __forceinline__ void ph5_m2(const Frame& F, const Args& A) {
;     ...
;         f32x2_t uA[16], uB[16]; float nA[16], nB[16];
; #pragma unroll
;         for (int i = 0; i < 16; ++i) { const unsigned wa = *(const unsigned*)(srcA + (size_t)(16 * g + i) * 8192), wb = *(const unsigned*)(srcB + (size_t)(16 * g + i) * 8192);
;             uA[i] = (f32x2_t){bflo(wa), bfhi(wa)}; uB[i] = (f32x2_t){bflo(wb), bfhi(wb)};
;             nA[i] = snA[(16 * g + i) * 64]; nB[i] = snB[(16 * g + i) * 64]; }
;         float ApA = 1.f, ApB = 1.f, BnA = 0.f, BnB = 0.f; f32x2_t BpA = {0.f, 0.f}, BpB = {0.f, 0.f};
; #pragma unroll
;         for (int i = 0; i < 16; ++i) { const float dA = decL[hA * 128 + 16 * g + i], sA = sclL[hA * 128 + 16 * g + i], dB = decL[hB * 128 + 16 * g + i], sB = sclL[hB * 128 + 16 * g + i];
;             ApA *= dA; BpA = BpA * dA + uA[i] * sA; BnA = BnA * dA + nA[i] * sA; ApB *= dB; BpB = BpB * dB + uB[i] * sB; BnB = BnB * dB + nB[i] * sB; }
	v_lshl_add_u64 v[4:5], v[66:67], 0, s[12:13]
	v_mov_b32_e32 v6, v134
	v_lshl_add_u64 v[4:5], v[68:69], 0, s[12:13]
	v_mov_b32_e32 v4, v135
	s_add_u32 s12, s9, s48
	s_addc_u32 s13, s10, s49
	global_load_dword v82, v3, s[12:13]
	s_add_u32 s12, s6, s48
	s_addc_u32 s13, s8, s49
	global_load_dword v113, v3, s[12:13]
	v_readlane_b32 s12, v254, 54
	v_readlane_b32 s13, v254, 55
	s_lshl_b64 s[12:13], s[12:13], 1
	s_mov_b64 s[24:25], s[18:19]
	s_mov_b64 s[22:23], s[20:21]
	v_readlane_b32 s16, v255, 15
	v_readlane_b32 s17, v255, 16
	v_lshlrev_b32_e32 v64, 16, v6
	v_and_b32_e32 v65, 0xffff0000, v6
	v_lshlrev_b32_e32 v58, 16, v4
	v_and_b32_e32 v59, 0xffff0000, v4
	v_lshl_add_u64 v[4:5], v[66:67], 0, s[12:13]
	v_mov_b32_e32 v6, v136
	v_lshl_add_u64 v[4:5], v[68:69], 0, s[12:13]
	v_mov_b32_e32 v4, v137
	s_add_u32 s12, s9, s52
	s_addc_u32 s13, s10, s53
	global_load_dword v114, v3, s[12:13]
	s_add_u32 s12, s6, s52
	s_addc_u32 s13, s8, s53
	global_load_dword v111, v3, s[12:13]
	v_readlane_b32 s12, v254, 56
	v_readlane_b32 s13, v254, 57
	s_lshl_b64 s[12:13], s[12:13], 1
	v_lshlrev_b32_e32 v60, 16, v6
	v_and_b32_e32 v61, 0xffff0000, v6
	v_lshlrev_b32_e32 v54, 16, v4
	v_and_b32_e32 v55, 0xffff0000, v4
	v_lshl_add_u64 v[4:5], v[66:67], 0, s[12:13]
	v_mov_b32_e32 v6, v138
	v_lshl_add_u64 v[4:5], v[68:69], 0, s[12:13]
	v_mov_b32_e32 v4, v139
	s_add_u32 s12, s9, s54
	s_addc_u32 s13, s10, s55
	global_load_dword v112, v3, s[12:13]
	s_add_u32 s12, s6, s54
	s_addc_u32 s13, s8, s55
	global_load_dword v109, v3, s[12:13]
	s_lshl_b64 s[12:13], s[20:21], 1
	v_lshlrev_b32_e32 v56, 16, v6
	v_and_b32_e32 v57, 0xffff0000, v6
	v_lshlrev_b32_e32 v50, 16, v4
	v_and_b32_e32 v51, 0xffff0000, v4
	v_lshl_add_u64 v[4:5], v[66:67], 0, s[12:13]
	v_mov_b32_e32 v6, v140
	v_lshl_add_u64 v[4:5], v[68:69], 0, s[12:13]
	v_mov_b32_e32 v4, v141
	s_add_u32 s12, s9, s58
	s_addc_u32 s13, s10, s59
	global_load_dword v110, v3, s[12:13]
	s_add_u32 s12, s6, s58
	s_addc_u32 s13, s8, s59
	global_load_dword v107, v3, s[12:13]
	s_lshl_b64 s[12:13], s[18:19], 1
	v_lshlrev_b32_e32 v52, 16, v6
	v_and_b32_e32 v53, 0xffff0000, v6
	v_lshlrev_b32_e32 v46, 16, v4
	v_and_b32_e32 v47, 0xffff0000, v4
	v_lshl_add_u64 v[4:5], v[66:67], 0, s[12:13]
	v_mov_b32_e32 v6, v142
	v_lshl_add_u64 v[4:5], v[68:69], 0, s[12:13]
	v_mov_b32_e32 v4, v143
	s_add_u32 s12, s9, s60
	s_addc_u32 s13, s10, s61
	global_load_dword v108, v3, s[12:13]
	s_add_u32 s12, s6, s60
	s_addc_u32 s13, s8, s61
	global_load_dword v105, v3, s[12:13]
	v_readlane_b32 s12, v254, 58
	v_readlane_b32 s13, v254, 59
	s_lshl_b64 s[12:13], s[12:13], 1
	v_lshlrev_b32_e32 v48, 16, v6
	v_and_b32_e32 v49, 0xffff0000, v6
	v_lshlrev_b32_e32 v42, 16, v4
	v_and_b32_e32 v43, 0xffff0000, v4
	v_lshl_add_u64 v[4:5], v[66:67], 0, s[12:13]
	v_mov_b32_e32 v6, v144
	v_lshl_add_u64 v[4:5], v[68:69], 0, s[12:13]
	v_mov_b32_e32 v4, v145
	s_add_u32 s12, s9, s62
	s_addc_u32 s13, s10, s63
	global_load_dword v106, v3, s[12:13]
	s_add_u32 s12, s6, s62
	s_addc_u32 s13, s8, s63
	global_load_dword v103, v3, s[12:13]
	v_readlane_b32 s12, v254, 60
	v_readlane_b32 s13, v254, 61
	s_lshl_b64 s[12:13], s[12:13], 1
	v_lshlrev_b32_e32 v44, 16, v6
	v_and_b32_e32 v45, 0xffff0000, v6
	v_lshlrev_b32_e32 v38, 16, v4
	v_and_b32_e32 v39, 0xffff0000, v4
	v_lshl_add_u64 v[4:5], v[66:67], 0, s[12:13]
	v_mov_b32_e32 v6, v146
	v_lshl_add_u64 v[4:5], v[68:69], 0, s[12:13]
	v_mov_b32_e32 v4, v147
	s_add_u32 s12, s9, s64
	s_addc_u32 s13, s10, s65
	global_load_dword v104, v3, s[12:13]
	s_add_u32 s12, s6, s64
	s_addc_u32 s13, s8, s65
	global_load_dword v101, v3, s[12:13]
	v_readlane_b32 s12, v254, 62
	v_readlane_b32 s13, v254, 63
	s_lshl_b64 s[12:13], s[12:13], 1
	v_lshlrev_b32_e32 v40, 16, v6
	v_and_b32_e32 v41, 0xffff0000, v6
	v_lshlrev_b32_e32 v34, 16, v4
	v_and_b32_e32 v35, 0xffff0000, v4
	v_lshl_add_u64 v[4:5], v[66:67], 0, s[12:13]
	v_mov_b32_e32 v6, v148
	v_lshl_add_u64 v[4:5], v[68:69], 0, s[12:13]
	v_mov_b32_e32 v4, v149
	s_add_u32 s12, s9, s66
	s_addc_u32 s13, s10, s67
	global_load_dword v102, v3, s[12:13]
	s_add_u32 s12, s6, s66
	s_addc_u32 s13, s8, s67
	global_load_dword v99, v3, s[12:13]
	s_lshl_b64 s[12:13], s[26:27], 1
	v_lshlrev_b32_e32 v36, 16, v6
	v_and_b32_e32 v37, 0xffff0000, v6
	v_lshlrev_b32_e32 v30, 16, v4
	v_and_b32_e32 v31, 0xffff0000, v4
	v_lshl_add_u64 v[4:5], v[66:67], 0, s[12:13]
	v_mov_b32_e32 v6, v150
	v_lshl_add_u64 v[4:5], v[68:69], 0, s[12:13]
	v_mov_b32_e32 v4, v151
	s_add_u32 s12, s9, s68
	s_addc_u32 s13, s10, s69
	global_load_dword v100, v3, s[12:13]
	s_add_u32 s12, s6, s68
	s_addc_u32 s13, s8, s69
	global_load_dword v97, v3, s[12:13]
	s_lshl_b64 s[12:13], s[28:29], 1
	v_lshlrev_b32_e32 v32, 16, v6
	v_and_b32_e32 v33, 0xffff0000, v6
	v_lshlrev_b32_e32 v26, 16, v4
	v_and_b32_e32 v27, 0xffff0000, v4
	v_lshl_add_u64 v[4:5], v[66:67], 0, s[12:13]
	v_mov_b32_e32 v6, v152
	v_lshl_add_u64 v[4:5], v[68:69], 0, s[12:13]
	v_mov_b32_e32 v4, v153
	s_add_u32 s12, s9, s72
	s_addc_u32 s13, s10, s73
	global_load_dword v98, v3, s[12:13]
	s_add_u32 s12, s6, s72
	s_addc_u32 s13, s8, s73
	global_load_dword v95, v3, s[12:13]
	s_lshl_b64 s[12:13], s[30:31], 1
	v_lshlrev_b32_e32 v28, 16, v6
	v_and_b32_e32 v29, 0xffff0000, v6
	v_lshlrev_b32_e32 v22, 16, v4
	v_and_b32_e32 v23, 0xffff0000, v4
	v_lshl_add_u64 v[4:5], v[66:67], 0, s[12:13]
	v_mov_b32_e32 v6, v154
	v_lshl_add_u64 v[4:5], v[68:69], 0, s[12:13]
	v_mov_b32_e32 v4, v155
	s_add_u32 s12, s9, s76
	s_addc_u32 s13, s10, s77
	global_load_dword v96, v3, s[12:13]
	s_add_u32 s12, s6, s76
	s_addc_u32 s13, s8, s77
	global_load_dword v93, v3, s[12:13]
	s_lshl_b64 s[12:13], s[34:35], 1
	v_lshlrev_b32_e32 v24, 16, v6
	v_and_b32_e32 v25, 0xffff0000, v6
; __device__ __forceinline__ void ph5_m2(const Frame& F, const Args& A) {
;     ...
;         for (int i = 0; i < 16; ++i) { const unsigned wa = *(const unsigned*)(srcA + (size_t)(16 * g + i) * 8192), wb = *(const unsigned*)(srcB + (size_t)(16 * g + i) * 8192);
;             uA[i] = (f32x2_t){bflo(wa), bfhi(wa)}; uB[i] = (f32x2_t){bflo(wb), bfhi(wb)};
;             nA[i] = snA[(16 * g + i) * 64]; nB[i] = snB[(16 * g + i) * 64]; }
;         float ApA = 1.f, ApB = 1.f, BnA = 0.f, BnB = 0.f; f32x2_t BpA = {0.f, 0.f}, BpB = {0.f, 0.f};
; #pragma unroll
;         for (int i = 0; i < 16; ++i) { const float dA = decL[hA * 128 + 16 * g + i], sA = sclL[hA * 128 + 16 * g + i], dB = decL[hB * 128 + 16 * g + i], sB = sclL[hB * 128 + 16 * g + i];
;             ApA *= dA; BpA = BpA * dA + uA[i] * sA; BnA = BnA * dA + nA[i] * sA; ApB *= dB; BpB = BpB * dB + uB[i] * sB; BnB = BnB * dB + nB[i] * sB; }
	v_lshlrev_b32_e32 v18, 16, v4
	v_and_b32_e32 v19, 0xffff0000, v4
	v_lshl_add_u64 v[4:5], v[66:67], 0, s[12:13]
	v_mov_b32_e32 v6, v156
	v_lshl_add_u64 v[4:5], v[68:69], 0, s[12:13]
	v_mov_b32_e32 v4, v157
	s_add_u32 s12, s9, s80
	s_addc_u32 s13, s10, s81
	global_load_dword v94, v3, s[12:13]
	s_add_u32 s12, s6, s80
	s_addc_u32 s13, s8, s81
	global_load_dword v91, v3, s[12:13]
	s_lshl_b64 s[12:13], s[36:37], 1
	v_lshlrev_b32_e32 v20, 16, v6
	v_and_b32_e32 v21, 0xffff0000, v6
	v_lshlrev_b32_e32 v14, 16, v4
	v_and_b32_e32 v15, 0xffff0000, v4
	v_lshl_add_u64 v[4:5], v[66:67], 0, s[12:13]
	v_mov_b32_e32 v6, v158
	v_lshl_add_u64 v[4:5], v[68:69], 0, s[12:13]
	v_mov_b32_e32 v4, v159
	s_add_u32 s12, s9, s96
	s_addc_u32 s13, s10, s97
	global_load_dword v92, v3, s[12:13]
	s_add_u32 s12, s6, s96
	s_addc_u32 s13, s8, s97
	global_load_dword v89, v3, s[12:13]
	s_lshl_b64 s[12:13], s[38:39], 1
	v_lshlrev_b32_e32 v16, 16, v6
	v_and_b32_e32 v17, 0xffff0000, v6
	v_lshlrev_b32_e32 v10, 16, v4
	v_and_b32_e32 v11, 0xffff0000, v4
	v_lshl_add_u64 v[4:5], v[66:67], 0, s[12:13]
	v_mov_b32_e32 v6, v160
	v_lshl_add_u64 v[4:5], v[68:69], 0, s[12:13]
	v_mov_b32_e32 v4, v161
	s_add_u32 s12, s9, s84
	s_addc_u32 s13, s10, s85
	global_load_dword v90, v3, s[12:13]
	s_add_u32 s12, s6, s84
	s_addc_u32 s13, s8, s85
	global_load_dword v88, v3, s[12:13]
	s_lshl_b64 s[12:13], s[40:41], 1
	v_lshlrev_b32_e32 v12, 16, v6
	v_and_b32_e32 v13, 0xffff0000, v6
	v_lshlrev_b32_e32 v6, 16, v4
	v_and_b32_e32 v7, 0xffff0000, v4
	v_lshl_add_u64 v[4:5], v[66:67], 0, s[12:13]
	v_mov_b32_e32 v9, v162
	v_lshl_add_u64 v[4:5], v[68:69], 0, s[12:13]
	s_add_u32 s12, s9, s86
	s_addc_u32 s13, s10, s87
	v_mov_b32_e32 v5, v163
	v_lshlrev_b32_e32 v8, 16, v9
	global_load_dword v87, v3, s[12:13]
	s_add_u32 s12, s6, s86
	s_addc_u32 s13, s8, s87
	global_load_dword v86, v3, s[12:13]
	s_lshl_b64 s[12:13], s[42:43], 1
	v_lshl_add_u64 v[66:67], v[66:67], 0, s[12:13]
	v_mov_b32_e32 v63, v164
	v_lshl_add_u64 v[66:67], v[68:69], 0, s[12:13]
	s_add_u32 s12, s9, s94
	s_addc_u32 s13, s10, s95
	v_mov_b32_e32 v67, v165
	s_add_u32 s10, s6, s94
	s_addc_u32 s11, s8, s95
	global_load_dword v78, v3, s[10:11]
	s_lshl_b32 s6, s4, 7
	s_add_i32 s6, s6, s0
	s_lshl_b32 s8, s92, 7
	s_lshl_b32 s57, s6, 2
	s_add_i32 s8, s8, s0
	s_add_i32 s18, s1, s57
	v_mov_b32_e32 v70, s18
	s_add_i32 s19, s88, s57
	s_lshl_b32 s45, s8, 2
	ds_read_b128 v[70:73], v70
	v_mov_b32_e32 v74, s19
	s_add_i32 s20, s1, s45
	ds_read_b128 v[116:119], v74
	v_mov_b32_e32 v74, s20
	s_add_i32 s21, s88, s45
	ds_read_b128 v[120:123], v74
	v_mov_b32_e32 v74, s21
	ds_read_b128 v[124:127], v74
	s_waitcnt lgkmcnt(3)
	v_mul_f32_e32 v74, 0, v70
	s_waitcnt lgkmcnt(2)
	v_pk_fma_f32 v[80:81], v[116:117], v[64:65], v[74:75] op_sel_hi:[0,1,0]
	v_pk_mul_f32 v[130:131], v[116:117], v[60:61] op_sel:[1,0]
	s_waitcnt vmcnt(16)
	v_fmac_f32_e32 v74, v82, v116
	s_waitcnt lgkmcnt(1)
	v_mul_f32_e32 v76, 0, v120
	v_pk_fma_f32 v[80:81], v[80:81], v[70:71], v[130:131] op_sel:[0,1,0]
	v_mul_f32_e32 v130, v114, v117
	s_waitcnt lgkmcnt(0)
	v_pk_fma_f32 v[128:129], v[124:125], v[58:59], v[76:77] op_sel_hi:[0,1,0]
	v_mul_f32_e32 v115, v70, v71
	v_fmac_f32_e32 v130, v74, v71
	v_pk_mul_f32 v[70:71], v[124:125], v[54:55] op_sel:[1,0]
	v_fmac_f32_e32 v76, v113, v124
	v_mul_f32_e32 v74, v120, v121
	v_pk_fma_f32 v[70:71], v[128:129], v[120:121], v[70:71] op_sel:[0,1,0]
	v_mul_f32_e32 v120, v111, v125
	v_pk_mul_f32 v[116:117], v[118:119], v[56:57] op_sel_hi:[0,1]
	v_fmac_f32_e32 v120, v76, v121
	v_mul_f32_e32 v76, v115, v72
	v_pk_fma_f32 v[80:81], v[80:81], v[72:73], v[116:117] op_sel_hi:[1,0,1]
	v_mul_f32_e32 v115, v112, v118
	v_mul_f32_e32 v118, v74, v122
	v_pk_mul_f32 v[116:117], v[126:127], v[50:51] op_sel_hi:[0,1]
	v_mov_b32_e32 v74, v119
	v_fmac_f32_e32 v115, v130, v72
	v_pk_fma_f32 v[70:71], v[70:71], v[122:123], v[116:117] op_sel_hi:[1,0,1]
	v_mov_b32_e32 v72, v73
	v_pk_mul_f32 v[116:117], v[74:75], v[52:53] op_sel_hi:[0,1]
	v_mov_b32_e32 v74, v127
	s_or_b32 s6, s57, 16
	v_pk_fma_f32 v[80:81], v[80:81], v[72:73], v[116:117] op_sel_hi:[1,0,1]
	v_mov_b32_e32 v72, v123
	v_pk_mul_f32 v[116:117], v[74:75], v[46:47] op_sel_hi:[0,1]
	v_mul_f32_e32 v121, v109, v126
	v_mul_f32_e32 v132, v110, v119
	v_pk_fma_f32 v[128:129], v[70:71], v[72:73], v[116:117] op_sel_hi:[1,0,1]
	v_fmac_f32_e32 v121, v120, v122
	v_mul_f32_e32 v76, v76, v73
	v_fmac_f32_e32 v132, v115, v73
	v_mul_f32_e32 v115, v118, v123
	v_mul_f32_e32 v74, v107, v127
	v_fmac_f32_e32 v74, v121, v123
	v_and_b32_e32 v9, 0xffff0000, v9
	s_waitcnt vmcnt(5)
	v_lshlrev_b32_e32 v4, 16, v5
	v_and_b32_e32 v5, 0xffff0000, v5
	s_andn2_b64 vcc, exec, s[16:17]
	s_waitcnt vmcnt(2)
	v_lshlrev_b32_e32 v68, 16, v63
	v_and_b32_e32 v69, 0xffff0000, v63
	global_load_dword v63, v3, s[12:13]
	s_add_i32 s12, s1, s6
	s_add_i32 s13, s88, s6
	s_or_b32 s6, s45, 16
	v_mov_b32_e32 v70, s12
	v_mov_b32_e32 v116, s13
	s_add_i32 s14, s1, s6
	s_add_i32 s15, s88, s6
	ds_read_b128 v[70:73], v70
	ds_read_b128 v[116:119], v116
	v_mov_b32_e32 v120, s14
	v_mov_b32_e32 v124, s15
	ds_read_b128 v[120:123], v120
	ds_read_b128 v[124:127], v124
	s_waitcnt lgkmcnt(2)
	v_pk_mul_f32 v[130:131], v[116:117], v[48:49] op_sel_hi:[0,1]
	v_mul_f32_e32 v133, v108, v116
	v_mul_f32_e32 v76, v76, v70
	v_pk_fma_f32 v[80:81], v[80:81], v[70:71], v[130:131] op_sel_hi:[1,0,1]
	v_fmac_f32_e32 v133, v132, v70
	s_waitcnt lgkmcnt(0)
; __device__ __forceinline__ void ph5_m2(const Frame& F, const Args& A) {
;     ...
; #pragma unroll
;         for (int i = 0; i < 16; ++i) { const float dA = decL[hA * 128 + 16 * g + i], sA = sclL[hA * 128 + 16 * g + i], dB = decL[hB * 128 + 16 * g + i], sB = sclL[hB * 128 + 16 * g + i];
;             ApA *= dA; BpA = BpA * dA + uA[i] * sA; BnA = BnA * dA + nA[i] * sA; ApB *= dB; BpB = BpB * dB + uB[i] * sB; BnB = BnB * dB + nB[i] * sB; }
;         seg[g * 128 + 2 * l] = ApA; seg[1024 + g * 128 + 2 * l] = BpA.x; seg[1024 + g * 128 + 2 * l + 1] = BpA.y; seg[2048 + g * 64 + l] = BnA;
;         seg[3072 + g * 128 + 2 * l] = ApB; seg[3072 + 1024 + g * 128 + 2 * l] = BpB.x; seg[3072 + 1024 + g * 128 + 2 * l + 1] = BpB.y; seg[3072 + 2048 + g * 64 + l] = BnB;
;         __syncthreads();
	v_pk_mul_f32 v[130:131], v[124:125], v[42:43] op_sel_hi:[0,1]
	v_mul_f32_e32 v132, v105, v124
	v_pk_fma_f32 v[128:129], v[128:129], v[120:121], v[130:131] op_sel_hi:[1,0,1]
	v_fmac_f32_e32 v132, v74, v120
	v_mul_f32_e32 v74, v76, v71
	v_pk_mul_f32 v[130:131], v[116:117], v[44:45] op_sel:[1,0]
	v_mul_f32_e32 v76, v106, v117
	v_mul_f32_e32 v115, v115, v120
	v_pk_fma_f32 v[80:81], v[80:81], v[70:71], v[130:131] op_sel:[0,1,0]
	v_fmac_f32_e32 v76, v133, v71
	v_pk_mul_f32 v[70:71], v[124:125], v[38:39] op_sel:[1,0]
	v_mul_f32_e32 v74, v74, v72
	v_pk_mul_f32 v[116:117], v[118:119], v[40:41] op_sel_hi:[0,1]
	v_mul_f32_e32 v115, v115, v121
	v_pk_fma_f32 v[70:71], v[128:129], v[120:121], v[70:71] op_sel:[0,1,0]
	v_mul_f32_e32 v120, v103, v125
	v_pk_fma_f32 v[80:81], v[80:81], v[72:73], v[116:117] op_sel_hi:[1,0,1]
	v_mul_f32_e32 v118, v104, v118
	v_pk_mul_f32 v[116:117], v[126:127], v[34:35] op_sel_hi:[0,1]
	v_mul_f32_e32 v130, v74, v73
	v_mov_b32_e32 v74, v119
	v_fmac_f32_e32 v120, v132, v121
	v_fmac_f32_e32 v118, v76, v72
	v_mul_f32_e32 v76, v115, v122
	v_pk_fma_f32 v[70:71], v[70:71], v[122:123], v[116:117] op_sel_hi:[1,0,1]
	v_mul_f32_e32 v115, v101, v126
	v_mov_b32_e32 v72, v73
	v_pk_mul_f32 v[116:117], v[74:75], v[36:37] op_sel_hi:[0,1]
	v_mov_b32_e32 v74, v127
	s_or_b32 s6, s57, 32
	v_fmac_f32_e32 v115, v120, v122
	v_pk_fma_f32 v[80:81], v[80:81], v[72:73], v[116:117] op_sel_hi:[1,0,1]
	v_mov_b32_e32 v72, v123
	v_pk_mul_f32 v[116:117], v[74:75], v[30:31] op_sel_hi:[0,1]
	v_mul_f32_e32 v74, v99, v127
	s_add_i32 s8, s1, s6
	s_add_i32 s9, s88, s6
	s_or_b32 s6, s45, 32
	v_mul_f32_e32 v132, v102, v119
	v_pk_fma_f32 v[128:129], v[70:71], v[72:73], v[116:117] op_sel_hi:[1,0,1]
	v_fmac_f32_e32 v74, v115, v123
	v_mov_b32_e32 v70, s8
	v_mov_b32_e32 v115, s9
	s_add_i32 s10, s1, s6
	v_fmac_f32_e32 v132, v118, v73
	ds_read_b128 v[70:73], v70
	ds_read_b128 v[116:119], v115
	v_mov_b32_e32 v115, s10
	s_add_i32 s11, s88, s6
	v_mul_f32_e32 v76, v76, v123
	ds_read_b128 v[120:123], v115
	v_mov_b32_e32 v115, s11
	ds_read_b128 v[124:127], v115
	s_waitcnt lgkmcnt(3)
	v_mul_f32_e32 v115, v130, v70
	s_waitcnt lgkmcnt(2)
	v_pk_mul_f32 v[130:131], v[116:117], v[32:33] op_sel_hi:[0,1]
	v_mul_f32_e32 v133, v100, v116
	v_pk_fma_f32 v[80:81], v[80:81], v[70:71], v[130:131] op_sel_hi:[1,0,1]
	v_fmac_f32_e32 v133, v132, v70
	s_waitcnt lgkmcnt(0)
	v_pk_mul_f32 v[130:131], v[124:125], v[26:27] op_sel_hi:[0,1]
	v_mul_f32_e32 v132, v97, v124
	v_pk_fma_f32 v[128:129], v[128:129], v[120:121], v[130:131] op_sel_hi:[1,0,1]
	v_fmac_f32_e32 v132, v74, v120
	v_mul_f32_e32 v74, v115, v71
	v_pk_mul_f32 v[130:131], v[116:117], v[28:29] op_sel:[1,0]
	v_mul_f32_e32 v115, v98, v117
	v_pk_fma_f32 v[80:81], v[80:81], v[70:71], v[130:131] op_sel:[0,1,0]
	v_fmac_f32_e32 v115, v133, v71
	v_pk_mul_f32 v[70:71], v[124:125], v[22:23] op_sel:[1,0]
	v_mul_f32_e32 v74, v74, v72
	v_pk_mul_f32 v[116:117], v[118:119], v[24:25] op_sel_hi:[0,1]
	v_mul_f32_e32 v76, v76, v120
	v_pk_fma_f32 v[70:71], v[128:129], v[120:121], v[70:71] op_sel:[0,1,0]
	v_mul_f32_e32 v120, v95, v125
	v_pk_fma_f32 v[80:81], v[80:81], v[72:73], v[116:117] op_sel_hi:[1,0,1]
	v_mul_f32_e32 v118, v96, v118
	v_pk_mul_f32 v[116:117], v[126:127], v[18:19] op_sel_hi:[0,1]
	v_mul_f32_e32 v130, v74, v73
	v_mov_b32_e32 v74, v119
	v_fmac_f32_e32 v120, v132, v121
	v_fmac_f32_e32 v118, v115, v72
	v_pk_fma_f32 v[70:71], v[70:71], v[122:123], v[116:117] op_sel_hi:[1,0,1]
	v_mul_f32_e32 v115, v93, v126
	v_mov_b32_e32 v72, v73
	v_pk_mul_f32 v[116:117], v[74:75], v[20:21] op_sel_hi:[0,1]
	v_mov_b32_e32 v74, v127
	s_or_b32 s6, s57, 48
	v_fmac_f32_e32 v115, v120, v122
	v_pk_fma_f32 v[80:81], v[80:81], v[72:73], v[116:117] op_sel_hi:[1,0,1]
	v_mov_b32_e32 v72, v123
	v_pk_mul_f32 v[116:117], v[74:75], v[14:15] op_sel_hi:[0,1]
	v_mul_f32_e32 v74, v91, v127
	s_add_i32 s46, s1, s6
	s_add_i32 s47, s88, s6
	s_or_b32 s6, s45, 48
	v_mul_f32_e32 v76, v76, v121
	v_mul_f32_e32 v132, v94, v119
	v_pk_fma_f32 v[128:129], v[70:71], v[72:73], v[116:117] op_sel_hi:[1,0,1]
	v_fmac_f32_e32 v74, v115, v123
	v_mov_b32_e32 v70, s46
	v_mov_b32_e32 v115, s47
	s_add_i32 s33, s1, s6
	v_mul_f32_e32 v76, v76, v122
	v_fmac_f32_e32 v132, v118, v73
	ds_read_b128 v[70:73], v70
	ds_read_b128 v[116:119], v115
	v_mov_b32_e32 v115, s33
	s_add_i32 s6, s88, s6
	v_mul_f32_e32 v76, v76, v123
	ds_read_b128 v[120:123], v115
	v_mov_b32_e32 v115, s6
	ds_read_b128 v[124:127], v115
	s_waitcnt lgkmcnt(3)
	v_mul_f32_e32 v115, v130, v70
	s_waitcnt lgkmcnt(2)
	v_pk_mul_f32 v[130:131], v[116:117], v[16:17] op_sel_hi:[0,1]
	v_mul_f32_e32 v133, v92, v116
	v_pk_fma_f32 v[80:81], v[80:81], v[70:71], v[130:131] op_sel_hi:[1,0,1]
	v_fmac_f32_e32 v133, v132, v70
	s_waitcnt lgkmcnt(0)
	v_pk_mul_f32 v[130:131], v[124:125], v[10:11] op_sel_hi:[0,1]
	v_mul_f32_e32 v132, v89, v124
	v_pk_fma_f32 v[128:129], v[128:129], v[120:121], v[130:131] op_sel_hi:[1,0,1]
	v_fmac_f32_e32 v132, v74, v120
	v_mul_f32_e32 v74, v115, v71
	v_pk_mul_f32 v[130:131], v[116:117], v[12:13] op_sel:[1,0]
	v_mul_f32_e32 v115, v90, v117
	v_pk_fma_f32 v[80:81], v[80:81], v[70:71], v[130:131] op_sel:[0,1,0]
	v_fmac_f32_e32 v115, v133, v71
	v_pk_mul_f32 v[70:71], v[124:125], v[6:7] op_sel:[1,0]
	v_pk_mul_f32 v[116:117], v[118:119], v[8:9] op_sel_hi:[0,1]
	v_mul_f32_e32 v76, v76, v120
	v_pk_fma_f32 v[70:71], v[128:129], v[120:121], v[70:71] op_sel:[0,1,0]
	v_mul_f32_e32 v74, v74, v72
	v_pk_fma_f32 v[80:81], v[80:81], v[72:73], v[116:117] op_sel_hi:[1,0,1]
	v_pk_mul_f32 v[116:117], v[126:127], v[4:5] op_sel_hi:[0,1]
	v_mul_f32_e32 v76, v76, v121
	v_mul_f32_e32 v118, v87, v118
	v_pk_fma_f32 v[70:71], v[70:71], v[122:123], v[116:117] op_sel_hi:[1,0,1]
	v_mul_f32_e32 v116, v74, v73
	v_mov_b32_e32 v74, v119
	s_waitcnt vmcnt(2)
	v_lshlrev_b32_e32 v66, 16, v67
	v_and_b32_e32 v67, 0xffff0000, v67
	v_mul_f32_e32 v120, v88, v125
	v_fmac_f32_e32 v118, v115, v72
	v_mul_f32_e32 v76, v76, v122
	v_mov_b32_e32 v72, v73
	v_pk_mul_f32 v[68:69], v[74:75], v[68:69] op_sel_hi:[0,1]
	s_waitcnt vmcnt(0)
	v_mul_f32_e32 v63, v63, v119
	v_mov_b32_e32 v74, v127
	v_fmac_f32_e32 v120, v132, v121
	v_mul_f32_e32 v115, v86, v126
	v_pk_fma_f32 v[68:69], v[80:81], v[72:73], v[68:69] op_sel_hi:[1,0,1]
	v_fmac_f32_e32 v63, v118, v73
	v_mul_f32_e32 v73, v76, v123
	v_mov_b32_e32 v72, v123
	v_pk_mul_f32 v[66:67], v[74:75], v[66:67] op_sel_hi:[0,1]
	v_fmac_f32_e32 v115, v120, v122
	v_pk_fma_f32 v[66:67], v[70:71], v[72:73], v[66:67] op_sel_hi:[1,0,1]
	v_mul_f32_e32 v70, v78, v127
	v_fmac_f32_e32 v70, v115, v123
	ds_write_b32 v77, v116
	ds_write_b64 v77, v[68:69] offset:4096
	ds_write_b32 v79, v63 offset:8192
	ds_write_b32 v77, v73 offset:12288
	ds_write_b64 v77, v[66:67] offset:16384
	ds_write_b32 v79, v70 offset:20480
	v_mov_b32_e32 v69, 0
	v_mov_b32_e32 v68, 0
	v_mov_b32_e32 v71, 0
	v_mov_b32_e32 v70, 0
	v_mov_b32_e32 v73, 0
	v_mov_b32_e32 v72, 0
	s_waitcnt lgkmcnt(0)
	s_barrier
; __device__ __forceinline__ void ph5_m2(const Frame& F, const Args& A) {
;     ...
;         f32x2_t stA = {0.f, 0.f}, stB = {0.f, 0.f}; float snsA = 0.f, snsB = 0.f;
;         for (int q = 0; q < g; ++q) { const float a = seg[q * 128 + 2 * l], b = seg[3072 + q * 128 + 2 * l];
	s_cbranch_vccnz .LBB0_592
	v_readlane_b32 s16, v254, 50
	v_readlane_b32 s17, v254, 51
	s_andn2_b64 vcc, exec, s[16:17]
	s_cbranch_vccnz .LBB0_588
	v_mov_b32_e32 v70, 0
	s_mov_b32 s16, 0
	v_mov_b32_e32 v63, v84
	v_mov_b32_e32 v66, v83
	v_mov_b32_e32 v71, v70
	v_mov_b32_e32 v72, v70
	v_mov_b32_e32 v73, v70
	v_mov_b32_e32 v68, v70
	v_mov_b32_e32 v69, v70

; __device__ __forceinline__ void ph6_unit(const Frame& F, const Args& A, int c, int h) {
;     ...
;     {
;         const v4u* Qg = (const v4u*)((const bf16*)(ws + WS_QM) + ((size_t)h * S_ + t0) * 64); const v4u* Kg = (const v4u*)((const bf16*)(ws + WS_KM) + ((size_t)h * S_ + t0) * 64);
;         const v4u* Cg = (const v4u*)((const bf16*)(ws + WS_CST) + ((size_t)h * 128 + c) * 8192);
;         const v4u q4 = Qg[tid], k4 = Kg[tid], c40 = Cg[tid], c41 = Cg[tid + 512];
;         v4u vv[2];
; #pragma unroll
;         for (int i = 0; i < 2; ++i) { const int idx = tid + 512 * i, sx = idx >> 4, c8 = (idx & 15) * 8; vv[i] = *(const v4u*)(Z + (size_t)(t0 + sx) * pg8::ZLD + 1024 + h * 128 + c8); }
;         const float mprev = ((const float*)(ws + WS_SC))[3072 + h * 128 + c];
;         if (F.wave == 0) { const float b = ((const float*)(ws + WS_BL))[h * S_ + t0 + lane], ip = ((const float*)(ws + WS_IPL))[h * S_ + t0 + lane];
;             const float pm = wave_scan_max(ip - b, lane); const float mt = b + fmaxf(mprev, pm);
;             mtL[lane] = mt; wiL[lane] = expf(b + mprev - mt); btm[lane] = b - mt; ibs[lane] = ip - b;
;             nL[lane] = ((const float*)(ws + WS_NST))[((size_t)h * 128 + c) * 64 + lane]; }
.LBB0_942:
	s_ashr_i32 s80, s89, 3
	s_lshl_b32 s0, s80, 6
	s_and_b32 s77, s89, 7
	s_ashr_i32 s1, s0, 31
	s_lshl_b32 s54, s77, 19
	s_lshl_b64 s[50:51], s[0:1], 6
	s_add_u32 s84, s50, s54
	s_addc_u32 s85, s51, 0
	s_ashr_i32 s1, s80, 31
	s_lshl_b32 s96, s77, 7
	s_add_u32 s50, s96, s80
	s_addc_u32 s51, 0, s1
	s_lshl_b64 s[84:85], s[84:85], 1
	v_add_u32_e32 v18, s0, v35
	s_lshl_b64 s[90:91], s[50:51], 14
	v_lshl_add_u64 v[2:3], v[40:41], 0, s[84:85]
	v_lshl_add_u64 v[6:7], v[42:43], 0, s[84:85]
	v_mad_i64_i32 v[18:19], s[84:85], v18, s88, v[56:57]
	v_lshl_add_u64 v[10:11], v[44:45], 0, s[90:91]
	s_movk_i32 s1, 0x2000
	s_lshl_b32 s84, s77, 8
	s_mov_b32 s85, s97
	v_add_co_u32_e32 v14, vcc, s1, v10
	v_lshl_add_u64 v[18:19], v[18:19], 0, s[84:85]
	v_add_u32_e32 v20, s0, v39
	v_addc_co_u32_e32 v15, vcc, 0, v11, vcc
	v_lshl_add_u64 v[18:19], v[18:19], 0, v[46:47]
	s_mov_b32 s1, 0x17e00000
	v_mad_i64_i32 v[20:21], s[90:91], v20, s88, v[56:57]
	v_add_co_u32_e32 v18, vcc, s1, v18
	v_lshl_add_u64 v[20:21], v[20:21], 0, s[84:85]
	s_nop 0
	v_addc_co_u32_e32 v19, vcc, 0, v19, vcc
	v_lshl_add_u64 v[20:21], v[20:21], 0, v[46:47]
	v_add_co_u32_e32 v22, vcc, 0x17e00000, v20
	v_mov_b64_e32 v[120:121], v[2:3]
	global_load_dwordx4 v[2:5], v[2:3], off
	s_nop 0
	v_mov_b64_e32 v[122:123], v[6:7]
	global_load_dwordx4 v[6:9], v[6:7], off
	v_addc_co_u32_e32 v23, vcc, 0, v21, vcc
	v_mov_b64_e32 v[124:125], v[10:11]
	global_load_dwordx4 v[10:13], v[10:11], off
	s_nop 0
	v_mov_b64_e32 v[126:127], v[14:15]
	global_load_dwordx4 v[14:17], v[14:15], off
	s_nop 0
	v_mov_b64_e32 v[128:129], v[18:19]
	global_load_dwordx4 v[18:21], v[18:19], off offset:2048
	s_nop 0
	v_mov_b64_e32 v[130:131], v[22:23]
	global_load_dwordx4 v[22:25], v[22:23], off offset:2048
	s_andn2_b64 vcc, exec, s[2:3]
	s_cbranch_vccnz .LBB0_944
	s_add_i32 s1, s80, s96
	s_add_i32 s80, s1, 0xc00
	s_ashr_i32 s81, s80, 31
	s_lshl_b64 s[80:81], s[80:81], 2
	s_add_u32 s80, s33, s80
	s_addc_u32 s81, s86, s81
	s_lshl_b32 s1, s77, 13
	s_add_i32 s1, s1, s0
	v_or_b32_e32 v26, s1, v1
	v_ashrrev_i32_e32 v27, 31, v26
	v_lshlrev_b64 v[26:27], 2, v[26:27]
	v_lshl_add_u64 v[28:29], s[4:5], 0, v[26:27]
	v_lshl_add_u64 v[26:27], s[6:7], 0, v[26:27]
	global_load_dword v30, v47, s[80:81]
	v_add_u32_e32 v31, -2, v76
	global_load_dword v28, v[28:29], off
	s_mov_b32 s1, 0x3fb8aa3b
	global_load_dword v26, v[26:27], off
	v_and_b32_e32 v27, 64, v76
	v_add_u32_e32 v29, -1, v76
	v_cmp_lt_i32_e32 vcc, v29, v27
	s_lshl_b64 s[50:51], s[50:51], 8
	v_lshl_add_u64 v[116:117], v[48:49], 0, s[50:51]
	global_load_dword v118, v[116:117], off
	s_waitcnt vmcnt(0)
	v_sub_f32_e32 v26, v26, v28
	v_cndmask_b32_e32 v29, v29, v76, vcc
	v_lshlrev_b32_e32 v29, 2, v29
	ds_bpermute_b32 v29, v29, v26
	v_cmp_lt_i32_e32 vcc, v31, v27
	s_waitcnt lgkmcnt(0)
	v_max_f32_e32 v29, v29, v29
	v_max_f32_e32 v29, v26, v29
	v_cndmask_b32_e32 v31, v31, v76, vcc
	v_cndmask_b32_e64 v29, v29, v26, s[52:53]
	v_lshlrev_b32_e32 v31, 2, v31
	ds_bpermute_b32 v31, v31, v29
	s_waitcnt lgkmcnt(0)
	v_max_f32_e32 v31, v31, v31
	v_max_f32_e32 v31, v29, v31
	v_cndmask_b32_e64 v29, v31, v29, s[58:59]
	v_add_u32_e32 v31, -4, v76
	v_cmp_lt_i32_e32 vcc, v31, v27
	s_nop 1
	v_cndmask_b32_e32 v31, v31, v76, vcc
	v_lshlrev_b32_e32 v31, 2, v31
	ds_bpermute_b32 v31, v31, v29
	s_waitcnt lgkmcnt(0)
	v_max_f32_e32 v31, v31, v31
	v_max_f32_e32 v31, v29, v31
	v_cndmask_b32_e64 v29, v31, v29, s[60:61]
	v_add_u32_e32 v31, -8, v76
	v_cmp_lt_i32_e32 vcc, v31, v27
	s_nop 1
	v_cndmask_b32_e32 v31, v31, v76, vcc
	v_lshlrev_b32_e32 v31, 2, v31
	ds_bpermute_b32 v31, v31, v29
	s_waitcnt lgkmcnt(0)
	v_max_f32_e32 v31, v31, v31
	v_max_f32_e32 v31, v29, v31
	v_cndmask_b32_e64 v29, v31, v29, s[62:63]
	v_add_u32_e32 v31, -16, v76
	v_cmp_lt_i32_e32 vcc, v31, v27
	s_nop 1
	v_cndmask_b32_e32 v31, v31, v76, vcc
	v_lshlrev_b32_e32 v31, 2, v31
	ds_bpermute_b32 v31, v31, v29
	s_waitcnt lgkmcnt(0)
	v_max_f32_e32 v31, v31, v31
	v_max_f32_e32 v31, v29, v31
	v_cndmask_b32_e64 v29, v31, v29, s[64:65]
	v_subrev_u32_e32 v31, 32, v76
	v_cmp_lt_i32_e32 vcc, v31, v27
	s_nop 1
	v_cndmask_b32_e32 v27, v31, v76, vcc
	v_lshlrev_b32_e32 v27, 2, v27
	ds_bpermute_b32 v27, v27, v29
	v_max_f32_e32 v31, v29, v29
	s_waitcnt lgkmcnt(0)
	v_max_f32_e32 v27, v27, v27
	v_max_f32_e32 v27, v31, v27
	v_cndmask_b32_e64 v27, v27, v29, s[12:13]
	v_max_f32_e32 v27, v27, v27
	v_max_f32_e32 v29, v30, v30
	v_max_f32_e32 v27, v29, v27
	v_add_f32_e32 v27, v28, v27
	v_add_f32_e32 v29, v30, v28
	v_sub_f32_e32 v29, v29, v27
	v_mul_f32_e32 v30, 0x3fb8aa3b, v29
	v_fma_f32 v31, v29, s1, -v30
	v_rndne_f32_e32 v32, v30
	v_fmac_f32_e32 v31, 0x32a5705f, v29
	v_sub_f32_e32 v30, v30, v32
	v_add_f32_e32 v30, v30, v31
	v_exp_f32_e32 v30, v30
	v_cvt_i32_f32_e32 v31, v32
	s_mov_b32 s1, 0xc2ce8ed0
	v_cmp_ngt_f32_e32 vcc, s1, v29
	s_mov_b32 s1, 0x42b17218
	v_ldexp_f32 v30, v30, v31
	v_cndmask_b32_e32 v30, 0, v30, vcc
	v_cmp_nlt_f32_e32 vcc, s1, v29
	s_nop 1
	v_cndmask_b32_e32 v29, v79, v30, vcc
	ds_write2st64_b32 v62, v27, v29 offset0:246 offset1:247
	v_sub_f32_e32 v27, v28, v27
	ds_write2st64_b32 v62, v27, v26 offset0:244 offset1:245
	v_mov_b32_e32 v26, v118
	ds_write_b32 v62, v26 offset:63488
; __device__ __forceinline__ int v_st(int k, int c) { const int kk = (k & ~0xC) | ((k & 4) << 1) | ((k & 8) >> 1); return ((kk >> 3) * 4 + (c >> 5)) * 512 + ((kk & 7) * 32 + (c & 31)) * 2; }
; #define LAS __attribute__((address_space(3)))
; __device__ __forceinline__ void ph6_unit(const Frame& F, const Args& A, int c, int h) {
;     ...
;         *(LAS v4u*)(Qb + (tid >> 3) * LP + (tid & 7) * 8) = q4; *(LAS v4u*)(Kb + (tid >> 3) * LP + (tid & 7) * 8) = k4;
;         *(LAS v4u*)(Cb + (tid >> 3) * LP + (tid & 7) * 8) = c40; *(LAS v4u*)(Cb + (64 + (tid >> 3)) * LP + (tid & 7) * 8) = c41;
; #pragma unroll
;         for (int i = 0; i < 2; ++i) { const int idx = tid + 512 * i, sx = idx >> 4, c8 = (idx & 15) * 8; *(LAS v4u*)(Vt + fox::v_st(sx, c8)) = vv[i]; }
;     }
;     __syncthreads();
;     ...
;         const int j = tid - 256, t = j >> 2, dq = (j & 3) * 16; float qn = 0.f;
; #pragma unroll
;         for (int i = 0; i < 16; ++i) qn += pg8::bf2f(Qb[t * LP + dq + i]) * nL[dq + i];
;         qn += __shfl_xor(qn, 1); qn += __shfl_xor(qn, 2);
;         if ((j & 3) == 0) qnL[t] = qn;
.LBB0_944:
	s_mov_b64 s[50:51], -1
	s_and_b64 vcc, exec, s[8:9]
	s_waitcnt vmcnt(0)
	ds_write_b128 v37, v[2:5] offset:16384
	ds_write_b128 v37, v[6:9] offset:25600
	ds_write_b128 v37, v[10:13] offset:44032
	ds_write_b128 v37, v[14:17] offset:53248
	ds_write_b128 v74, v[18:21]
	ds_write_b128 v75, v[22:25]
	s_waitcnt lgkmcnt(0)
	s_barrier
	s_mov_b32 s98, 0x40000
	s_mov_b32 s99, 0
	v_lshl_add_u64 v[132:133], v[120:121], 0, s[98:99]
	global_load_dword v134, v[132:133], off
	v_lshl_add_u64 v[132:133], v[122:123], 0, s[98:99]
	global_load_dword v134, v[132:133], off
	s_mov_b32 s98, 0x80000
	v_lshl_add_u64 v[132:133], v[124:125], 0, s[98:99]
	global_load_dword v134, v[132:133], off
	v_lshl_add_u64 v[132:133], v[126:127], 0, s[98:99]
	global_load_dword v134, v[132:133], off
	s_mov_b32 s98, 0x2c00000
	v_lshl_add_u64 v[132:133], v[128:129], 0, s[98:99]
	global_load_dword v134, v[132:133], off offset:2048
	v_lshl_add_u64 v[132:133], v[130:131], 0, s[98:99]
	global_load_dword v134, v[132:133], off offset:2048
	s_cbranch_vccz .LBB0_948
	ds_read_b128 v[2:5], v63 offset:16384
	ds_read_b128 v[6:9], v63 offset:16400
	ds_read_b128 v[10:13], v64 offset:63488
	ds_read_b128 v[14:17], v64 offset:63504
	ds_read_b128 v[18:21], v64 offset:63520
	ds_read_b128 v[22:25], v64 offset:63536
	s_waitcnt lgkmcnt(5)
	v_lshlrev_b32_e32 v26, 16, v2
	v_and_b32_e32 v2, 0xffff0000, v2
	s_waitcnt lgkmcnt(3)
	v_fma_f32 v10, v10, v26, 0
	v_fmac_f32_e32 v10, v11, v2
	v_lshlrev_b32_e32 v2, 16, v3
	v_fmac_f32_e32 v10, v12, v2
	v_and_b32_e32 v2, 0xffff0000, v3
	v_fmac_f32_e32 v10, v13, v2
	v_lshlrev_b32_e32 v2, 16, v4
	s_waitcnt lgkmcnt(2)
	v_fmac_f32_e32 v10, v14, v2
	v_and_b32_e32 v2, 0xffff0000, v4
	v_fmac_f32_e32 v10, v15, v2
	v_lshlrev_b32_e32 v2, 16, v5
	v_fmac_f32_e32 v10, v16, v2
	v_and_b32_e32 v2, 0xffff0000, v5
	v_fmac_f32_e32 v10, v17, v2
	v_lshlrev_b32_e32 v2, 16, v6
	s_waitcnt lgkmcnt(1)
	v_fmac_f32_e32 v10, v18, v2
	v_and_b32_e32 v2, 0xffff0000, v6
	v_fmac_f32_e32 v10, v19, v2
	v_lshlrev_b32_e32 v2, 16, v7
	v_fmac_f32_e32 v10, v20, v2
	v_and_b32_e32 v2, 0xffff0000, v7
	v_fmac_f32_e32 v10, v21, v2
	v_lshlrev_b32_e32 v2, 16, v8
	s_waitcnt lgkmcnt(0)
	v_fmac_f32_e32 v10, v22, v2
	v_and_b32_e32 v2, 0xffff0000, v8
	v_fmac_f32_e32 v10, v23, v2
	v_lshlrev_b32_e32 v2, 16, v9
	v_fmac_f32_e32 v10, v24, v2
	v_and_b32_e32 v2, 0xffff0000, v9
	v_and_b32_e32 v3, 64, v76
	v_fmac_f32_e32 v10, v25, v2
	v_xor_b32_e32 v2, 1, v76
	v_add_u32_e32 v3, 64, v3
	v_cmp_lt_i32_e32 vcc, v2, v3
	v_xor_b32_e32 v4, 2, v76
	s_nop 0
	v_cndmask_b32_e32 v2, v76, v2, vcc
	v_lshlrev_b32_e32 v2, 2, v2
	ds_bpermute_b32 v2, v2, v10
	v_cmp_lt_i32_e32 vcc, v4, v3
	s_waitcnt lgkmcnt(0)
	v_add_f32_e32 v2, v10, v2
	v_cndmask_b32_e32 v3, v76, v4, vcc
	v_lshlrev_b32_e32 v3, 2, v3
	ds_bpermute_b32 v3, v3, v2
	s_and_saveexec_b64 s[50:51], s[14:15]
	s_cbranch_execz .LBB0_947
	s_waitcnt lgkmcnt(0)
	v_add_f32_e32 v2, v2, v3
	ds_write_b32 v65, v2 offset:63744

; __device__ __forceinline__ void ph13_final(const Frame& F, const Args& A) {
;     ...
;     for (int row = gw; row < S_; row += NGW) {
;         f32x4 v[8], mo[8];
;         const f32x4* xr = (const f32x4*)(A.in[I_X] + (size_t)row * DM) + lane; const uint2* dr = (const uint2*)((const bf16*)(ws + WS_XN) + (size_t)row * DM) + lane;
; #pragma unroll
;         for (int j = 0; j < 8; ++j) { const f32x4 xv = xr[64 * j]; const uint2 dw = dr[64 * j];
;             v[j].x = xv.x + bflo(dw.x); v[j].y = xv.y + bfhi(dw.x); v[j].z = xv.z + bflo(dw.y); v[j].w = xv.w + bfhi(dw.y); mo[j] = (f32x4){0.f, 0.f, 0.f, 0.f}; }
; #pragma unroll
;         for (int k = 0; k < 4; ++k) { const int dst = EOFF[EIDX[row * 4 + k]] + ESLOT[row * 4 + k]; const unsigned* yr = (const unsigned*)(YS + (size_t)dst * DM) + lane;
; #pragma unroll
;             for (int j = 0; j < 8; ++j) { const unsigned w = yr[64 * j]; const auto lo2 = __builtin_amdgcn_cvt_pk_f32_fp8((int)w, false), hi2 = __builtin_amdgcn_cvt_pk_f32_fp8((int)w, true);
;                 mo[j].x += lo2[0]; mo[j].y += lo2[1]; mo[j].z += hi2[0]; mo[j].w += hi2[1]; } }
.LBB0_1568:
	s_ashr_i32 s7, s6, 31
	v_lshl_add_u64 v[104:105], s[8:9], 0, v[16:17]
	s_lshl_b64 s[0:1], s[6:7], 2
	v_add_co_u32_e32 v120, vcc, s3, v104
	s_add_u32 s24, s17, s0
	s_nop 0
	v_addc_co_u32_e32 v121, vcc, 0, v105, vcc
	s_addc_u32 s25, s18, s1
	global_load_dwordx2 v[42:43], v[40:41], off
	global_load_dwordx2 v[44:45], v[40:41], off offset:512
	global_load_dwordx2 v[46:47], v[40:41], off offset:1024
	global_load_dwordx2 v[48:49], v[40:41], off offset:1536
	global_load_dwordx2 v[50:51], v[40:41], off offset:2048
	global_load_dwordx2 v[52:53], v[40:41], off offset:2560
	global_load_dwordx2 v[54:55], v[40:41], off offset:3072
	global_load_dwordx2 v[56:57], v[40:41], off offset:3584
	global_load_dwordx4 v[4:7], v[20:21], off
	global_load_dwordx4 v[8:11], v[20:21], off offset:1024
	global_load_dwordx4 v[12:15], v[20:21], off offset:2048
	global_load_dwordx4 v[68:71], v[20:21], off offset:3072
	global_load_dwordx4 v[72:75], v[24:25], off
	global_load_dwordx4 v[76:79], v[26:27], off
	global_load_dwordx4 v[80:83], v[28:29], off
	global_load_dwordx4 v[84:87], v[30:31], off
	global_load_dwordx4 v[0:3], v[22:23], off
	global_load_dwordx4 v[88:91], v[104:105], off
	global_load_dwordx4 v[92:95], v[104:105], off offset:1024
	global_load_dwordx4 v[96:99], v[104:105], off offset:2048
	global_load_dwordx4 v[100:103], v[104:105], off offset:3072
	s_nop 0
	global_load_dwordx4 v[104:107], v[120:121], off
	global_load_dwordx4 v[108:111], v[120:121], off offset:1024
	global_load_dwordx4 v[112:115], v[120:121], off offset:2048
	global_load_dwordx4 v[116:119], v[120:121], off offset:3072
	s_add_u32 s0, s19, s0
	global_load_dwordx4 v[120:123], v17, s[24:25]
	s_addc_u32 s1, s20, s1
	global_load_dword v127, v17, s[0:1]
	s_add_i32 s24, s6, 1
	s_ashr_i32 s25, s24, 31
	s_lshl_b64 s[0:1], s[24:25], 2
	s_add_u32 s0, s19, s0
	s_addc_u32 s1, s20, s1
	global_load_dwordx3 v[124:126], v17, s[0:1]
	v_lshl_add_u64 v[58:59], s[12:13], 0, v[16:17]
	s_add_i32 s2, s2, s4
	s_add_i32 s6, s6, s21
	s_add_u32 s8, s8, s10
	s_addc_u32 s9, s9, s11
	s_add_u32 s12, s12, s10
	s_addc_u32 s13, s13, s11
	v_lshl_add_u64 v[40:41], v[40:41], 0, s[14:15]
	s_cmpk_lt_i32 s2, 0x2000
	s_waitcnt vmcnt(0)
	v_lshlrev_b32_e32 v128, 16, v42
	v_and_b32_e32 v129, 0xffff0000, v42
	v_lshlrev_b32_e32 v42, 16, v43
	v_and_b32_e32 v43, 0xffff0000, v43
	v_lshlrev_b32_e32 v130, 16, v44
	v_and_b32_e32 v131, 0xffff0000, v44
	v_lshlrev_b32_e32 v132, 16, v46
	v_and_b32_e32 v133, 0xffff0000, v46
	v_lshlrev_b32_e32 v136, 16, v50
	v_and_b32_e32 v137, 0xffff0000, v50
	v_lshlrev_b32_e32 v50, 16, v51
	v_and_b32_e32 v51, 0xffff0000, v51
	v_pk_add_f32 v[42:43], v[90:91], v[42:43]
	v_pk_add_f32 v[90:91], v[92:93], v[130:131]
	v_pk_add_f32 v[92:93], v[96:97], v[132:133]
	v_pk_add_f32 v[96:97], v[104:105], v[136:137]
	v_pk_add_f32 v[50:51], v[106:107], v[50:51]
	v_lshlrev_b32_e32 v104, 2, v120
	v_lshlrev_b32_e32 v105, 2, v121
	v_lshlrev_b32_e32 v107, 2, v123
	v_lshlrev_b32_e32 v46, 16, v47
	v_and_b32_e32 v47, 0xffff0000, v47
	v_lshlrev_b32_e32 v138, 16, v52
	v_and_b32_e32 v139, 0xffff0000, v52
	v_lshlrev_b32_e32 v106, 2, v122
	v_add_u32_e32 v104, s5, v104
	v_add_u32_e32 v105, s5, v105
	v_add_u32_e32 v107, s5, v107
	v_pk_add_f32 v[46:47], v[98:99], v[46:47]
	v_pk_add_f32 v[98:99], v[108:109], v[138:139]
	v_add_u32_e32 v106, s5, v106
	ds_read_b32 v104, v104
	ds_read_b32 v105, v105
	ds_read_b32 v108, v106
	ds_read_b32 v107, v107
	v_lshlrev_b32_e32 v52, 16, v53
	v_and_b32_e32 v53, 0xffff0000, v53
	s_waitcnt lgkmcnt(3)
	v_add_u32_e32 v104, v127, v104
	v_pk_add_f32 v[52:53], v[110:111], v[52:53]
	s_waitcnt lgkmcnt(2)
	v_add_u32_e32 v106, v124, v105
	s_waitcnt lgkmcnt(1)
	v_add_u32_e32 v108, v125, v108
	s_waitcnt lgkmcnt(0)
	v_add_u32_e32 v110, v126, v107
	v_ashrrev_i32_e32 v105, 31, v104
	v_ashrrev_i32_e32 v107, 31, v106
	v_ashrrev_i32_e32 v109, 31, v108
	v_ashrrev_i32_e32 v111, 31, v110
	v_lshlrev_b64 v[104:105], 11, v[104:105]
	v_lshlrev_b32_e32 v44, 16, v45
	v_and_b32_e32 v45, 0xffff0000, v45
	v_lshlrev_b32_e32 v134, 16, v48
	v_and_b32_e32 v135, 0xffff0000, v48
	v_lshlrev_b32_e32 v48, 16, v49
	v_and_b32_e32 v49, 0xffff0000, v49
	v_lshlrev_b32_e32 v140, 16, v54
	v_and_b32_e32 v141, 0xffff0000, v54
	v_lshlrev_b32_e32 v54, 16, v55
	v_and_b32_e32 v55, 0xffff0000, v55
	v_lshlrev_b32_e32 v142, 16, v56
	v_and_b32_e32 v143, 0xffff0000, v56
	v_lshlrev_b32_e32 v56, 16, v57
	v_and_b32_e32 v57, 0xffff0000, v57
	v_lshlrev_b64 v[106:107], 11, v[106:107]
	v_lshlrev_b64 v[108:109], 11, v[108:109]
	v_lshlrev_b64 v[110:111], 11, v[110:111]
	v_lshl_add_u64 v[104:105], v[18:19], 0, v[104:105]
	v_pk_add_f32 v[44:45], v[94:95], v[44:45]
	v_pk_add_f32 v[48:49], v[102:103], v[48:49]
	v_pk_add_f32 v[94:95], v[100:101], v[134:135]
	v_pk_add_f32 v[100:101], v[112:113], v[140:141]
	v_pk_add_f32 v[54:55], v[114:115], v[54:55]
	v_pk_add_f32 v[102:103], v[116:117], v[142:143]
	v_pk_add_f32 v[56:57], v[118:119], v[56:57]
	v_lshl_add_u64 v[106:107], v[18:19], 0, v[106:107]
	v_lshl_add_u64 v[108:109], v[18:19], 0, v[108:109]
	v_lshl_add_u64 v[110:111], v[18:19], 0, v[110:111]
	global_load_dword v112, v[104:105], off
	global_load_dword v113, v[104:105], off offset:256
	global_load_dword v114, v[104:105], off offset:512
	global_load_dword v118, v[104:105], off offset:768
	global_load_dword v122, v[104:105], off offset:1024
	global_load_dword v126, v[104:105], off offset:1280
	global_load_dword v130, v[104:105], off offset:1536
	global_load_dword v134, v[104:105], off offset:1792
	global_load_dword v138, v[106:107], off
	global_load_dword v142, v[106:107], off offset:256
	global_load_dword v146, v[106:107], off offset:512
	global_load_dword v150, v[106:107], off offset:768
; __device__ __forceinline__ void ph13_final(const Frame& F, const Args& A) {
;     ...
;         for (int k = 0; k < 4; ++k) { const int dst = EOFF[EIDX[row * 4 + k]] + ESLOT[row * 4 + k]; const unsigned* yr = (const unsigned*)(YS + (size_t)dst * DM) + lane;
; #pragma unroll
;             for (int j = 0; j < 8; ++j) { const unsigned w = yr[64 * j]; const auto lo2 = __builtin_amdgcn_cvt_pk_f32_fp8((int)w, false), hi2 = __builtin_amdgcn_cvt_pk_f32_fp8((int)w, true);
;                 mo[j].x += lo2[0]; mo[j].y += lo2[1]; mo[j].z += hi2[0]; mo[j].w += hi2[1]; } }
;         float ss = 0.f;
; #pragma unroll
;         for (int j = 0; j < 8; ++j) { const f32x4 g2 = *(const f32x4*)(MOD + 10240 + 4 * lane + 256 * j) * 0.03125f; v[j] = v[j] + g2 * mo[j];
	global_load_dword v154, v[106:107], off offset:1024
	global_load_dword v158, v[106:107], off offset:1280
	global_load_dword v162, v[106:107], off offset:1536
	global_load_dword v166, v[106:107], off offset:1792
	global_load_dword v170, v[108:109], off
	global_load_dword v174, v[108:109], off offset:256
	global_load_dword v178, v[108:109], off offset:512
	global_load_dword v182, v[108:109], off offset:768
	global_load_dword v186, v[108:109], off offset:1024
	global_load_dword v190, v[108:109], off offset:1280
	global_load_dword v194, v[108:109], off offset:1536
	global_load_dword v198, v[108:109], off offset:1792
	global_load_dword v202, v[110:111], off
	global_load_dword v206, v[110:111], off offset:256
	global_load_dword v210, v[110:111], off offset:512
	global_load_dword v214, v[110:111], off offset:768
	global_load_dword v218, v[110:111], off offset:1024
	global_load_dword v222, v[110:111], off offset:1280
	global_load_dword v226, v[110:111], off offset:1536
	global_load_dword v230, v[110:111], off offset:1792
	v_pk_add_f32 v[88:89], v[88:89], v[128:129]
	v_pk_mul_f32 v[6:7], v[6:7], s[16:17] op_sel_hi:[1,0]
	v_pk_mul_f32 v[4:5], v[4:5], s[16:17] op_sel_hi:[1,0]
	v_pk_mul_f32 v[10:11], v[10:11], s[16:17] op_sel_hi:[1,0]
	v_pk_mul_f32 v[8:9], v[8:9], s[16:17] op_sel_hi:[1,0]
	v_pk_mul_f32 v[14:15], v[14:15], s[16:17] op_sel_hi:[1,0]
	v_pk_mul_f32 v[12:13], v[12:13], s[16:17] op_sel_hi:[1,0]
	v_pk_mul_f32 v[74:75], v[74:75], s[16:17] op_sel_hi:[1,0]
	v_pk_mul_f32 v[78:79], v[78:79], s[16:17] op_sel_hi:[1,0]
	v_pk_mul_f32 v[70:71], v[70:71], s[16:17] op_sel_hi:[1,0]
	v_pk_mul_f32 v[68:69], v[68:69], s[16:17] op_sel_hi:[1,0]
	v_pk_mul_f32 v[72:73], v[72:73], s[16:17] op_sel_hi:[1,0]
	v_pk_mul_f32 v[76:77], v[76:77], s[16:17] op_sel_hi:[1,0]
	v_pk_mul_f32 v[82:83], v[82:83], s[16:17] op_sel_hi:[1,0]
	v_pk_mul_f32 v[80:81], v[80:81], s[16:17] op_sel_hi:[1,0]
	v_pk_mul_f32 v[86:87], v[86:87], s[16:17] op_sel_hi:[1,0]
	v_pk_mul_f32 v[84:85], v[84:85], s[16:17] op_sel_hi:[1,0]
	s_waitcnt vmcnt(31)
	v_cvt_pk_f32_fp8_e32 v[104:105], v112
	v_cvt_pk_f32_fp8_sdwa v[106:107], v112 src0_sel:WORD_1
	s_waitcnt vmcnt(30)
	v_cvt_pk_f32_fp8_e32 v[108:109], v113
	v_cvt_pk_f32_fp8_sdwa v[110:111], v113 src0_sel:WORD_1
	s_waitcnt vmcnt(29)
	v_cvt_pk_f32_fp8_e32 v[112:113], v114
	v_cvt_pk_f32_fp8_sdwa v[114:115], v114 src0_sel:WORD_1
	s_waitcnt vmcnt(27)
	v_cvt_pk_f32_fp8_e32 v[120:121], v122
	v_cvt_pk_f32_fp8_sdwa v[122:123], v122 src0_sel:WORD_1
	s_waitcnt vmcnt(26)
	v_cvt_pk_f32_fp8_e32 v[124:125], v126
	v_cvt_pk_f32_fp8_sdwa v[126:127], v126 src0_sel:WORD_1
	s_waitcnt vmcnt(23)
	v_cvt_pk_f32_fp8_e32 v[136:137], v138
	v_cvt_pk_f32_fp8_sdwa v[138:139], v138 src0_sel:WORD_1
	s_waitcnt vmcnt(22)
	v_cvt_pk_f32_fp8_e32 v[140:141], v142
	v_cvt_pk_f32_fp8_sdwa v[142:143], v142 src0_sel:WORD_1
	v_cvt_pk_f32_fp8_e32 v[116:117], v118
	v_cvt_pk_f32_fp8_sdwa v[118:119], v118 src0_sel:WORD_1
	v_cvt_pk_f32_fp8_e32 v[128:129], v130
	v_cvt_pk_f32_fp8_sdwa v[130:131], v130 src0_sel:WORD_1
	s_waitcnt vmcnt(21)
	v_cvt_pk_f32_fp8_e32 v[144:145], v146
	v_cvt_pk_f32_fp8_sdwa v[146:147], v146 src0_sel:WORD_1
	s_waitcnt vmcnt(19)
	v_cvt_pk_f32_fp8_e32 v[152:153], v154
	v_cvt_pk_f32_fp8_sdwa v[154:155], v154 src0_sel:WORD_1
	s_waitcnt vmcnt(18)
	v_cvt_pk_f32_fp8_e32 v[156:157], v158
	v_cvt_pk_f32_fp8_sdwa v[158:159], v158 src0_sel:WORD_1
	s_waitcnt vmcnt(15)
	v_cvt_pk_f32_fp8_e32 v[168:169], v170
	v_cvt_pk_f32_fp8_sdwa v[170:171], v170 src0_sel:WORD_1
	s_waitcnt vmcnt(14)
	v_cvt_pk_f32_fp8_e32 v[172:173], v174
	v_cvt_pk_f32_fp8_sdwa v[174:175], v174 src0_sel:WORD_1
	v_cvt_pk_f32_fp8_e32 v[148:149], v150
	v_cvt_pk_f32_fp8_sdwa v[150:151], v150 src0_sel:WORD_1
	v_cvt_pk_f32_fp8_e32 v[160:161], v162
	v_cvt_pk_f32_fp8_sdwa v[162:163], v162 src0_sel:WORD_1
	s_waitcnt vmcnt(13)
	v_cvt_pk_f32_fp8_e32 v[176:177], v178
	v_cvt_pk_f32_fp8_sdwa v[178:179], v178 src0_sel:WORD_1
	s_waitcnt vmcnt(11)
	v_cvt_pk_f32_fp8_e32 v[184:185], v186
	v_cvt_pk_f32_fp8_sdwa v[186:187], v186 src0_sel:WORD_1
	s_waitcnt vmcnt(10)
	v_cvt_pk_f32_fp8_e32 v[188:189], v190
	v_cvt_pk_f32_fp8_sdwa v[190:191], v190 src0_sel:WORD_1
	s_waitcnt vmcnt(7)
	v_cvt_pk_f32_fp8_e32 v[200:201], v202
	v_cvt_pk_f32_fp8_sdwa v[202:203], v202 src0_sel:WORD_1
	s_waitcnt vmcnt(6)
	v_cvt_pk_f32_fp8_e32 v[204:205], v206
	v_cvt_pk_f32_fp8_sdwa v[206:207], v206 src0_sel:WORD_1
	v_cvt_pk_f32_fp8_e32 v[132:133], v134
	v_cvt_pk_f32_fp8_sdwa v[134:135], v134 src0_sel:WORD_1
	v_cvt_pk_f32_fp8_e32 v[180:181], v182
	v_cvt_pk_f32_fp8_sdwa v[182:183], v182 src0_sel:WORD_1
	v_cvt_pk_f32_fp8_e32 v[192:193], v194
	v_cvt_pk_f32_fp8_sdwa v[194:195], v194 src0_sel:WORD_1
	s_waitcnt vmcnt(5)
	v_cvt_pk_f32_fp8_e32 v[208:209], v210
	v_cvt_pk_f32_fp8_sdwa v[210:211], v210 src0_sel:WORD_1
	s_waitcnt vmcnt(3)
	v_cvt_pk_f32_fp8_e32 v[216:217], v218
	v_cvt_pk_f32_fp8_sdwa v[218:219], v218 src0_sel:WORD_1
	s_waitcnt vmcnt(2)
	v_cvt_pk_f32_fp8_e32 v[220:221], v222
	v_cvt_pk_f32_fp8_sdwa v[222:223], v222 src0_sel:WORD_1
	v_pk_add_f32 v[106:107], v[106:107], 0 op_sel_hi:[1,0]
	v_pk_add_f32 v[104:105], v[104:105], 0 op_sel_hi:[1,0]
	v_pk_add_f32 v[110:111], v[110:111], 0 op_sel_hi:[1,0]
	v_pk_add_f32 v[108:109], v[108:109], 0 op_sel_hi:[1,0]
	v_cvt_pk_f32_fp8_e32 v[164:165], v166
	v_cvt_pk_f32_fp8_sdwa v[166:167], v166 src0_sel:WORD_1
	v_cvt_pk_f32_fp8_e32 v[212:213], v214
	v_cvt_pk_f32_fp8_sdwa v[214:215], v214 src0_sel:WORD_1
	s_waitcnt vmcnt(1)
; __device__ __forceinline__ float wave_sum(float v) {
;     ...
;     for (int o = 1; o < 64; o <<= 1) v += __shfl_xor(v, o);
; __device__ __forceinline__ void ph13_final(const Frame& F, const Args& A) {
;     ...
;         for (int k = 0; k < 4; ++k) { const int dst = EOFF[EIDX[row * 4 + k]] + ESLOT[row * 4 + k]; const unsigned* yr = (const unsigned*)(YS + (size_t)dst * DM) + lane;
; #pragma unroll
;             for (int j = 0; j < 8; ++j) { const unsigned w = yr[64 * j]; const auto lo2 = __builtin_amdgcn_cvt_pk_f32_fp8((int)w, false), hi2 = __builtin_amdgcn_cvt_pk_f32_fp8((int)w, true);
;                 mo[j].x += lo2[0]; mo[j].y += lo2[1]; mo[j].z += hi2[0]; mo[j].w += hi2[1]; } }
;         float ss = 0.f;
; #pragma unroll
;         for (int j = 0; j < 8; ++j) { const f32x4 g2 = *(const f32x4*)(MOD + 10240 + 4 * lane + 256 * j) * 0.03125f; v[j] = v[j] + g2 * mo[j];
;             ss += (v[j].x * v[j].x + v[j].y * v[j].y) + (v[j].z * v[j].z + v[j].w * v[j].w); }
;         const float rstd = 1.f / sqrtf(wave_sum(ss) * (1.f / DM) + EPS_);
;         f32x4* orow = (f32x4*)(out + (size_t)row * DM) + lane;
; #pragma unroll
;         for (int j = 0; j < 8; ++j) { const f32x4 g = *(const f32x4*)(fg + 4 * lane + 256 * j); orow[64 * j] = v[j] * rstd * g; }
	v_cvt_pk_f32_fp8_e32 v[224:225], v226
	v_cvt_pk_f32_fp8_sdwa v[226:227], v226 src0_sel:WORD_1
	v_pk_add_f32 v[112:113], v[112:113], 0 op_sel_hi:[1,0]
	v_pk_add_f32 v[114:115], v[114:115], 0 op_sel_hi:[1,0]
	v_pk_add_f32 v[122:123], v[122:123], 0 op_sel_hi:[1,0]
	v_pk_add_f32 v[126:127], v[126:127], 0 op_sel_hi:[1,0]
	v_pk_add_f32 v[104:105], v[104:105], v[136:137]
	v_pk_add_f32 v[106:107], v[106:107], v[138:139]
	v_pk_add_f32 v[108:109], v[108:109], v[140:141]
	v_pk_add_f32 v[110:111], v[110:111], v[142:143]
	v_cvt_pk_f32_fp8_e32 v[196:197], v198
	v_cvt_pk_f32_fp8_sdwa v[198:199], v198 src0_sel:WORD_1
	v_pk_add_f32 v[118:119], v[118:119], 0 op_sel_hi:[1,0]
	v_pk_add_f32 v[116:117], v[116:117], 0 op_sel_hi:[1,0]
	v_pk_add_f32 v[120:121], v[120:121], 0 op_sel_hi:[1,0]
	v_pk_add_f32 v[124:125], v[124:125], 0 op_sel_hi:[1,0]
	v_pk_add_f32 v[130:131], v[130:131], 0 op_sel_hi:[1,0]
	v_pk_add_f32 v[128:129], v[128:129], 0 op_sel_hi:[1,0]
	v_pk_add_f32 v[114:115], v[114:115], v[146:147]
	v_pk_add_f32 v[112:113], v[112:113], v[144:145]
	v_pk_add_f32 v[122:123], v[122:123], v[154:155]
	v_pk_add_f32 v[126:127], v[126:127], v[158:159]
	v_pk_add_f32 v[106:107], v[106:107], v[170:171]
	v_pk_add_f32 v[104:105], v[104:105], v[168:169]
	v_pk_add_f32 v[110:111], v[110:111], v[174:175]
	v_pk_add_f32 v[108:109], v[108:109], v[172:173]
	s_waitcnt vmcnt(0)
	v_cvt_pk_f32_fp8_e32 v[228:229], v230
	v_cvt_pk_f32_fp8_sdwa v[230:231], v230 src0_sel:WORD_1
	v_pk_add_f32 v[116:117], v[116:117], v[148:149]
	v_pk_add_f32 v[118:119], v[118:119], v[150:151]
	v_pk_add_f32 v[120:121], v[120:121], v[152:153]
	v_pk_add_f32 v[124:125], v[124:125], v[156:157]
	v_pk_add_f32 v[128:129], v[128:129], v[160:161]
	v_pk_add_f32 v[130:131], v[130:131], v[162:163]
	v_pk_add_f32 v[112:113], v[112:113], v[176:177]
	v_pk_add_f32 v[114:115], v[114:115], v[178:179]
	v_pk_add_f32 v[122:123], v[122:123], v[186:187]
	v_pk_add_f32 v[126:127], v[126:127], v[190:191]
	v_pk_add_f32 v[104:105], v[104:105], v[200:201]
	v_pk_add_f32 v[106:107], v[106:107], v[202:203]
	v_pk_add_f32 v[108:109], v[108:109], v[204:205]
	v_pk_add_f32 v[110:111], v[110:111], v[206:207]
	v_pk_add_f32 v[134:135], v[134:135], 0 op_sel_hi:[1,0]
	v_pk_add_f32 v[132:133], v[132:133], 0 op_sel_hi:[1,0]
	v_pk_add_f32 v[118:119], v[118:119], v[182:183]
	v_pk_add_f32 v[116:117], v[116:117], v[180:181]
	v_pk_add_f32 v[120:121], v[120:121], v[184:185]
	v_pk_add_f32 v[124:125], v[124:125], v[188:189]
	v_pk_add_f32 v[130:131], v[130:131], v[194:195]
	v_pk_add_f32 v[128:129], v[128:129], v[192:193]
	v_pk_add_f32 v[114:115], v[114:115], v[210:211]
	v_pk_add_f32 v[112:113], v[112:113], v[208:209]
	v_pk_add_f32 v[122:123], v[122:123], v[218:219]
	v_pk_add_f32 v[126:127], v[126:127], v[222:223]
	v_pk_fma_f32 v[6:7], v[106:107], v[6:7], v[42:43]
	v_pk_fma_f32 v[4:5], v[104:105], v[4:5], v[88:89]
	v_pk_fma_f32 v[10:11], v[110:111], v[10:11], v[44:45]
	v_pk_fma_f32 v[8:9], v[108:109], v[8:9], v[90:91]
	v_pk_add_f32 v[132:133], v[132:133], v[164:165]
	v_pk_add_f32 v[134:135], v[134:135], v[166:167]
	v_pk_add_f32 v[116:117], v[116:117], v[212:213]
	v_pk_add_f32 v[118:119], v[118:119], v[214:215]
	v_pk_add_f32 v[120:121], v[120:121], v[216:217]
	v_pk_add_f32 v[124:125], v[124:125], v[220:221]
	v_pk_add_f32 v[128:129], v[128:129], v[224:225]
	v_pk_add_f32 v[130:131], v[130:131], v[226:227]
	v_pk_fma_f32 v[12:13], v[112:113], v[12:13], v[92:93]
	v_pk_fma_f32 v[14:15], v[114:115], v[14:15], v[46:47]
	v_pk_fma_f32 v[46:47], v[122:123], v[74:75], v[50:51]
	v_pk_fma_f32 v[52:53], v[126:127], v[78:79], v[52:53]
	v_mov_b32_e32 v74, v5
	v_mov_b32_e32 v75, v9
	v_mov_b32_e32 v78, v7
	v_mov_b32_e32 v79, v11
	v_pk_add_f32 v[134:135], v[134:135], v[198:199]
	v_pk_add_f32 v[132:133], v[132:133], v[196:197]
	v_pk_fma_f32 v[42:43], v[118:119], v[70:71], v[48:49]
	v_pk_fma_f32 v[44:45], v[116:117], v[68:69], v[94:95]
	v_pk_fma_f32 v[48:49], v[120:121], v[72:73], v[96:97]
	v_pk_fma_f32 v[50:51], v[124:125], v[76:77], v[98:99]
	v_pk_fma_f32 v[54:55], v[130:131], v[82:83], v[54:55]
	v_pk_fma_f32 v[68:69], v[128:129], v[80:81], v[100:101]
	v_mov_b32_e32 v72, v4
	v_mov_b32_e32 v73, v8
	v_mov_b32_e32 v76, v6
	v_mov_b32_e32 v77, v10
	v_pk_mul_f32 v[80:81], v[14:15], v[14:15]
	v_pk_mul_f32 v[82:83], v[12:13], v[12:13]
	v_pk_mul_f32 v[74:75], v[74:75], v[74:75]
	v_pk_mul_f32 v[78:79], v[78:79], v[78:79]
	v_pk_add_f32 v[132:133], v[132:133], v[228:229]
	v_pk_add_f32 v[134:135], v[134:135], v[230:231]
	v_pk_mov_b32 v[96:97], v[82:83], v[80:81] op_sel:[1,0]
	v_mov_b32_e32 v83, v81
	v_pk_fma_f32 v[72:73], v[72:73], v[72:73], v[74:75]
	v_pk_fma_f32 v[74:75], v[76:77], v[76:77], v[78:79]
	v_pk_fma_f32 v[56:57], v[134:135], v[86:87], v[56:57]
	v_pk_fma_f32 v[70:71], v[132:133], v[84:85], v[102:103]
	v_mul_f32_e32 v84, v45, v45
	v_mul_f32_e32 v86, v43, v43
	v_pk_add_f32 v[76:77], v[96:97], v[82:83]
	v_pk_add_f32 v[72:73], v[72:73], v[74:75]
	v_mul_f32_e32 v95, v48, v48
	v_mul_f32_e32 v98, v49, v49
	v_mul_f32_e32 v99, v46, v46
	v_mul_f32_e32 v100, v47, v47
	v_pk_fma_f32 v[80:81], v[44:45], v[44:45], v[84:85] op_sel_hi:[1,1,0]
	v_pk_fma_f32 v[84:85], v[42:43], v[42:43], v[86:87] op_sel_hi:[1,1,0]
	v_pk_add_f32 v[74:75], v[76:77], v[76:77] op_sel:[0,1] op_sel_hi:[1,0]
	v_pk_add_f32 v[72:73], v[72:73], v[72:73] op_sel:[0,1] op_sel_hi:[1,0]
	v_pk_mul_f32 v[88:89], v[52:53], v[52:53]
	v_pk_mul_f32 v[90:91], v[50:51], v[50:51]
	v_mov_b32_e32 v81, v99
	v_mov_b32_e32 v85, v100
	v_mov_b32_e32 v75, v98
	v_mov_b32_e32 v73, v95
	v_pk_mov_b32 v[86:87], v[90:91], v[88:89] op_sel:[1,0]
	v_mov_b32_e32 v91, v89
	v_pk_add_f32 v[76:77], v[80:81], v[84:85]
	v_pk_add_f32 v[72:73], v[72:73], v[74:75]
	v_mul_f32_e32 v92, v69, v69
	v_mul_f32_e32 v94, v55, v55
	v_pk_add_f32 v[78:79], v[86:87], v[90:91]
	v_pk_add_f32 v[72:73], v[72:73], v[76:77]
	v_mul_f32_e32 v101, v70, v70
	v_mul_f32_e32 v102, v71, v71
	v_mul_f32_e32 v103, v56, v56
	v_mul_f32_e32 v104, v57, v57
	v_pk_fma_f32 v[88:89], v[68:69], v[68:69], v[92:93] op_sel_hi:[1,1,0]
	v_pk_fma_f32 v[92:93], v[54:55], v[54:55], v[94:95] op_sel_hi:[1,1,0]
	v_pk_add_f32 v[78:79], v[78:79], v[78:79] op_sel:[0,1] op_sel_hi:[1,0]
	v_pk_add_f32 v[72:73], v[72:73], v[72:73] op_sel:[0,1] op_sel_hi:[1,0]
	v_mov_b32_e32 v89, v103
	v_mov_b32_e32 v93, v104
	v_mov_b32_e32 v79, v102
	v_mov_b32_e32 v73, v101
	v_pk_add_f32 v[80:81], v[88:89], v[92:93]
	v_pk_add_f32 v[72:73], v[72:73], v[78:79]
	s_nop 0
	v_pk_add_f32 v[72:73], v[72:73], v[80:81]
	s_nop 0
	v_add_f32_e32 v72, v72, v73
	global_load_dwordx4 v[204:207], v[22:23], off offset:1024
	global_load_dwordx4 v[208:211], v[22:23], off offset:2048
	global_load_dwordx4 v[212:215], v[22:23], off offset:3072
	global_load_dwordx4 v[216:219], v[32:33], off
	global_load_dwordx4 v[220:223], v[34:35], off
	global_load_dwordx4 v[224:227], v[36:37], off
	global_load_dwordx4 v[228:231], v[38:39], off
	v_mov_b32_dpp v73, v72 quad_perm:[1,0,3,2] row_mask:0xf bank_mask:0xf
	s_waitcnt lgkmcnt(0)
; __device__ __forceinline__ float wave_sum(float v) {
;     ...
;     for (int o = 1; o < 64; o <<= 1) v += __shfl_xor(v, o);
; __device__ __forceinline__ void ph13_final(const Frame& F, const Args& A) {
;     ...
;         const float rstd = 1.f / sqrtf(wave_sum(ss) * (1.f / DM) + EPS_);
;         f32x4* orow = (f32x4*)(out + (size_t)row * DM) + lane;
; #pragma unroll
;         for (int j = 0; j < 8; ++j) { const f32x4 g = *(const f32x4*)(fg + 4 * lane + 256 * j); orow[64 * j] = v[j] * rstd * g; }
	v_add_f32_e32 v72, v72, v73
	s_nop 1
	v_mov_b32_dpp v73, v72 quad_perm:[2,3,0,1] row_mask:0xf bank_mask:0xf
	s_waitcnt lgkmcnt(0)
	v_add_f32_e32 v72, v72, v73
	ds_bpermute_b32 v73, v62, v72
	s_waitcnt lgkmcnt(0)
	v_add_f32_e32 v72, v72, v73
	s_nop 1
	v_mov_b32_dpp v73, v72 row_ror:8 row_mask:0xf bank_mask:0xf
	s_waitcnt lgkmcnt(0)
	v_add_f32_e32 v72, v72, v73
	ds_bpermute_b32 v73, v64, v72
	s_waitcnt lgkmcnt(0)
	v_add_f32_e32 v72, v72, v73
	ds_bpermute_b32 v73, v65, v72
	s_waitcnt lgkmcnt(0)
	v_add_f32_e32 v72, v72, v73
	v_fmamk_f32 v72, v72, 0x3a000000, v66
	v_mul_f32_e32 v73, 0x4f800000, v72
	v_cmp_gt_f32_e32 vcc, s22, v72
	s_nop 1
	v_cndmask_b32_e32 v72, v72, v73, vcc
	v_sqrt_f32_e32 v73, v72
	s_nop 0
	v_add_u32_e32 v74, -1, v73
	v_add_u32_e32 v75, 1, v73
	v_fma_f32 v76, -v74, v73, v72
	v_fma_f32 v77, -v75, v73, v72
	v_cmp_ge_f32_e64 s[0:1], 0, v76
	s_nop 1
	v_cndmask_b32_e64 v73, v73, v74, s[0:1]
	v_cmp_lt_f32_e64 s[0:1], 0, v77
	s_nop 1
	v_cndmask_b32_e64 v73, v73, v75, s[0:1]
	v_mul_f32_e32 v74, 0x37800000, v73
	v_cndmask_b32_e32 v73, v73, v74, vcc
	v_cmp_class_f32_e32 vcc, v72, v67
	s_nop 1
	v_cndmask_b32_e32 v72, v73, v72, vcc
	v_div_scale_f32 v73, s[0:1], v72, v72, 1.0
	v_rcp_f32_e32 v75, v73
	v_div_scale_f32 v74, vcc, 1.0, v72, 1.0
	v_fma_f32 v76, -v73, v75, 1.0
	v_fmac_f32_e32 v75, v76, v75
	v_mul_f32_e32 v76, v74, v75
	v_fma_f32 v77, -v73, v76, v74
	v_fmac_f32_e32 v76, v77, v75
	v_fma_f32 v73, -v73, v76, v74
	v_div_fmas_f32 v73, v73, v75, v76
	v_div_fixup_f32 v72, v73, v72, 1.0
	v_pk_mul_f32 v[4:5], v[4:5], v[72:73] op_sel_hi:[1,0]
	v_pk_mul_f32 v[6:7], v[6:7], v[72:73] op_sel_hi:[1,0]
	v_pk_mul_f32 v[0:1], v[0:1], v[4:5]
	v_pk_mul_f32 v[2:3], v[2:3], v[6:7]
	global_store_dwordx4 v[58:59], v[0:3], off
	s_waitcnt vmcnt(1)
	s_nop 0
	v_mov_b64_e32 v[0:1], v[204:205]
	v_mov_b64_e32 v[2:3], v[206:207]
	v_pk_mul_f32 v[4:5], v[10:11], v[72:73] op_sel_hi:[1,0]
	v_pk_mul_f32 v[6:7], v[8:9], v[72:73] op_sel_hi:[1,0]
	v_pk_mul_f32 v[8:9], v[48:49], v[72:73] op_sel_hi:[1,0]
	v_pk_mul_f32 v[0:1], v[0:1], v[6:7]
	v_pk_mul_f32 v[2:3], v[2:3], v[4:5]
	global_store_dwordx4 v[58:59], v[0:3], off offset:1024
	s_nop 1
	v_mov_b64_e32 v[0:1], v[208:209]
	v_mov_b64_e32 v[2:3], v[210:211]
	v_pk_mul_f32 v[4:5], v[14:15], v[72:73] op_sel_hi:[1,0]
	v_pk_mul_f32 v[6:7], v[12:13], v[72:73] op_sel_hi:[1,0]
	v_pk_mul_f32 v[2:3], v[2:3], v[4:5]
	v_pk_mul_f32 v[0:1], v[0:1], v[6:7]
	global_store_dwordx4 v[58:59], v[0:3], off offset:2048
	s_nop 1
	v_mov_b64_e32 v[0:1], v[212:213]
	v_mov_b64_e32 v[2:3], v[214:215]
	v_pk_mul_f32 v[4:5], v[42:43], v[72:73] op_sel_hi:[1,0]
	v_pk_mul_f32 v[6:7], v[44:45], v[72:73] op_sel_hi:[1,0]
	v_pk_mul_f32 v[2:3], v[2:3], v[4:5]
	v_pk_mul_f32 v[0:1], v[0:1], v[6:7]
	global_store_dwordx4 v[58:59], v[0:3], off offset:3072
	s_nop 1
	v_mov_b64_e32 v[0:1], v[216:217]
	v_mov_b64_e32 v[2:3], v[218:219]
	v_add_co_u32_e32 v4, vcc, s3, v58
	v_pk_mul_f32 v[6:7], v[46:47], v[72:73] op_sel_hi:[1,0]
	s_nop 0
	v_addc_co_u32_e32 v5, vcc, 0, v59, vcc
	v_pk_mul_f32 v[0:1], v[0:1], v[8:9]
	v_pk_mul_f32 v[2:3], v[2:3], v[6:7]
	global_store_dwordx4 v[4:5], v[0:3], off
	s_nop 1
	v_mov_b64_e32 v[0:1], v[220:221]
	v_mov_b64_e32 v[2:3], v[222:223]
	v_pk_mul_f32 v[6:7], v[52:53], v[72:73] op_sel_hi:[1,0]
	v_pk_mul_f32 v[8:9], v[50:51], v[72:73] op_sel_hi:[1,0]
	v_pk_mul_f32 v[2:3], v[2:3], v[6:7]
	v_pk_mul_f32 v[0:1], v[0:1], v[8:9]
	global_store_dwordx4 v[4:5], v[0:3], off offset:1024
	s_nop 1
	v_mov_b64_e32 v[0:1], v[224:225]
	v_mov_b64_e32 v[2:3], v[226:227]
	v_pk_mul_f32 v[6:7], v[54:55], v[72:73] op_sel_hi:[1,0]
	v_pk_mul_f32 v[8:9], v[68:69], v[72:73] op_sel_hi:[1,0]
	v_pk_mul_f32 v[2:3], v[2:3], v[6:7]
	v_pk_mul_f32 v[0:1], v[0:1], v[8:9]
	global_store_dwordx4 v[4:5], v[0:3], off offset:2048
	s_nop 1
	v_mov_b64_e32 v[0:1], v[228:229]
	v_mov_b64_e32 v[2:3], v[230:231]
	v_pk_mul_f32 v[6:7], v[56:57], v[72:73] op_sel_hi:[1,0]
	v_pk_mul_f32 v[8:9], v[70:71], v[72:73] op_sel_hi:[1,0]
	v_pk_mul_f32 v[2:3], v[6:7], v[2:3]
	v_pk_mul_f32 v[0:1], v[8:9], v[0:1]
	global_store_dwordx4 v[4:5], v[0:3], off offset:3072
	s_cbranch_scc1 .LBB0_1568
